# c1
# baseline (speedup 1.0000x reference)
	.text
	.p2alignl 8, 3212836864

	.section	.text._Z6mxgemmILi0ELi1024ELi4EEvPKcS1_PKfS3_Pvi,"axG",@progbits,_Z6mxgemmILi0ELi1024ELi4EEvPKcS1_PKfS3_Pvi,comdat
	.p2alignl 8, 3212836864

_Z6mxgemmILi1ELi4096ELi4EEvPKcS1_PKfS3_Pvi:
	s_load_dwordx4 s[4:7], s[0:1], 0x0
	s_load_dwordx2 s[10:11], s[0:1], 0x10
	s_load_dword s3, s[0:1], 0x28
	s_ashr_i32 s8, s2, 31
	s_lshr_b32 s8, s8, 29
	s_add_i32 s8, s2, s8
	s_ashr_i32 s9, s8, 3
	s_waitcnt lgkmcnt(0)
	s_lshl_b32 s12, s3, 3
	s_abs_i32 s13, s12
	v_cvt_f32_u32_e32 v1, s13
	s_and_b32 s8, s8, 0x3ffffff8
	s_sub_i32 s2, s2, s8
	s_mul_i32 s2, s2, s3
	v_rcp_iflag_f32_e32 v1, v1
	s_lshl_b32 s2, s2, 2
	s_add_i32 s2, s2, s9
	s_sub_i32 s9, 0, s13
	v_mul_f32_e32 v1, 0x4f7ffffe, v1
	v_cvt_u32_f32_e32 v1, v1
	s_abs_i32 s8, s2
	v_readfirstlane_b32 s33, v0
	s_xor_b32 s3, s2, s12
	v_readfirstlane_b32 s14, v1
	s_mul_i32 s9, s9, s14
	s_mul_hi_u32 s9, s14, s9
	s_add_i32 s14, s14, s9
	s_mul_hi_u32 s9, s8, s14
	s_mul_i32 s14, s9, s13
	s_sub_i32 s8, s8, s14
	s_lshr_b32 s48, s33, 6
	s_lshr_b32 s27, s33, 8
	s_ashr_i32 s3, s3, 31
	s_add_i32 s14, s9, 1
	s_sub_i32 s15, s8, s13
	s_cmp_ge_u32 s8, s13
	s_cselect_b32 s9, s14, s9
	s_cselect_b32 s8, s15, s8
	s_add_i32 s14, s9, 1
	s_cmp_ge_u32 s8, s13
	s_cselect_b32 s8, s14, s9
	s_xor_b32 s8, s8, s3
	s_sub_i32 s3, s8, s3
	s_lshl_b32 s8, s3, 3
	s_mul_i32 s3, s3, s12
	s_sub_i32 s2, s2, s3
	s_ashr_i32 s3, s2, 31
	s_lshr_b32 s3, s3, 29
	s_add_i32 s3, s2, s3
	s_ashr_i32 s12, s3, 3
	s_and_b32 s3, s3, -8
	s_sub_i32 s2, s2, s3
	s_add_i32 s8, s2, s8
	s_ashr_i32 s13, s12, 31
	s_ashr_i32 s9, s8, 31
	s_lshl_b64 s[22:23], s[12:13], 19
	s_lshl_b64 s[42:43], s[8:9], 16
	s_add_u32 s2, s6, s42
	s_addc_u32 s3, s7, s43
	s_add_u32 s14, s2, 0x3000000
	s_mul_hi_u32 s2, s33, 0xaaaaaaab
	s_addc_u32 s15, s3, 0
	s_lshr_b32 s28, s2, 8
	s_mul_i32 s3, s28, -6
	s_lshl_b32 s26, s48, 10
	s_add_i32 s3, s3, s48
	s_lshr_b32 s9, s2, 9
	s_bitcmp1_b32 s2, 8
	s_cselect_b32 s30, 0x3000, 0
	s_lshl_b32 s2, s3, 10
	s_add_i32 s50, s2, s30
	s_add_i32 s2, s48, 8
	s_mul_hi_u32 s31, s2, 0x2aaaaaab
	s_mul_i32 s29, s9, 0x6000
	s_mul_i32 s3, s31, -6
	s_add_i32 s16, s50, s29
	s_lshl_b32 s9, s9, 15
	s_add_i32 s3, s3, s2
	s_lshr_b32 s39, s31, 1
	s_bitcmp1_b32 s31, 0
	s_cselect_b32 s35, 0x3000, 0
	s_add_i32 s2, s48, 16
	s_lshl_b32 s40, s3, 10
	s_mul_hi_u32 s36, s2, 0x2aaaaaab
	s_mul_i32 s34, s39, 0x6000
	s_add_i32 s40, s40, s35
	s_mul_i32 s3, s36, -6
	s_add_i32 s18, s40, s34
	s_add_i32 s3, s3, s2
	s_lshr_b32 s41, s36, 1
	s_bitcmp1_b32 s36, 0
	s_cselect_b32 s38, 0x3000, 0
	s_lshl_b32 s49, s3, 10
	s_mul_i32 s37, s41, 0x6000
	s_add_i32 s49, s49, s38
	s_mul_i32 s24, s8, 0x180000
	s_add_i32 s20, s49, s37
	s_mul_hi_i32 s25, s8, 0x180000
	s_add_u32 s2, s6, s24
	s_addc_u32 s3, s7, s25
	s_add_u32 s44, s4, s22
	s_addc_u32 s45, s5, s23
	s_add_i32 s50, s50, s9
	s_lshl_b32 s9, s39, 13
	s_add_i32 s9, s18, s9
	s_add_i32 s56, s9, 0
	s_lshl_b32 s9, s41, 13
	v_mov_b32_e32 v2, 0
	s_add_i32 s13, s26, 0
	s_add_i32 s9, s20, s9
	v_lshlrev_b32_e32 v4, 4, v0
	v_mov_b32_e32 v5, v2
	s_mov_b32 m0, s13
	s_add_i32 s57, s9, 0
	s_lshl_b32 s9, s48, 8
	v_lshl_add_u64 v[138:139], s[44:45], 0, v[4:5]
	global_load_lds_dwordx4 v4, s[44:45]
	s_mov_b64 s[44:45], 0x2000
	s_add_i32 s51, s50, 0
	s_add_i32 s9, s9, 0
	v_and_b32_e32 v1, 63, v0
	v_lshl_add_u64 v[8:9], v[138:139], 0, s[44:45]
	s_add_i32 s44, s13, 0x8000
	s_ashr_i32 s17, s16, 31
	s_add_i32 s45, s51, 0x2000
	s_ashr_i32 s19, s18, 31
	s_add_i32 s46, s56, 0x2000
	s_ashr_i32 s21, s20, 31
	s_add_i32 s47, s57, 0x2000
	s_add_i32 s48, s9, 0x20000
	v_lshlrev_b32_e32 v6, 4, v1
	v_mov_b32_e32 v7, v2
	s_add_u32 s52, s2, s16
	s_mov_b32 m0, s44
	v_lshl_add_u64 v[140:141], s[2:3], 0, v[6:7]
	s_addc_u32 s53, s3, s17
	s_addk_i32 s51, 0x3800
	global_load_lds_dwordx4 v[8:9], off
	v_lshl_add_u64 v[8:9], v[140:141], 0, s[16:17]
	s_mov_b32 m0, s45
	v_lshl_add_u64 v[132:133], s[52:53], 0, v[6:7]
	s_add_u32 s52, s2, s18
	global_load_lds_dwordx4 v[8:9], off
	v_lshl_add_u64 v[8:9], v[140:141], 0, s[18:19]
	s_mov_b32 m0, s46
	s_addc_u32 s53, s3, s19
	global_load_lds_dwordx4 v[8:9], off
	v_lshl_add_u64 v[8:9], v[140:141], 0, s[20:21]
	s_mov_b32 m0, s47
	v_lshl_add_u64 v[134:135], s[52:53], 0, v[6:7]
	s_add_i32 s53, s56, 0x3800
	v_lshlrev_b32_e32 v130, 2, v0
	global_load_lds_dwordx4 v[8:9], off
	s_mov_b32 m0, s48
	s_mov_b64 s[54:55], 0x1800
	s_add_u32 s2, s2, s20
	global_load_lds_dword v130, s[14:15]
	v_lshl_add_u64 v[8:9], v[132:133], 0, s[54:55]
	s_mov_b32 m0, s51
	s_addc_u32 s3, s3, s21
	global_load_lds_dwordx4 v[8:9], off
	v_lshl_add_u64 v[8:9], v[134:135], 0, s[54:55]
	s_mov_b32 m0, s53
	v_lshl_add_u64 v[136:137], s[2:3], 0, v[6:7]
	global_load_lds_dwordx4 v[8:9], off
	v_lshl_add_u64 v[8:9], v[136:137], 0, s[54:55]
	s_add_i32 s54, s57, 0x3800
	s_mov_b32 m0, s54
	s_load_dwordx2 s[2:3], s[0:1], 0x20
	global_load_lds_dwordx4 v[8:9], off
	s_mov_b64 s[70:71], 0x4000
	s_add_i32 m0, s26, 0x10000
	v_lshl_add_u64 v[8:9], v[138:139], 0, s[70:71]
	global_load_lds_dwordx4 v[8:9], off
	s_mov_b64 s[70:71], 0x6000
	s_add_i32 m0, s13, 0x18000
	v_lshl_add_u64 v[8:9], v[138:139], 0, s[70:71]
	global_load_lds_dwordx4 v[8:9], off
	s_cmp_lg_u32 s27, 1
	v_mov_b32_e32 v131, v2
	s_cbranch_scc1 .LBB3_2
	s_barrier
.LBB3_2:
	s_lshl_b32 s0, s39, 15
	s_add_i32 s0, s40, s0
	s_add_i32 s39, s0, 0x2000
	s_lshl_b32 s0, s41, 15
	v_bfe_u32 v3, v0, 4, 1
	s_add_i32 s0, s49, s0
	s_add_i32 s40, s0, 0x2000
	v_and_b32_e32 v8, 15, v0
	v_lshlrev_b32_e32 v10, 8, v3
	v_lshlrev_b32_e32 v3, 9, v3
	s_and_b32 s0, s33, 0xc0
	v_lshrrev_b32_e32 v1, 5, v1
	v_or3_b32 v3, s0, v3, v8
	v_lshlrev_b32_e32 v9, 15, v1
	v_lshl_add_u32 v11, s27, 7, v10
	v_mul_u32_u24_e32 v3, 24, v3
	s_waitcnt vmcnt(5)
	v_or_b32_e32 v11, v11, v8
	v_or3_b32 v8, v10, s0, v8
	v_or_b32_e32 v3, v3, v9
	s_add_i32 s41, 0, 0x10000
	s_addk_i32 s50, 0x2000
	v_lshl_add_u32 v11, v11, 4, v9
	v_lshlrev_b32_e32 v1, 10, v1
	v_lshlrev_b32_e32 v8, 1, v8
	v_add_u32_e32 v9, s41, v3
	s_barrier
	s_barrier
	s_add_i32 s0, s38, s37
	s_add_i32 s0, s0, s26
	s_mulk_i32 s36, 0x1800
	s_sub_i32 s0, s0, s36
	s_addk_i32 s0, 0x4000
	v_lshl_add_u64 v[6:7], s[24:25], 0, v[6:7]
	s_ashr_i32 s1, s0, 31
	v_lshl_add_u64 v[142:143], v[6:7], 0, s[0:1]
	s_add_i32 s0, s35, s34
	s_add_i32 s0, s0, s26
	s_mulk_i32 s31, 0x1800
	s_sub_i32 s0, s0, s31
	s_addk_i32 s0, 0x2000
	s_ashr_i32 s1, s0, 31
	v_lshl_add_u64 v[144:145], v[6:7], 0, s[0:1]
	s_add_i32 s0, s30, s29
	s_add_i32 s0, s0, s26
	s_mulk_i32 s28, 0x1800
	s_sub_i32 s0, s0, s28
	s_ashr_i32 s1, s0, 31
	v_lshl_add_u64 v[146:147], v[6:7], 0, s[0:1]
	s_add_u32 s0, s4, s22
	s_addc_u32 s1, s5, s23
	v_lshl_add_u64 v[4:5], s[0:1], 0, v[4:5]
	s_mov_b64 s[0:1], 0xa000
	v_add_u32_e32 v3, 0, v3
	v_add3_u32 v248, 0, v8, v1
	v_lshl_add_u64 v[148:149], v[4:5], 0, s[0:1]
	s_movk_i32 s0, 0xa000
	s_movk_i32 s4, 0xc000
	s_add_i32 s57, s41, s50
	s_add_i32 s56, s41, s39
	s_add_i32 s55, s41, s40
	s_movk_i32 s28, 0xe000
	v_add_u32_e32 v171, 0x2000, v3
	v_add_u32_e32 v167, 0x3800, v3
	v_add_u32_e32 v162, 0x2000, v9
	v_add_u32_e32 v1, 0x3800, v9
	v_add_u32_e32 v174, 0x2180, v3
	v_add_u32_e32 v173, 0x2300, v3
	v_add_u32_e32 v172, 0x2480, v3
	v_add_u32_e32 v170, 0x3980, v3
	v_add_u32_e32 v169, 0x3b00, v3
	v_add_u32_e32 v168, 0x3c80, v3
	v_add_u32_e32 v165, 0x2180, v9
	v_add_u32_e32 v164, 0x2300, v9
	v_add_u32_e32 v163, 0x2480, v9
	v_add_u32_e32 v160, 0x3980, v9
	v_add_u32_e32 v159, 0x3b00, v9
	v_add_u32_e32 v158, 0x3c80, v9
	s_mov_b32 s59, -2
	s_movk_i32 s60, 0x1000
	v_add_u32_e32 v175, 0, v11
	s_mov_b32 s1, -1
	s_add_i32 s61, s41, s26
	s_mov_b32 s5, -1
	s_add_i32 s58, s13, 0x18000
	s_mov_b64 s[22:23], 0xc000
	s_mov_b64 s[24:25], 0x3000800
	s_mov_b64 s[26:27], 0xd800
	s_add_i32 s52, s57, 0x1800
	s_add_i32 s50, s56, 0x1800
	s_add_i32 s49, s55, 0x1800
	v_add_u32_e32 v166, s41, v11
	s_mov_b32 s29, -1
	s_mov_b64 s[30:31], 0x18000
	s_mov_b64 s[34:35], 0x3001000
	s_mov_b64 s[36:37], 0x19800
	s_mov_b64 s[38:39], 0x1000
	s_mov_b64 s[40:41], 0x8000
	v_mov_b32_e32 v3, v2
	v_mov_b32_e32 v4, v2
	v_mov_b32_e32 v5, v2
	v_mov_b32_e32 v10, v2
	v_mov_b32_e32 v11, v2
	v_mov_b32_e32 v12, v2
	v_mov_b32_e32 v13, v2
	v_mov_b32_e32 v22, v2
	v_mov_b32_e32 v23, v2
	v_mov_b32_e32 v24, v2
	v_mov_b32_e32 v25, v2
	v_mov_b32_e32 v38, v2
	v_mov_b32_e32 v39, v2
	v_mov_b32_e32 v40, v2
	v_mov_b32_e32 v41, v2
	v_mov_b32_e32 v6, v2
	v_mov_b32_e32 v7, v2
	v_mov_b32_e32 v8, v2
	v_mov_b32_e32 v9, v2
	v_mov_b32_e32 v18, v2
	v_mov_b32_e32 v19, v2
	v_mov_b32_e32 v20, v2
	v_mov_b32_e32 v21, v2
	v_mov_b32_e32 v34, v2
	v_mov_b32_e32 v35, v2
	v_mov_b32_e32 v36, v2
	v_mov_b32_e32 v37, v2
	v_mov_b32_e32 v54, v2
	v_mov_b32_e32 v55, v2
	v_mov_b32_e32 v56, v2
	v_mov_b32_e32 v57, v2
	v_mov_b32_e32 v14, v2
	v_mov_b32_e32 v15, v2
	v_mov_b32_e32 v16, v2
	v_mov_b32_e32 v17, v2
	v_mov_b32_e32 v30, v2
	v_mov_b32_e32 v31, v2
	v_mov_b32_e32 v32, v2
	v_mov_b32_e32 v33, v2
	v_mov_b32_e32 v50, v2
	v_mov_b32_e32 v51, v2
	v_mov_b32_e32 v52, v2
	v_mov_b32_e32 v53, v2
	v_mov_b32_e32 v70, v2
	v_mov_b32_e32 v71, v2
	v_mov_b32_e32 v72, v2
	v_mov_b32_e32 v73, v2
	v_mov_b32_e32 v26, v2
	v_mov_b32_e32 v27, v2
	v_mov_b32_e32 v28, v2
	v_mov_b32_e32 v29, v2
	v_mov_b32_e32 v46, v2
	v_mov_b32_e32 v47, v2
	v_mov_b32_e32 v48, v2
	v_mov_b32_e32 v49, v2
	v_mov_b32_e32 v66, v2
	v_mov_b32_e32 v67, v2
	v_mov_b32_e32 v68, v2
	v_mov_b32_e32 v69, v2
	v_mov_b32_e32 v86, v2
	v_mov_b32_e32 v87, v2
	v_mov_b32_e32 v88, v2
	v_mov_b32_e32 v89, v2
	v_mov_b32_e32 v42, v2
	v_mov_b32_e32 v43, v2
	v_mov_b32_e32 v44, v2
	v_mov_b32_e32 v45, v2
	v_mov_b32_e32 v62, v2
	v_mov_b32_e32 v63, v2
	v_mov_b32_e32 v64, v2
	v_mov_b32_e32 v65, v2
	v_mov_b32_e32 v82, v2
	v_mov_b32_e32 v83, v2
	v_mov_b32_e32 v84, v2
	v_mov_b32_e32 v85, v2
	v_mov_b32_e32 v102, v2
	v_mov_b32_e32 v103, v2
	v_mov_b32_e32 v104, v2
	v_mov_b32_e32 v105, v2
	v_mov_b32_e32 v58, v2
	v_mov_b32_e32 v59, v2
	v_mov_b32_e32 v60, v2
	v_mov_b32_e32 v61, v2
	v_mov_b32_e32 v78, v2
	v_mov_b32_e32 v79, v2
	v_mov_b32_e32 v80, v2
	v_mov_b32_e32 v81, v2
	v_mov_b32_e32 v98, v2
	v_mov_b32_e32 v99, v2
	v_mov_b32_e32 v100, v2
	v_mov_b32_e32 v101, v2
	v_mov_b32_e32 v114, v2
	v_mov_b32_e32 v115, v2
	v_mov_b32_e32 v116, v2
	v_mov_b32_e32 v117, v2
	v_mov_b32_e32 v74, v2
	v_mov_b32_e32 v75, v2
	v_mov_b32_e32 v76, v2
	v_mov_b32_e32 v77, v2
	v_mov_b32_e32 v94, v2
	v_mov_b32_e32 v95, v2
	v_mov_b32_e32 v96, v2
	v_mov_b32_e32 v97, v2
	v_mov_b32_e32 v110, v2
	v_mov_b32_e32 v111, v2
	v_mov_b32_e32 v112, v2
	v_mov_b32_e32 v113, v2
	v_mov_b32_e32 v122, v2
	v_mov_b32_e32 v123, v2
	v_mov_b32_e32 v124, v2
	v_mov_b32_e32 v125, v2
	v_mov_b32_e32 v90, v2
	v_mov_b32_e32 v91, v2
	v_mov_b32_e32 v92, v2
	v_mov_b32_e32 v93, v2
	v_mov_b32_e32 v106, v2
	v_mov_b32_e32 v107, v2
	v_mov_b32_e32 v108, v2
	v_mov_b32_e32 v109, v2
	v_mov_b32_e32 v118, v2
	v_mov_b32_e32 v119, v2
	v_mov_b32_e32 v120, v2
	v_mov_b32_e32 v121, v2
	v_mov_b32_e32 v126, v2
	v_mov_b32_e32 v127, v2
	v_mov_b32_e32 v128, v2
	v_mov_b32_e32 v129, v2
	v_add_u32_e32 v176, 0x20000, v248
	v_mov_b32_e32 v177, 0x7f7f7f7f
	v_lshl_add_u64 v[150:151], s[42:43], 0, v[130:131]
	s_mov_b64 s[62:63], 0x2000
	s_mov_b64 s[64:65], 0x4000
.LBB3_3:
	ds_read_b128 v[202:205], v175
	ds_read_b128 v[206:209], v175 offset:256
	ds_read_b128 v[210:213], v175 offset:512
	ds_read_b128 v[214:217], v175 offset:768
	ds_read_b128 v[218:221], v175 offset:1024
	ds_read_b128 v[222:225], v175 offset:1280
	ds_read_b128 v[226:229], v175 offset:1536
	ds_read_b128 v[230:233], v175 offset:1792
	ds_read_b64 v[178:179], v171
	ds_read_b64 v[180:181], v171 offset:8
	ds_read_b64 v[182:183], v171 offset:16
	ds_read_b64 v[184:185], v174
	ds_read_b64 v[186:187], v174 offset:8
	ds_read_b64 v[188:189], v174 offset:16
	s_add_i32 s42, s60, 0xfffff000
	ds_read_b64 v[190:191], v173
	ds_read_b64 v[192:193], v173 offset:8
	ds_read_b64 v[194:195], v173 offset:16
	s_and_b32 s42, s42, 0x1000
	ds_read_b64 v[196:197], v172
	ds_read_b64 v[198:199], v172 offset:8
	ds_read_b64 v[200:201], v172 offset:16
	v_add_u32_e32 v152, s42, v176
	ds_read_u16 v240, v152
	ds_read_u16 v241, v152 offset:32
	ds_read_u16 v242, v152 offset:64
	ds_read_u16 v243, v152 offset:96
	s_add_i32 s42, s60, 0xfffff800
	v_lshl_add_u64 v[152:153], s[6:7], 0, v[146:147]
	v_lshl_add_u64 v[154:155], v[152:153], 0, s[22:23]
	s_mov_b32 m0, s57
	v_lshl_add_u64 v[238:239], s[6:7], 0, v[150:151]
	global_load_lds_dwordx4 v[154:155], off
	v_lshl_add_u64 v[154:155], s[6:7], 0, v[144:145]
	v_lshl_add_u64 v[156:157], v[154:155], 0, s[22:23]
	s_mov_b32 m0, s56
	s_and_b32 s42, s42, 0x1800
	global_load_lds_dwordx4 v[156:157], off
	v_lshl_add_u64 v[156:157], s[6:7], 0, v[142:143]
	v_lshl_add_u64 v[234:235], v[156:157], 0, s[22:23]
	s_mov_b32 m0, s55
	s_waitcnt lgkmcnt(0)
	v_mov_b32_e32 v236, v242
	global_load_lds_dwordx4 v[234:235], off
	v_lshl_add_u64 v[234:235], v[238:239], 0, s[24:25]
	s_add_i32 m0, s48, s42
	v_mov_b32_e32 v244, v243
	global_load_lds_dword v[234:235], off
	s_waitcnt vmcnt(6)
	s_waitcnt lgkmcnt(0)
	v_mov_b32_e32 v234, v240
	v_mov_b32_e32 v235, v241
	s_barrier
	v_mfma_scale_f32_16x16x128_f8f6f4 v[126:129], v[202:205], v[178:183], v[126:129], v177, v234 op_sel_hi:[0,0,0] cbsz:4 blgp:2
	v_mfma_scale_f32_16x16x128_f8f6f4 v[122:125], v[206:209], v[178:183], v[122:125], v177, v234 op_sel_hi:[0,0,0] cbsz:4 blgp:2
	v_mfma_scale_f32_16x16x128_f8f6f4 v[114:117], v[210:213], v[178:183], v[114:117], v177, v234 op_sel_hi:[0,0,0] cbsz:4 blgp:2
	v_mfma_scale_f32_16x16x128_f8f6f4 v[102:105], v[214:217], v[178:183], v[102:105], v177, v234 op_sel_hi:[0,0,0] cbsz:4 blgp:2
	v_mfma_scale_f32_16x16x128_f8f6f4 v[86:89], v[218:221], v[178:183], v[86:89], v177, v234 op_sel_hi:[0,0,0] cbsz:4 blgp:2
	v_mfma_scale_f32_16x16x128_f8f6f4 v[70:73], v[222:225], v[178:183], v[70:73], v177, v234 op_sel_hi:[0,0,0] cbsz:4 blgp:2
	v_mfma_scale_f32_16x16x128_f8f6f4 v[54:57], v[226:229], v[178:183], v[54:57], v177, v234 op_sel_hi:[0,0,0] cbsz:4 blgp:2
	v_mfma_scale_f32_16x16x128_f8f6f4 v[38:41], v[230:233], v[178:183], v[38:41], v177, v234 op_sel_hi:[0,0,0] cbsz:4 blgp:2
	v_mfma_scale_f32_16x16x128_f8f6f4 v[118:121], v[202:205], v[184:189], v[118:121], v177, v235 op_sel_hi:[0,0,0] cbsz:4 blgp:2
	v_mfma_scale_f32_16x16x128_f8f6f4 v[110:113], v[206:209], v[184:189], v[110:113], v177, v235 op_sel_hi:[0,0,0] cbsz:4 blgp:2
	v_mfma_scale_f32_16x16x128_f8f6f4 v[98:101], v[210:213], v[184:189], v[98:101], v177, v235 op_sel_hi:[0,0,0] cbsz:4 blgp:2
	v_mfma_scale_f32_16x16x128_f8f6f4 v[82:85], v[214:217], v[184:189], v[82:85], v177, v235 op_sel_hi:[0,0,0] cbsz:4 blgp:2
	v_mfma_scale_f32_16x16x128_f8f6f4 v[66:69], v[218:221], v[184:189], v[66:69], v177, v235 op_sel_hi:[0,0,0] cbsz:4 blgp:2
	v_mfma_scale_f32_16x16x128_f8f6f4 v[50:53], v[222:225], v[184:189], v[50:53], v177, v235 op_sel_hi:[0,0,0] cbsz:4 blgp:2
	v_mfma_scale_f32_16x16x128_f8f6f4 v[34:37], v[226:229], v[184:189], v[34:37], v177, v235 op_sel_hi:[0,0,0] cbsz:4 blgp:2
	v_mfma_scale_f32_16x16x128_f8f6f4 v[106:109], v[202:205], v[190:195], v[106:109], v177, v236 op_sel_hi:[0,0,0] cbsz:4 blgp:2
	v_mfma_scale_f32_16x16x128_f8f6f4 v[94:97], v[206:209], v[190:195], v[94:97], v177, v236 op_sel_hi:[0,0,0] cbsz:4 blgp:2
	v_mfma_scale_f32_16x16x128_f8f6f4 v[78:81], v[210:213], v[190:195], v[78:81], v177, v236 op_sel_hi:[0,0,0] cbsz:4 blgp:2
	v_mfma_scale_f32_16x16x128_f8f6f4 v[62:65], v[214:217], v[190:195], v[62:65], v177, v236 op_sel_hi:[0,0,0] cbsz:4 blgp:2
	v_mfma_scale_f32_16x16x128_f8f6f4 v[46:49], v[218:221], v[190:195], v[46:49], v177, v236 op_sel_hi:[0,0,0] cbsz:4 blgp:2
	v_mfma_scale_f32_16x16x128_f8f6f4 v[30:33], v[222:225], v[190:195], v[30:33], v177, v236 op_sel_hi:[0,0,0] cbsz:4 blgp:2
	v_mfma_scale_f32_16x16x128_f8f6f4 v[90:93], v[202:205], v[196:201], v[90:93], v177, v244 op_sel_hi:[0,0,0] cbsz:4 blgp:2
	v_mfma_scale_f32_16x16x128_f8f6f4 v[74:77], v[206:209], v[196:201], v[74:77], v177, v244 op_sel_hi:[0,0,0] cbsz:4 blgp:2
	v_mfma_scale_f32_16x16x128_f8f6f4 v[58:61], v[210:213], v[196:201], v[58:61], v177, v244 op_sel_hi:[0,0,0] cbsz:4 blgp:2
	v_mfma_scale_f32_16x16x128_f8f6f4 v[42:45], v[214:217], v[196:201], v[42:45], v177, v244 op_sel_hi:[0,0,0] cbsz:4 blgp:2
	v_mfma_scale_f32_16x16x128_f8f6f4 v[26:29], v[218:221], v[196:201], v[26:29], v177, v244 op_sel_hi:[0,0,0] cbsz:4 blgp:2
	v_mfma_scale_f32_16x16x128_f8f6f4 v[178:181], v[230:233], v[184:189], v[22:25], v177, v235 op_sel_hi:[0,0,0] cbsz:4 blgp:2
	v_mfma_scale_f32_16x16x128_f8f6f4 v[182:185], v[226:229], v[190:195], v[18:21], v177, v236 op_sel_hi:[0,0,0] cbsz:4 blgp:2
	v_mfma_scale_f32_16x16x128_f8f6f4 v[186:189], v[230:233], v[190:195], v[10:13], v177, v236 op_sel_hi:[0,0,0] cbsz:4 blgp:2
	v_mfma_scale_f32_16x16x128_f8f6f4 v[190:193], v[222:225], v[196:201], v[14:17], v177, v244 op_sel_hi:[0,0,0] cbsz:4 blgp:2
	v_mfma_scale_f32_16x16x128_f8f6f4 v[234:237], v[226:229], v[196:201], v[6:9], v177, v244 op_sel_hi:[0,0,0] cbsz:4 blgp:2
	v_mfma_scale_f32_16x16x128_f8f6f4 v[194:197], v[230:233], v[196:201], v[2:5], v177, v244 op_sel_hi:[0,0,0] cbsz:4 blgp:2
	s_barrier
	ds_read_b64 v[2:3], v167
	ds_read_b64 v[4:5], v167 offset:8
	ds_read_b64 v[6:7], v167 offset:16
	ds_read_b64 v[8:9], v170
	ds_read_b64 v[10:11], v170 offset:8
	ds_read_b64 v[12:13], v170 offset:16
	ds_read_b64 v[14:15], v169
	ds_read_b64 v[16:17], v169 offset:8
	ds_read_b64 v[18:19], v169 offset:16
	s_mov_b32 m0, s52
	ds_read_b64 v[20:21], v168
	ds_read_b64 v[22:23], v168 offset:8
	ds_read_b64 v[24:25], v168 offset:16
	v_lshl_add_u64 v[198:199], v[152:153], 0, s[26:27]
	global_load_lds_dwordx4 v[198:199], off
	v_lshl_add_u64 v[198:199], v[154:155], 0, s[26:27]
	s_mov_b32 m0, s50
	v_lshrrev_b32_e32 v200, 8, v242
	global_load_lds_dwordx4 v[198:199], off
	v_lshl_add_u64 v[198:199], v[156:157], 0, s[26:27]
	s_mov_b32 m0, s49
	s_nop 0
	global_load_lds_dwordx4 v[198:199], off
	v_lshl_add_u64 v[198:199], v[148:149], 0, s[28:29]
	s_mov_b32 m0, s13
	s_nop 0
	global_load_lds_dwordx4 v[198:199], off
	s_mov_b32 m0, s44
	s_nop 0
	global_load_lds_dwordx4 v[148:149], off
	s_waitcnt vmcnt(5)
	s_waitcnt lgkmcnt(0)
	v_lshrrev_b32_e32 v198, 8, v240
	v_lshrrev_b32_e32 v199, 8, v241
	v_lshrrev_b32_e32 v240, 8, v243
	s_barrier
	v_mfma_scale_f32_16x16x128_f8f6f4 v[126:129], v[202:205], v[2:7], v[126:129], v177, v198 op_sel_hi:[0,0,0] cbsz:4 blgp:2
	v_mfma_scale_f32_16x16x128_f8f6f4 v[122:125], v[206:209], v[2:7], v[122:125], v177, v198 op_sel_hi:[0,0,0] cbsz:4 blgp:2
	v_mfma_scale_f32_16x16x128_f8f6f4 v[114:117], v[210:213], v[2:7], v[114:117], v177, v198 op_sel_hi:[0,0,0] cbsz:4 blgp:2
	v_mfma_scale_f32_16x16x128_f8f6f4 v[102:105], v[214:217], v[2:7], v[102:105], v177, v198 op_sel_hi:[0,0,0] cbsz:4 blgp:2
	v_mfma_scale_f32_16x16x128_f8f6f4 v[86:89], v[218:221], v[2:7], v[86:89], v177, v198 op_sel_hi:[0,0,0] cbsz:4 blgp:2
	v_mfma_scale_f32_16x16x128_f8f6f4 v[70:73], v[222:225], v[2:7], v[70:73], v177, v198 op_sel_hi:[0,0,0] cbsz:4 blgp:2
	v_mfma_scale_f32_16x16x128_f8f6f4 v[54:57], v[226:229], v[2:7], v[54:57], v177, v198 op_sel_hi:[0,0,0] cbsz:4 blgp:2
	v_mfma_scale_f32_16x16x128_f8f6f4 v[38:41], v[230:233], v[2:7], v[38:41], v177, v198 op_sel_hi:[0,0,0] cbsz:4 blgp:2
	v_mfma_scale_f32_16x16x128_f8f6f4 v[118:121], v[202:205], v[8:13], v[118:121], v177, v199 op_sel_hi:[0,0,0] cbsz:4 blgp:2
	v_mfma_scale_f32_16x16x128_f8f6f4 v[110:113], v[206:209], v[8:13], v[110:113], v177, v199 op_sel_hi:[0,0,0] cbsz:4 blgp:2
	v_mfma_scale_f32_16x16x128_f8f6f4 v[98:101], v[210:213], v[8:13], v[98:101], v177, v199 op_sel_hi:[0,0,0] cbsz:4 blgp:2
	v_mfma_scale_f32_16x16x128_f8f6f4 v[82:85], v[214:217], v[8:13], v[82:85], v177, v199 op_sel_hi:[0,0,0] cbsz:4 blgp:2
	v_mfma_scale_f32_16x16x128_f8f6f4 v[66:69], v[218:221], v[8:13], v[66:69], v177, v199 op_sel_hi:[0,0,0] cbsz:4 blgp:2
	v_mfma_scale_f32_16x16x128_f8f6f4 v[50:53], v[222:225], v[8:13], v[50:53], v177, v199 op_sel_hi:[0,0,0] cbsz:4 blgp:2
	v_mfma_scale_f32_16x16x128_f8f6f4 v[34:37], v[226:229], v[8:13], v[34:37], v177, v199 op_sel_hi:[0,0,0] cbsz:4 blgp:2
	v_mfma_scale_f32_16x16x128_f8f6f4 v[106:109], v[202:205], v[14:19], v[106:109], v177, v200 op_sel_hi:[0,0,0] cbsz:4 blgp:2
	v_mfma_scale_f32_16x16x128_f8f6f4 v[94:97], v[206:209], v[14:19], v[94:97], v177, v200 op_sel_hi:[0,0,0] cbsz:4 blgp:2
	v_mfma_scale_f32_16x16x128_f8f6f4 v[78:81], v[210:213], v[14:19], v[78:81], v177, v200 op_sel_hi:[0,0,0] cbsz:4 blgp:2
	v_mfma_scale_f32_16x16x128_f8f6f4 v[62:65], v[214:217], v[14:19], v[62:65], v177, v200 op_sel_hi:[0,0,0] cbsz:4 blgp:2
	v_mfma_scale_f32_16x16x128_f8f6f4 v[46:49], v[218:221], v[14:19], v[46:49], v177, v200 op_sel_hi:[0,0,0] cbsz:4 blgp:2
	v_mfma_scale_f32_16x16x128_f8f6f4 v[30:33], v[222:225], v[14:19], v[30:33], v177, v200 op_sel_hi:[0,0,0] cbsz:4 blgp:2
	v_mfma_scale_f32_16x16x128_f8f6f4 v[90:93], v[202:205], v[20:25], v[90:93], v177, v240 op_sel_hi:[0,0,0] cbsz:4 blgp:2
	v_mfma_scale_f32_16x16x128_f8f6f4 v[74:77], v[206:209], v[20:25], v[74:77], v177, v240 op_sel_hi:[0,0,0] cbsz:4 blgp:2
	v_mfma_scale_f32_16x16x128_f8f6f4 v[58:61], v[210:213], v[20:25], v[58:61], v177, v240 op_sel_hi:[0,0,0] cbsz:4 blgp:2
	v_mfma_scale_f32_16x16x128_f8f6f4 v[42:45], v[214:217], v[20:25], v[42:45], v177, v240 op_sel_hi:[0,0,0] cbsz:4 blgp:2
	v_mfma_scale_f32_16x16x128_f8f6f4 v[26:29], v[218:221], v[20:25], v[26:29], v177, v240 op_sel_hi:[0,0,0] cbsz:4 blgp:2
	v_mfma_scale_f32_16x16x128_f8f6f4 v[178:181], v[230:233], v[8:13], v[178:181], v177, v199 op_sel_hi:[0,0,0] cbsz:4 blgp:2
	v_mfma_scale_f32_16x16x128_f8f6f4 v[182:185], v[226:229], v[14:19], v[182:185], v177, v200 op_sel_hi:[0,0,0] cbsz:4 blgp:2
	v_mfma_scale_f32_16x16x128_f8f6f4 v[186:189], v[230:233], v[14:19], v[186:189], v177, v200 op_sel_hi:[0,0,0] cbsz:4 blgp:2
	v_mfma_scale_f32_16x16x128_f8f6f4 v[190:193], v[222:225], v[20:25], v[190:193], v177, v240 op_sel_hi:[0,0,0] cbsz:4 blgp:2
	v_mfma_scale_f32_16x16x128_f8f6f4 v[198:201], v[226:229], v[20:25], v[234:237], v177, v240 op_sel_hi:[0,0,0] cbsz:4 blgp:2
	v_mfma_scale_f32_16x16x128_f8f6f4 v[194:197], v[230:233], v[20:25], v[194:197], v177, v240 op_sel_hi:[0,0,0] cbsz:4 blgp:2
	s_barrier
	ds_read_b128 v[202:205], v166
	ds_read_b128 v[206:209], v166 offset:256
	ds_read_b128 v[210:213], v166 offset:512
	ds_read_b128 v[214:217], v166 offset:768
	ds_read_b128 v[218:221], v166 offset:1024
	ds_read_b128 v[222:225], v166 offset:1280
	ds_read_b128 v[226:229], v166 offset:1536
	ds_read_b128 v[230:233], v166 offset:1792
	ds_read_b64 v[2:3], v162
	ds_read_b64 v[4:5], v162 offset:8
	ds_read_b64 v[6:7], v162 offset:16
	ds_read_b64 v[8:9], v165
	ds_read_b64 v[10:11], v165 offset:8
	ds_read_b64 v[12:13], v165 offset:16
	ds_read_b64 v[14:15], v164
	ds_read_b64 v[16:17], v164 offset:8
	ds_read_b64 v[18:19], v164 offset:16
	ds_read_b64 v[20:21], v163
	ds_read_b64 v[22:23], v163 offset:8
	ds_read_b64 v[24:25], v163 offset:16
	v_add_u32_e32 v234, s42, v176
	ds_read_u16 v242, v234
	ds_read_u16 v243, v234 offset:32
	ds_read_u16 v244, v234 offset:64
	ds_read_u16 v245, v234 offset:96
	s_mov_b32 m0, s45
	v_lshl_add_u64 v[234:235], v[152:153], 0, s[30:31]
	s_and_b32 s42, s60, 0x1000
	global_load_lds_dwordx4 v[234:235], off
	v_lshl_add_u64 v[234:235], v[154:155], 0, s[30:31]
	s_mov_b32 m0, s46
	s_waitcnt lgkmcnt(0)
	v_mov_b32_e32 v246, v244
	global_load_lds_dwordx4 v[234:235], off
	v_lshl_add_u64 v[234:235], v[156:157], 0, s[30:31]
	s_mov_b32 m0, s47
	v_mov_b32_e32 v247, v245
	global_load_lds_dwordx4 v[234:235], off
	v_lshl_add_u64 v[234:235], v[238:239], 0, s[34:35]
	s_add_i32 m0, s48, s42
	s_nop 0
	global_load_lds_dword v[234:235], off
	s_waitcnt vmcnt(6)
	s_waitcnt lgkmcnt(0)
	v_mov_b32_e32 v234, v242
	v_mov_b32_e32 v235, v243
	s_barrier
	v_mfma_scale_f32_16x16x128_f8f6f4 v[126:129], v[202:205], v[2:7], v[126:129], v177, v234 op_sel_hi:[0,0,0] cbsz:4 blgp:2
	v_mfma_scale_f32_16x16x128_f8f6f4 v[122:125], v[206:209], v[2:7], v[122:125], v177, v234 op_sel_hi:[0,0,0] cbsz:4 blgp:2
	v_mfma_scale_f32_16x16x128_f8f6f4 v[114:117], v[210:213], v[2:7], v[114:117], v177, v234 op_sel_hi:[0,0,0] cbsz:4 blgp:2
	v_mfma_scale_f32_16x16x128_f8f6f4 v[102:105], v[214:217], v[2:7], v[102:105], v177, v234 op_sel_hi:[0,0,0] cbsz:4 blgp:2
	v_mfma_scale_f32_16x16x128_f8f6f4 v[86:89], v[218:221], v[2:7], v[86:89], v177, v234 op_sel_hi:[0,0,0] cbsz:4 blgp:2
	v_mfma_scale_f32_16x16x128_f8f6f4 v[70:73], v[222:225], v[2:7], v[70:73], v177, v234 op_sel_hi:[0,0,0] cbsz:4 blgp:2
	v_mfma_scale_f32_16x16x128_f8f6f4 v[54:57], v[226:229], v[2:7], v[54:57], v177, v234 op_sel_hi:[0,0,0] cbsz:4 blgp:2
	v_mfma_scale_f32_16x16x128_f8f6f4 v[38:41], v[230:233], v[2:7], v[38:41], v177, v234 op_sel_hi:[0,0,0] cbsz:4 blgp:2
	v_mfma_scale_f32_16x16x128_f8f6f4 v[118:121], v[202:205], v[8:13], v[118:121], v177, v235 op_sel_hi:[0,0,0] cbsz:4 blgp:2
	v_mfma_scale_f32_16x16x128_f8f6f4 v[110:113], v[206:209], v[8:13], v[110:113], v177, v235 op_sel_hi:[0,0,0] cbsz:4 blgp:2
	v_mfma_scale_f32_16x16x128_f8f6f4 v[98:101], v[210:213], v[8:13], v[98:101], v177, v235 op_sel_hi:[0,0,0] cbsz:4 blgp:2
	v_mfma_scale_f32_16x16x128_f8f6f4 v[82:85], v[214:217], v[8:13], v[82:85], v177, v235 op_sel_hi:[0,0,0] cbsz:4 blgp:2
	v_mfma_scale_f32_16x16x128_f8f6f4 v[66:69], v[218:221], v[8:13], v[66:69], v177, v235 op_sel_hi:[0,0,0] cbsz:4 blgp:2
	v_mfma_scale_f32_16x16x128_f8f6f4 v[50:53], v[222:225], v[8:13], v[50:53], v177, v235 op_sel_hi:[0,0,0] cbsz:4 blgp:2
	v_mfma_scale_f32_16x16x128_f8f6f4 v[34:37], v[226:229], v[8:13], v[34:37], v177, v235 op_sel_hi:[0,0,0] cbsz:4 blgp:2
	v_mfma_scale_f32_16x16x128_f8f6f4 v[106:109], v[202:205], v[14:19], v[106:109], v177, v246 op_sel_hi:[0,0,0] cbsz:4 blgp:2
	v_mfma_scale_f32_16x16x128_f8f6f4 v[94:97], v[206:209], v[14:19], v[94:97], v177, v246 op_sel_hi:[0,0,0] cbsz:4 blgp:2
	v_mfma_scale_f32_16x16x128_f8f6f4 v[78:81], v[210:213], v[14:19], v[78:81], v177, v246 op_sel_hi:[0,0,0] cbsz:4 blgp:2
	v_mfma_scale_f32_16x16x128_f8f6f4 v[62:65], v[214:217], v[14:19], v[62:65], v177, v246 op_sel_hi:[0,0,0] cbsz:4 blgp:2
	v_mfma_scale_f32_16x16x128_f8f6f4 v[46:49], v[218:221], v[14:19], v[46:49], v177, v246 op_sel_hi:[0,0,0] cbsz:4 blgp:2
	v_mfma_scale_f32_16x16x128_f8f6f4 v[30:33], v[222:225], v[14:19], v[30:33], v177, v246 op_sel_hi:[0,0,0] cbsz:4 blgp:2
	v_mfma_scale_f32_16x16x128_f8f6f4 v[238:241], v[226:229], v[14:19], v[182:185], v177, v246 op_sel_hi:[0,0,0] cbsz:4 blgp:2
	v_mfma_scale_f32_16x16x128_f8f6f4 v[14:17], v[230:233], v[14:19], v[186:189], v177, v246 op_sel_hi:[0,0,0] cbsz:4 blgp:2
	v_mfma_scale_f32_16x16x128_f8f6f4 v[90:93], v[202:205], v[20:25], v[90:93], v177, v247 op_sel_hi:[0,0,0] cbsz:4 blgp:2
	v_mfma_scale_f32_16x16x128_f8f6f4 v[74:77], v[206:209], v[20:25], v[74:77], v177, v247 op_sel_hi:[0,0,0] cbsz:4 blgp:2
	v_mfma_scale_f32_16x16x128_f8f6f4 v[58:61], v[210:213], v[20:25], v[58:61], v177, v247 op_sel_hi:[0,0,0] cbsz:4 blgp:2
	v_mfma_scale_f32_16x16x128_f8f6f4 v[42:45], v[214:217], v[20:25], v[42:45], v177, v247 op_sel_hi:[0,0,0] cbsz:4 blgp:2
	v_mfma_scale_f32_16x16x128_f8f6f4 v[26:29], v[218:221], v[20:25], v[26:29], v177, v247 op_sel_hi:[0,0,0] cbsz:4 blgp:2
	v_mfma_scale_f32_16x16x128_f8f6f4 v[234:237], v[230:233], v[8:13], v[178:181], v177, v235 op_sel_hi:[0,0,0] cbsz:4 blgp:2
	v_mfma_scale_f32_16x16x128_f8f6f4 v[190:193], v[222:225], v[20:25], v[190:193], v177, v247 op_sel_hi:[0,0,0] cbsz:4 blgp:2
	v_mfma_scale_f32_16x16x128_f8f6f4 v[198:201], v[226:229], v[20:25], v[198:201], v177, v247 op_sel_hi:[0,0,0] cbsz:4 blgp:2
	v_mfma_scale_f32_16x16x128_f8f6f4 v[194:197], v[230:233], v[20:25], v[194:197], v177, v247 op_sel_hi:[0,0,0] cbsz:4 blgp:2
	s_barrier
	ds_read_b64 v[2:3], v1
	ds_read_b64 v[4:5], v1 offset:8
	ds_read_b64 v[6:7], v1 offset:16
	ds_read_b64 v[8:9], v160
	ds_read_b64 v[10:11], v160 offset:8
	ds_read_b64 v[12:13], v160 offset:16
	ds_read_b64 v[178:179], v159
	ds_read_b64 v[180:181], v159 offset:8
	ds_read_b64 v[182:183], v159 offset:16
	s_mov_b32 m0, s51
	ds_read_b64 v[184:185], v158
	ds_read_b64 v[186:187], v158 offset:8
	ds_read_b64 v[188:189], v158 offset:16
	v_lshl_add_u64 v[18:19], v[152:153], 0, s[36:37]
	global_load_lds_dwordx4 v[18:19], off
	v_lshl_add_u64 v[18:19], v[154:155], 0, s[36:37]
	s_mov_b32 m0, s53
	v_lshrrev_b32_e32 v152, 8, v244
	global_load_lds_dwordx4 v[18:19], off
	v_lshl_add_u64 v[18:19], v[156:157], 0, s[36:37]
	s_mov_b32 m0, s54
	v_lshrrev_b32_e32 v153, 8, v245
	global_load_lds_dwordx4 v[18:19], off
	v_lshl_add_u64 v[18:19], v[148:149], 0, s[62:63]
	s_mov_b32 m0, s61
	s_nop 0
	global_load_lds_dwordx4 v[18:19], off
	v_lshl_add_u64 v[18:19], v[148:149], 0, s[64:65]
	s_mov_b32 m0, s58
	s_nop 0
	global_load_lds_dwordx4 v[18:19], off
	s_waitcnt vmcnt(5)
	s_waitcnt lgkmcnt(0)
	v_lshrrev_b32_e32 v18, 8, v242
	v_lshrrev_b32_e32 v19, 8, v243
	s_barrier
	v_mfma_scale_f32_16x16x128_f8f6f4 v[126:129], v[202:205], v[2:7], v[126:129], v177, v18 op_sel_hi:[0,0,0] cbsz:4 blgp:2
	v_mfma_scale_f32_16x16x128_f8f6f4 v[122:125], v[206:209], v[2:7], v[122:125], v177, v18 op_sel_hi:[0,0,0] cbsz:4 blgp:2
	v_mfma_scale_f32_16x16x128_f8f6f4 v[114:117], v[210:213], v[2:7], v[114:117], v177, v18 op_sel_hi:[0,0,0] cbsz:4 blgp:2
	v_mfma_scale_f32_16x16x128_f8f6f4 v[102:105], v[214:217], v[2:7], v[102:105], v177, v18 op_sel_hi:[0,0,0] cbsz:4 blgp:2
	v_mfma_scale_f32_16x16x128_f8f6f4 v[86:89], v[218:221], v[2:7], v[86:89], v177, v18 op_sel_hi:[0,0,0] cbsz:4 blgp:2
	v_mfma_scale_f32_16x16x128_f8f6f4 v[70:73], v[222:225], v[2:7], v[70:73], v177, v18 op_sel_hi:[0,0,0] cbsz:4 blgp:2
	v_mfma_scale_f32_16x16x128_f8f6f4 v[54:57], v[226:229], v[2:7], v[54:57], v177, v18 op_sel_hi:[0,0,0] cbsz:4 blgp:2
	v_mfma_scale_f32_16x16x128_f8f6f4 v[38:41], v[230:233], v[2:7], v[38:41], v177, v18 op_sel_hi:[0,0,0] cbsz:4 blgp:2
	v_mfma_scale_f32_16x16x128_f8f6f4 v[118:121], v[202:205], v[8:13], v[118:121], v177, v19 op_sel_hi:[0,0,0] cbsz:4 blgp:2
	v_mfma_scale_f32_16x16x128_f8f6f4 v[110:113], v[206:209], v[8:13], v[110:113], v177, v19 op_sel_hi:[0,0,0] cbsz:4 blgp:2
	v_mfma_scale_f32_16x16x128_f8f6f4 v[98:101], v[210:213], v[8:13], v[98:101], v177, v19 op_sel_hi:[0,0,0] cbsz:4 blgp:2
	v_mfma_scale_f32_16x16x128_f8f6f4 v[82:85], v[214:217], v[8:13], v[82:85], v177, v19 op_sel_hi:[0,0,0] cbsz:4 blgp:2
	v_mfma_scale_f32_16x16x128_f8f6f4 v[66:69], v[218:221], v[8:13], v[66:69], v177, v19 op_sel_hi:[0,0,0] cbsz:4 blgp:2
	v_mfma_scale_f32_16x16x128_f8f6f4 v[50:53], v[222:225], v[8:13], v[50:53], v177, v19 op_sel_hi:[0,0,0] cbsz:4 blgp:2
	v_mfma_scale_f32_16x16x128_f8f6f4 v[34:37], v[226:229], v[8:13], v[34:37], v177, v19 op_sel_hi:[0,0,0] cbsz:4 blgp:2
	v_mfma_scale_f32_16x16x128_f8f6f4 v[22:25], v[230:233], v[8:13], v[234:237], v177, v19 op_sel_hi:[0,0,0] cbsz:4 blgp:2
	v_mfma_scale_f32_16x16x128_f8f6f4 v[106:109], v[202:205], v[178:183], v[106:109], v177, v152 op_sel_hi:[0,0,0] cbsz:4 blgp:2
	v_mfma_scale_f32_16x16x128_f8f6f4 v[94:97], v[206:209], v[178:183], v[94:97], v177, v152 op_sel_hi:[0,0,0] cbsz:4 blgp:2
	v_mfma_scale_f32_16x16x128_f8f6f4 v[78:81], v[210:213], v[178:183], v[78:81], v177, v152 op_sel_hi:[0,0,0] cbsz:4 blgp:2
	v_mfma_scale_f32_16x16x128_f8f6f4 v[62:65], v[214:217], v[178:183], v[62:65], v177, v152 op_sel_hi:[0,0,0] cbsz:4 blgp:2
	v_mfma_scale_f32_16x16x128_f8f6f4 v[46:49], v[218:221], v[178:183], v[46:49], v177, v152 op_sel_hi:[0,0,0] cbsz:4 blgp:2
	v_mfma_scale_f32_16x16x128_f8f6f4 v[30:33], v[222:225], v[178:183], v[30:33], v177, v152 op_sel_hi:[0,0,0] cbsz:4 blgp:2
	v_mfma_scale_f32_16x16x128_f8f6f4 v[18:21], v[226:229], v[178:183], v[238:241], v177, v152 op_sel_hi:[0,0,0] cbsz:4 blgp:2
	v_mfma_scale_f32_16x16x128_f8f6f4 v[10:13], v[230:233], v[178:183], v[14:17], v177, v152 op_sel_hi:[0,0,0] cbsz:4 blgp:2
	v_mfma_scale_f32_16x16x128_f8f6f4 v[90:93], v[202:205], v[184:189], v[90:93], v177, v153 op_sel_hi:[0,0,0] cbsz:4 blgp:2
	v_mfma_scale_f32_16x16x128_f8f6f4 v[74:77], v[206:209], v[184:189], v[74:77], v177, v153 op_sel_hi:[0,0,0] cbsz:4 blgp:2
	v_mfma_scale_f32_16x16x128_f8f6f4 v[58:61], v[210:213], v[184:189], v[58:61], v177, v153 op_sel_hi:[0,0,0] cbsz:4 blgp:2
	v_mfma_scale_f32_16x16x128_f8f6f4 v[42:45], v[214:217], v[184:189], v[42:45], v177, v153 op_sel_hi:[0,0,0] cbsz:4 blgp:2
	v_mfma_scale_f32_16x16x128_f8f6f4 v[26:29], v[218:221], v[184:189], v[26:29], v177, v153 op_sel_hi:[0,0,0] cbsz:4 blgp:2
	v_mfma_scale_f32_16x16x128_f8f6f4 v[14:17], v[222:225], v[184:189], v[190:193], v177, v153 op_sel_hi:[0,0,0] cbsz:4 blgp:2
	v_mfma_scale_f32_16x16x128_f8f6f4 v[6:9], v[226:229], v[184:189], v[198:201], v177, v153 op_sel_hi:[0,0,0] cbsz:4 blgp:2
	v_mfma_scale_f32_16x16x128_f8f6f4 v[2:5], v[230:233], v[184:189], v[194:197], v177, v153 op_sel_hi:[0,0,0] cbsz:4 blgp:2
	s_barrier
	s_add_i32 s59, s59, 2
	s_addk_i32 s60, 0x1000
	v_lshl_add_u64 v[150:151], v[150:151], 0, s[38:39]
	v_lshl_add_u64 v[142:143], v[142:143], 0, s[30:31]
	v_lshl_add_u64 v[144:145], v[144:145], 0, s[30:31]
	v_lshl_add_u64 v[146:147], v[146:147], 0, s[30:31]
	s_cmp_lt_u32 s59, 28
	v_lshl_add_u64 v[148:149], v[148:149], 0, s[40:41]
	s_cbranch_scc1 .LBB3_3
	ds_read_b128 v[154:157], v175
	ds_read_b128 v[186:189], v175 offset:256
	ds_read_b128 v[190:193], v175 offset:512
	ds_read_b128 v[194:197], v175 offset:768
	ds_read_b128 v[198:201], v175 offset:1024
	ds_read_b128 v[202:205], v175 offset:1280
	ds_read_b128 v[206:209], v175 offset:1536
	ds_read_b128 v[210:213], v175 offset:1792
	ds_read_b64 v[142:143], v171
	ds_read_b64 v[144:145], v171 offset:8
	ds_read_b64 v[146:147], v171 offset:16
	ds_read_b64 v[148:149], v174
	ds_read_b64 v[150:151], v174 offset:8
	ds_read_b64 v[152:153], v174 offset:16
	ds_read_b64 v[174:175], v173
	ds_read_b64 v[176:177], v173 offset:8
	ds_read_b64 v[178:179], v173 offset:16
	ds_read_b64 v[180:181], v172
	ds_read_b64 v[182:183], v172 offset:8
	ds_read_b64 v[184:185], v172 offset:16
	v_add_u32_e32 v171, 0x21000, v248
	v_add_u32_e32 v172, 0x21020, v248
	v_add_u32_e32 v173, 0x21040, v248
	v_add_u32_e32 v214, 0x21060, v248
	s_mov_b64 s[0:1], 0x7c000
	s_mov_b32 m0, s61
	ds_read_u16 v171, v171
	ds_read_u16 v215, v172
	ds_read_u16 v216, v173
	ds_read_u16 v214, v214
	v_lshl_add_u64 v[172:173], v[138:139], 0, s[0:1]
	s_mov_b64 s[0:1], 0x7e000
	v_lshl_add_u64 v[138:139], v[138:139], 0, s[0:1]
	s_mov_b32 m0, s58
	s_mov_b64 s[0:1], 0x174000
	v_lshl_add_u64 v[138:139], v[140:141], 0, s[0:1]
	v_lshl_add_u64 v[140:141], v[138:139], 0, s[16:17]
	s_mov_b32 m0, s57
	v_lshl_add_u64 v[130:131], s[14:15], 0, v[130:131]
	global_load_lds_dwordx4 v[140:141], off
	v_lshl_add_u64 v[140:141], v[138:139], 0, s[18:19]
	s_mov_b32 m0, s56
	v_lshl_add_u64 v[138:139], v[138:139], 0, s[20:21]
	global_load_lds_dwordx4 v[140:141], off
	s_mov_b32 m0, s55
	s_mov_b64 s[0:1], 0xf800
	global_load_lds_dwordx4 v[138:139], off
	v_lshl_add_u64 v[130:131], v[130:131], 0, s[0:1]
	s_add_i32 m0, s9, 0x21800
	s_waitcnt lgkmcnt(0)
	v_mov_b32_e32 v172, v216
	global_load_lds_dword v[130:131], off
	s_waitcnt vmcnt(6)
	s_waitcnt lgkmcnt(0)
	v_mov_b32_e32 v130, v171
	v_mov_b32_e32 v131, v215
	v_mov_b32_e32 v217, v214
	s_barrier
	v_mov_b32_e32 v161, 0x7f7f7f7f
	s_nop 1
	v_mfma_scale_f32_16x16x128_f8f6f4 v[126:129], v[154:157], v[142:147], v[126:129], v161, v130 op_sel_hi:[0,0,0] cbsz:4 blgp:2
	v_mfma_scale_f32_16x16x128_f8f6f4 v[122:125], v[186:189], v[142:147], v[122:125], v161, v130 op_sel_hi:[0,0,0] cbsz:4 blgp:2
	v_mfma_scale_f32_16x16x128_f8f6f4 v[114:117], v[190:193], v[142:147], v[114:117], v161, v130 op_sel_hi:[0,0,0] cbsz:4 blgp:2
	v_mfma_scale_f32_16x16x128_f8f6f4 v[102:105], v[194:197], v[142:147], v[102:105], v161, v130 op_sel_hi:[0,0,0] cbsz:4 blgp:2
	v_mfma_scale_f32_16x16x128_f8f6f4 v[86:89], v[198:201], v[142:147], v[86:89], v161, v130 op_sel_hi:[0,0,0] cbsz:4 blgp:2
	v_mfma_scale_f32_16x16x128_f8f6f4 v[70:73], v[202:205], v[142:147], v[70:73], v161, v130 op_sel_hi:[0,0,0] cbsz:4 blgp:2
	v_mfma_scale_f32_16x16x128_f8f6f4 v[54:57], v[206:209], v[142:147], v[54:57], v161, v130 op_sel_hi:[0,0,0] cbsz:4 blgp:2
	v_mfma_scale_f32_16x16x128_f8f6f4 v[38:41], v[210:213], v[142:147], v[38:41], v161, v130 op_sel_hi:[0,0,0] cbsz:4 blgp:2
	v_mfma_scale_f32_16x16x128_f8f6f4 v[118:121], v[154:157], v[148:153], v[118:121], v161, v131 op_sel_hi:[0,0,0] cbsz:4 blgp:2
	v_mfma_scale_f32_16x16x128_f8f6f4 v[110:113], v[186:189], v[148:153], v[110:113], v161, v131 op_sel_hi:[0,0,0] cbsz:4 blgp:2
	v_mfma_scale_f32_16x16x128_f8f6f4 v[98:101], v[190:193], v[148:153], v[98:101], v161, v131 op_sel_hi:[0,0,0] cbsz:4 blgp:2
	v_mfma_scale_f32_16x16x128_f8f6f4 v[82:85], v[194:197], v[148:153], v[82:85], v161, v131 op_sel_hi:[0,0,0] cbsz:4 blgp:2
	v_mfma_scale_f32_16x16x128_f8f6f4 v[66:69], v[198:201], v[148:153], v[66:69], v161, v131 op_sel_hi:[0,0,0] cbsz:4 blgp:2
	v_mfma_scale_f32_16x16x128_f8f6f4 v[50:53], v[202:205], v[148:153], v[50:53], v161, v131 op_sel_hi:[0,0,0] cbsz:4 blgp:2
	v_mfma_scale_f32_16x16x128_f8f6f4 v[34:37], v[206:209], v[148:153], v[34:37], v161, v131 op_sel_hi:[0,0,0] cbsz:4 blgp:2
	v_mfma_scale_f32_16x16x128_f8f6f4 v[138:141], v[210:213], v[148:153], v[22:25], v161, v131 op_sel_hi:[0,0,0] cbsz:4 blgp:2
	v_mfma_scale_f32_16x16x128_f8f6f4 v[106:109], v[154:157], v[174:179], v[106:109], v161, v172 op_sel_hi:[0,0,0] cbsz:4 blgp:2
	v_mfma_scale_f32_16x16x128_f8f6f4 v[94:97], v[186:189], v[174:179], v[94:97], v161, v172 op_sel_hi:[0,0,0] cbsz:4 blgp:2
	v_mfma_scale_f32_16x16x128_f8f6f4 v[78:81], v[190:193], v[174:179], v[78:81], v161, v172 op_sel_hi:[0,0,0] cbsz:4 blgp:2
	v_mfma_scale_f32_16x16x128_f8f6f4 v[62:65], v[194:197], v[174:179], v[62:65], v161, v172 op_sel_hi:[0,0,0] cbsz:4 blgp:2
	v_mfma_scale_f32_16x16x128_f8f6f4 v[46:49], v[198:201], v[174:179], v[46:49], v161, v172 op_sel_hi:[0,0,0] cbsz:4 blgp:2
	v_mfma_scale_f32_16x16x128_f8f6f4 v[142:145], v[206:209], v[174:179], v[18:21], v161, v172 op_sel_hi:[0,0,0] cbsz:4 blgp:2
	v_mfma_scale_f32_16x16x128_f8f6f4 v[146:149], v[210:213], v[174:179], v[10:13], v161, v172 op_sel_hi:[0,0,0] cbsz:4 blgp:2
	v_mfma_scale_f32_16x16x128_f8f6f4 v[90:93], v[154:157], v[180:185], v[90:93], v161, v217 op_sel_hi:[0,0,0] cbsz:4 blgp:2
	v_mfma_scale_f32_16x16x128_f8f6f4 v[74:77], v[186:189], v[180:185], v[74:77], v161, v217 op_sel_hi:[0,0,0] cbsz:4 blgp:2
	v_mfma_scale_f32_16x16x128_f8f6f4 v[58:61], v[190:193], v[180:185], v[58:61], v161, v217 op_sel_hi:[0,0,0] cbsz:4 blgp:2
	v_mfma_scale_f32_16x16x128_f8f6f4 v[150:153], v[202:205], v[180:185], v[14:17], v161, v217 op_sel_hi:[0,0,0] cbsz:4 blgp:2
	v_mfma_scale_f32_16x16x128_f8f6f4 v[30:33], v[202:205], v[174:179], v[30:33], v161, v172 op_sel_hi:[0,0,0] cbsz:4 blgp:2
	v_mfma_scale_f32_16x16x128_f8f6f4 v[42:45], v[194:197], v[180:185], v[42:45], v161, v217 op_sel_hi:[0,0,0] cbsz:4 blgp:2
	v_mfma_scale_f32_16x16x128_f8f6f4 v[26:29], v[198:201], v[180:185], v[26:29], v161, v217 op_sel_hi:[0,0,0] cbsz:4 blgp:2
	v_mfma_scale_f32_16x16x128_f8f6f4 v[172:175], v[206:209], v[180:185], v[6:9], v161, v217 op_sel_hi:[0,0,0] cbsz:4 blgp:2
	v_mfma_scale_f32_16x16x128_f8f6f4 v[176:179], v[210:213], v[180:185], v[2:5], v161, v217 op_sel_hi:[0,0,0] cbsz:4 blgp:2
	s_barrier
	ds_read_b64 v[2:3], v167
	ds_read_b64 v[4:5], v167 offset:8
	ds_read_b64 v[6:7], v167 offset:16
	ds_read_b64 v[8:9], v170
	ds_read_b64 v[10:11], v170 offset:8
	ds_read_b64 v[12:13], v170 offset:16
	ds_read_b64 v[14:15], v169
	ds_read_b64 v[16:17], v169 offset:8
	ds_read_b64 v[18:19], v169 offset:16
	s_mov_b64 s[0:1], 0x175800
	s_mov_b32 m0, s52
	ds_read_b64 v[20:21], v168
	ds_read_b64 v[22:23], v168 offset:8
	ds_read_b64 v[24:25], v168 offset:16
	v_lshl_add_u64 v[130:131], v[132:133], 0, s[0:1]
	global_load_lds_dwordx4 v[130:131], off
	v_lshl_add_u64 v[130:131], v[134:135], 0, s[0:1]
	s_mov_b32 m0, s50
	v_lshrrev_b32_e32 v167, 8, v216
	global_load_lds_dwordx4 v[130:131], off
	v_lshl_add_u64 v[130:131], v[136:137], 0, s[0:1]
	s_mov_b32 m0, s49
	v_lshrrev_b32_e32 v168, 8, v214
	global_load_lds_dwordx4 v[130:131], off
	s_waitcnt vmcnt(3)
	s_waitcnt lgkmcnt(0)
	v_lshrrev_b32_e32 v130, 8, v171
	v_lshrrev_b32_e32 v131, 8, v215
	s_barrier
	v_mfma_scale_f32_16x16x128_f8f6f4 v[126:129], v[154:157], v[2:7], v[126:129], v161, v130 op_sel_hi:[0,0,0] cbsz:4 blgp:2
	v_mfma_scale_f32_16x16x128_f8f6f4 v[122:125], v[186:189], v[2:7], v[122:125], v161, v130 op_sel_hi:[0,0,0] cbsz:4 blgp:2
	v_mfma_scale_f32_16x16x128_f8f6f4 v[114:117], v[190:193], v[2:7], v[114:117], v161, v130 op_sel_hi:[0,0,0] cbsz:4 blgp:2
	v_mfma_scale_f32_16x16x128_f8f6f4 v[102:105], v[194:197], v[2:7], v[102:105], v161, v130 op_sel_hi:[0,0,0] cbsz:4 blgp:2
	v_mfma_scale_f32_16x16x128_f8f6f4 v[86:89], v[198:201], v[2:7], v[86:89], v161, v130 op_sel_hi:[0,0,0] cbsz:4 blgp:2
	v_mfma_scale_f32_16x16x128_f8f6f4 v[70:73], v[202:205], v[2:7], v[70:73], v161, v130 op_sel_hi:[0,0,0] cbsz:4 blgp:2
	v_mfma_scale_f32_16x16x128_f8f6f4 v[54:57], v[206:209], v[2:7], v[54:57], v161, v130 op_sel_hi:[0,0,0] cbsz:4 blgp:2
	v_mfma_scale_f32_16x16x128_f8f6f4 v[38:41], v[210:213], v[2:7], v[38:41], v161, v130 op_sel_hi:[0,0,0] cbsz:4 blgp:2
	v_mfma_scale_f32_16x16x128_f8f6f4 v[118:121], v[154:157], v[8:13], v[118:121], v161, v131 op_sel_hi:[0,0,0] cbsz:4 blgp:2
	v_mfma_scale_f32_16x16x128_f8f6f4 v[110:113], v[186:189], v[8:13], v[110:113], v161, v131 op_sel_hi:[0,0,0] cbsz:4 blgp:2
	v_mfma_scale_f32_16x16x128_f8f6f4 v[98:101], v[190:193], v[8:13], v[98:101], v161, v131 op_sel_hi:[0,0,0] cbsz:4 blgp:2
	v_mfma_scale_f32_16x16x128_f8f6f4 v[82:85], v[194:197], v[8:13], v[82:85], v161, v131 op_sel_hi:[0,0,0] cbsz:4 blgp:2
	v_mfma_scale_f32_16x16x128_f8f6f4 v[66:69], v[198:201], v[8:13], v[66:69], v161, v131 op_sel_hi:[0,0,0] cbsz:4 blgp:2
	v_mfma_scale_f32_16x16x128_f8f6f4 v[50:53], v[202:205], v[8:13], v[50:53], v161, v131 op_sel_hi:[0,0,0] cbsz:4 blgp:2
	v_mfma_scale_f32_16x16x128_f8f6f4 v[34:37], v[206:209], v[8:13], v[34:37], v161, v131 op_sel_hi:[0,0,0] cbsz:4 blgp:2
	v_mfma_scale_f32_16x16x128_f8f6f4 v[130:133], v[210:213], v[8:13], v[138:141], v161, v131 op_sel_hi:[0,0,0] cbsz:4 blgp:2
	v_mfma_scale_f32_16x16x128_f8f6f4 v[106:109], v[154:157], v[14:19], v[106:109], v161, v167 op_sel_hi:[0,0,0] cbsz:4 blgp:2
	v_mfma_scale_f32_16x16x128_f8f6f4 v[94:97], v[186:189], v[14:19], v[94:97], v161, v167 op_sel_hi:[0,0,0] cbsz:4 blgp:2
	v_mfma_scale_f32_16x16x128_f8f6f4 v[78:81], v[190:193], v[14:19], v[78:81], v161, v167 op_sel_hi:[0,0,0] cbsz:4 blgp:2
	v_mfma_scale_f32_16x16x128_f8f6f4 v[62:65], v[194:197], v[14:19], v[62:65], v161, v167 op_sel_hi:[0,0,0] cbsz:4 blgp:2
	v_mfma_scale_f32_16x16x128_f8f6f4 v[46:49], v[198:201], v[14:19], v[46:49], v161, v167 op_sel_hi:[0,0,0] cbsz:4 blgp:2
	v_mfma_scale_f32_16x16x128_f8f6f4 v[134:137], v[206:209], v[14:19], v[142:145], v161, v167 op_sel_hi:[0,0,0] cbsz:4 blgp:2
	v_mfma_scale_f32_16x16x128_f8f6f4 v[138:141], v[210:213], v[14:19], v[146:149], v161, v167 op_sel_hi:[0,0,0] cbsz:4 blgp:2
	v_mfma_scale_f32_16x16x128_f8f6f4 v[90:93], v[154:157], v[20:25], v[90:93], v161, v168 op_sel_hi:[0,0,0] cbsz:4 blgp:2
	v_mfma_scale_f32_16x16x128_f8f6f4 v[58:61], v[190:193], v[20:25], v[58:61], v161, v168 op_sel_hi:[0,0,0] cbsz:4 blgp:2
	v_mfma_scale_f32_16x16x128_f8f6f4 v[142:145], v[202:205], v[20:25], v[150:153], v161, v168 op_sel_hi:[0,0,0] cbsz:4 blgp:2
	v_mfma_scale_f32_16x16x128_f8f6f4 v[146:149], v[206:209], v[20:25], v[172:175], v161, v168 op_sel_hi:[0,0,0] cbsz:4 blgp:2
	v_mfma_scale_f32_16x16x128_f8f6f4 v[150:153], v[210:213], v[20:25], v[176:179], v161, v168 op_sel_hi:[0,0,0] cbsz:4 blgp:2
	v_mfma_scale_f32_16x16x128_f8f6f4 v[30:33], v[202:205], v[14:19], v[30:33], v161, v167 op_sel_hi:[0,0,0] cbsz:4 blgp:2
	v_mfma_scale_f32_16x16x128_f8f6f4 v[236:239], v[186:189], v[20:25], v[74:77], v161, v168 op_sel_hi:[0,0,0] cbsz:4 blgp:2
	v_mfma_scale_f32_16x16x128_f8f6f4 v[42:45], v[194:197], v[20:25], v[42:45], v161, v168 op_sel_hi:[0,0,0] cbsz:4 blgp:2
	v_mfma_scale_f32_16x16x128_f8f6f4 v[26:29], v[198:201], v[20:25], v[26:29], v161, v168 op_sel_hi:[0,0,0] cbsz:4 blgp:2
	s_barrier
	ds_read_b128 v[168:171], v166
	ds_read_b128 v[172:175], v166 offset:256
	ds_read_b128 v[176:179], v166 offset:512
	ds_read_b128 v[180:183], v166 offset:768
	ds_read_b128 v[184:187], v166 offset:1024
	ds_read_b128 v[188:191], v166 offset:1280
	ds_read_b128 v[192:195], v166 offset:1536
	ds_read_b128 v[196:199], v166 offset:1792
	ds_read_b64 v[2:3], v162
	ds_read_b64 v[4:5], v162 offset:8
	ds_read_b64 v[6:7], v162 offset:16
	ds_read_b64 v[8:9], v165
	ds_read_b64 v[10:11], v165 offset:8
	ds_read_b64 v[12:13], v165 offset:16
	ds_read_b64 v[14:15], v164
	ds_read_b64 v[16:17], v164 offset:8
	ds_read_b64 v[18:19], v164 offset:16
	ds_read_b64 v[20:21], v163
	ds_read_b64 v[22:23], v163 offset:8
	ds_read_b64 v[24:25], v163 offset:16
	v_add_u32_e32 v154, 0x21800, v248
	v_add_u32_e32 v155, 0x21820, v248
	v_add_u32_e32 v156, 0x21840, v248
	v_add_u32_e32 v157, 0x21860, v248
	ds_read_u16 v166, v154
	ds_read_u16 v167, v155
	ds_read_u16 v74, v156
	ds_read_u16 v75, v157
	s_waitcnt vmcnt(0)
	s_waitcnt lgkmcnt(0)
	s_waitcnt lgkmcnt(0)
	v_mov_b32_e32 v76, v166
	v_mov_b32_e32 v77, v167
	v_mov_b32_e32 v228, v74
	v_mov_b32_e32 v252, v75
	s_barrier
	v_mfma_scale_f32_16x16x128_f8f6f4 v[126:129], v[168:171], v[2:7], v[126:129], v161, v76 op_sel_hi:[0,0,0] cbsz:4 blgp:2
	v_mfma_scale_f32_16x16x128_f8f6f4 v[122:125], v[172:175], v[2:7], v[122:125], v161, v76 op_sel_hi:[0,0,0] cbsz:4 blgp:2
	v_mfma_scale_f32_16x16x128_f8f6f4 v[114:117], v[176:179], v[2:7], v[114:117], v161, v76 op_sel_hi:[0,0,0] cbsz:4 blgp:2
	v_mfma_scale_f32_16x16x128_f8f6f4 v[102:105], v[180:183], v[2:7], v[102:105], v161, v76 op_sel_hi:[0,0,0] cbsz:4 blgp:2
	v_mfma_scale_f32_16x16x128_f8f6f4 v[86:89], v[184:187], v[2:7], v[86:89], v161, v76 op_sel_hi:[0,0,0] cbsz:4 blgp:2
	v_mfma_scale_f32_16x16x128_f8f6f4 v[70:73], v[188:191], v[2:7], v[70:73], v161, v76 op_sel_hi:[0,0,0] cbsz:4 blgp:2
	v_mfma_scale_f32_16x16x128_f8f6f4 v[54:57], v[192:195], v[2:7], v[54:57], v161, v76 op_sel_hi:[0,0,0] cbsz:4 blgp:2
	v_mfma_scale_f32_16x16x128_f8f6f4 v[154:157], v[196:199], v[2:7], v[38:41], v161, v76 op_sel_hi:[0,0,0] cbsz:4 blgp:2
	v_mfma_scale_f32_16x16x128_f8f6f4 v[118:121], v[168:171], v[8:13], v[118:121], v161, v77 op_sel_hi:[0,0,0] cbsz:4 blgp:2
	v_mfma_scale_f32_16x16x128_f8f6f4 v[82:85], v[180:183], v[8:13], v[82:85], v161, v77 op_sel_hi:[0,0,0] cbsz:4 blgp:2
	v_mfma_scale_f32_16x16x128_f8f6f4 v[66:69], v[184:187], v[8:13], v[66:69], v161, v77 op_sel_hi:[0,0,0] cbsz:4 blgp:2
	v_mfma_scale_f32_16x16x128_f8f6f4 v[50:53], v[188:191], v[8:13], v[50:53], v161, v77 op_sel_hi:[0,0,0] cbsz:4 blgp:2
	v_mfma_scale_f32_16x16x128_f8f6f4 v[130:133], v[196:199], v[8:13], v[130:133], v161, v77 op_sel_hi:[0,0,0] cbsz:4 blgp:2
	v_mfma_scale_f32_16x16x128_f8f6f4 v[62:65], v[180:183], v[14:19], v[62:65], v161, v228 op_sel_hi:[0,0,0] cbsz:4 blgp:2
	v_mfma_scale_f32_16x16x128_f8f6f4 v[46:49], v[184:187], v[14:19], v[46:49], v161, v228 op_sel_hi:[0,0,0] cbsz:4 blgp:2
	v_mfma_scale_f32_16x16x128_f8f6f4 v[58:61], v[176:179], v[20:25], v[58:61], v161, v252 op_sel_hi:[0,0,0] cbsz:4 blgp:2
	v_mfma_scale_f32_16x16x128_f8f6f4 v[162:165], v[172:175], v[8:13], v[110:113], v161, v77 op_sel_hi:[0,0,0] cbsz:4 blgp:2
	v_mfma_scale_f32_16x16x128_f8f6f4 v[200:203], v[176:179], v[8:13], v[98:101], v161, v77 op_sel_hi:[0,0,0] cbsz:4 blgp:2
	v_mfma_scale_f32_16x16x128_f8f6f4 v[204:207], v[192:195], v[8:13], v[34:37], v161, v77 op_sel_hi:[0,0,0] cbsz:4 blgp:2
	v_mfma_scale_f32_16x16x128_f8f6f4 v[208:211], v[168:171], v[14:19], v[106:109], v161, v228 op_sel_hi:[0,0,0] cbsz:4 blgp:2
	v_mfma_scale_f32_16x16x128_f8f6f4 v[212:215], v[172:175], v[14:19], v[94:97], v161, v228 op_sel_hi:[0,0,0] cbsz:4 blgp:2
	v_mfma_scale_f32_16x16x128_f8f6f4 v[216:219], v[176:179], v[14:19], v[78:81], v161, v228 op_sel_hi:[0,0,0] cbsz:4 blgp:2
	v_mfma_scale_f32_16x16x128_f8f6f4 v[220:223], v[188:191], v[14:19], v[30:33], v161, v228 op_sel_hi:[0,0,0] cbsz:4 blgp:2
	v_mfma_scale_f32_16x16x128_f8f6f4 v[224:227], v[192:195], v[14:19], v[134:137], v161, v228 op_sel_hi:[0,0,0] cbsz:4 blgp:2
	v_mfma_scale_f32_16x16x128_f8f6f4 v[228:231], v[196:199], v[14:19], v[138:141], v161, v228 op_sel_hi:[0,0,0] cbsz:4 blgp:2
	v_mfma_scale_f32_16x16x128_f8f6f4 v[232:235], v[168:171], v[20:25], v[90:93], v161, v252 op_sel_hi:[0,0,0] cbsz:4 blgp:2
	v_mfma_scale_f32_16x16x128_f8f6f4 v[236:239], v[172:175], v[20:25], v[236:239], v161, v252 op_sel_hi:[0,0,0] cbsz:4 blgp:2
	v_mfma_scale_f32_16x16x128_f8f6f4 v[42:45], v[180:183], v[20:25], v[42:45], v161, v252 op_sel_hi:[0,0,0] cbsz:4 blgp:2
	v_mfma_scale_f32_16x16x128_f8f6f4 v[240:243], v[184:187], v[20:25], v[26:29], v161, v252 op_sel_hi:[0,0,0] cbsz:4 blgp:2
	v_mfma_scale_f32_16x16x128_f8f6f4 v[244:247], v[188:191], v[20:25], v[142:145], v161, v252 op_sel_hi:[0,0,0] cbsz:4 blgp:2
	v_mfma_scale_f32_16x16x128_f8f6f4 v[248:251], v[192:195], v[20:25], v[146:149], v161, v252 op_sel_hi:[0,0,0] cbsz:4 blgp:2
	v_mfma_scale_f32_16x16x128_f8f6f4 v[252:255], v[196:199], v[20:25], v[150:153], v161, v252 op_sel_hi:[0,0,0] cbsz:4 blgp:2
	s_barrier
	ds_read_b64 v[18:19], v1
	ds_read_b64 v[20:21], v1 offset:8
	ds_read_b64 v[22:23], v1 offset:16
	ds_read_b64 v[24:25], v160
	ds_read_b64 v[26:27], v160 offset:8
	ds_read_b64 v[28:29], v160 offset:16
	ds_read_b64 v[30:31], v159
	ds_read_b64 v[32:33], v159 offset:8
	ds_read_b64 v[34:35], v159 offset:16
	ds_read_b64 v[36:37], v158
	ds_read_b64 v[38:39], v158 offset:8
	ds_read_b64 v[40:41], v158 offset:16
	s_waitcnt lgkmcnt(0)
	v_lshrrev_b32_e32 v1, 8, v166
	v_lshrrev_b32_e32 v76, 8, v167
	v_lshrrev_b32_e32 v112, 8, v74
	v_lshrrev_b32_e32 v160, 8, v75
	s_barrier
	v_mfma_scale_f32_16x16x128_f8f6f4 v[14:17], v[168:171], v[18:23], v[126:129], v161, v1 op_sel_hi:[0,0,0] cbsz:4 blgp:2
	v_mfma_scale_f32_16x16x128_f8f6f4 v[10:13], v[172:175], v[18:23], v[122:125], v161, v1 op_sel_hi:[0,0,0] cbsz:4 blgp:2
	v_mfma_scale_f32_16x16x128_f8f6f4 v[6:9], v[176:179], v[18:23], v[114:117], v161, v1 op_sel_hi:[0,0,0] cbsz:4 blgp:2
	v_mfma_scale_f32_16x16x128_f8f6f4 v[2:5], v[180:183], v[18:23], v[102:105], v161, v1 op_sel_hi:[0,0,0] cbsz:4 blgp:2
	v_mfma_scale_f32_16x16x128_f8f6f4 v[108:111], v[184:187], v[18:23], v[86:89], v161, v1 op_sel_hi:[0,0,0] cbsz:4 blgp:2
	v_mfma_scale_f32_16x16x128_f8f6f4 v[104:107], v[188:191], v[18:23], v[70:73], v161, v1 op_sel_hi:[0,0,0] cbsz:4 blgp:2
	v_mfma_scale_f32_16x16x128_f8f6f4 v[100:103], v[192:195], v[18:23], v[54:57], v161, v1 op_sel_hi:[0,0,0] cbsz:4 blgp:2
	v_mfma_scale_f32_16x16x128_f8f6f4 v[96:99], v[196:199], v[18:23], v[154:157], v161, v1 op_sel_hi:[0,0,0] cbsz:4 blgp:2
	v_mfma_scale_f32_16x16x128_f8f6f4 v[156:159], v[168:171], v[24:29], v[118:121], v161, v76 op_sel_hi:[0,0,0] cbsz:4 blgp:2
	v_mfma_scale_f32_16x16x128_f8f6f4 v[152:155], v[172:175], v[24:29], v[162:165], v161, v76 op_sel_hi:[0,0,0] cbsz:4 blgp:2
	v_mfma_scale_f32_16x16x128_f8f6f4 v[148:151], v[176:179], v[24:29], v[200:203], v161, v76 op_sel_hi:[0,0,0] cbsz:4 blgp:2
	v_mfma_scale_f32_16x16x128_f8f6f4 v[144:147], v[180:183], v[24:29], v[82:85], v161, v76 op_sel_hi:[0,0,0] cbsz:4 blgp:2
	v_mfma_scale_f32_16x16x128_f8f6f4 v[92:95], v[184:187], v[24:29], v[66:69], v161, v76 op_sel_hi:[0,0,0] cbsz:4 blgp:2
	v_mfma_scale_f32_16x16x128_f8f6f4 v[88:91], v[188:191], v[24:29], v[50:53], v161, v76 op_sel_hi:[0,0,0] cbsz:4 blgp:2
	v_mfma_scale_f32_16x16x128_f8f6f4 v[84:87], v[192:195], v[24:29], v[204:207], v161, v76 op_sel_hi:[0,0,0] cbsz:4 blgp:2
	v_mfma_scale_f32_16x16x128_f8f6f4 v[80:83], v[196:199], v[24:29], v[130:133], v161, v76 op_sel_hi:[0,0,0] cbsz:4 blgp:2
	v_mfma_scale_f32_16x16x128_f8f6f4 v[140:143], v[168:171], v[30:35], v[208:211], v161, v112 op_sel_hi:[0,0,0] cbsz:4 blgp:2
	v_mfma_scale_f32_16x16x128_f8f6f4 v[136:139], v[172:175], v[30:35], v[212:215], v161, v112 op_sel_hi:[0,0,0] cbsz:4 blgp:2
	v_mfma_scale_f32_16x16x128_f8f6f4 v[132:135], v[176:179], v[30:35], v[216:219], v161, v112 op_sel_hi:[0,0,0] cbsz:4 blgp:2
	v_mfma_scale_f32_16x16x128_f8f6f4 v[128:131], v[180:183], v[30:35], v[62:65], v161, v112 op_sel_hi:[0,0,0] cbsz:4 blgp:2
	v_mfma_scale_f32_16x16x128_f8f6f4 v[76:79], v[184:187], v[30:35], v[46:49], v161, v112 op_sel_hi:[0,0,0] cbsz:4 blgp:2
	v_mfma_scale_f32_16x16x128_f8f6f4 v[72:75], v[188:191], v[30:35], v[220:223], v161, v112 op_sel_hi:[0,0,0] cbsz:4 blgp:2
	v_mfma_scale_f32_16x16x128_f8f6f4 v[68:71], v[192:195], v[30:35], v[224:227], v161, v112 op_sel_hi:[0,0,0] cbsz:4 blgp:2
	v_mfma_scale_f32_16x16x128_f8f6f4 v[64:67], v[196:199], v[30:35], v[228:231], v161, v112 op_sel_hi:[0,0,0] cbsz:4 blgp:2
	v_mfma_scale_f32_16x16x128_f8f6f4 v[124:127], v[168:171], v[36:41], v[232:235], v161, v160 op_sel_hi:[0,0,0] cbsz:4 blgp:2
	v_mfma_scale_f32_16x16x128_f8f6f4 v[120:123], v[172:175], v[36:41], v[236:239], v161, v160 op_sel_hi:[0,0,0] cbsz:4 blgp:2
	v_mfma_scale_f32_16x16x128_f8f6f4 v[116:119], v[176:179], v[36:41], v[58:61], v161, v160 op_sel_hi:[0,0,0] cbsz:4 blgp:2
	v_mfma_scale_f32_16x16x128_f8f6f4 v[112:115], v[180:183], v[36:41], v[42:45], v161, v160 op_sel_hi:[0,0,0] cbsz:4 blgp:2
	v_mfma_scale_f32_16x16x128_f8f6f4 v[60:63], v[184:187], v[36:41], v[240:243], v161, v160 op_sel_hi:[0,0,0] cbsz:4 blgp:2
	v_mfma_scale_f32_16x16x128_f8f6f4 v[56:59], v[188:191], v[36:41], v[244:247], v161, v160 op_sel_hi:[0,0,0] cbsz:4 blgp:2
	v_mfma_scale_f32_16x16x128_f8f6f4 v[52:55], v[192:195], v[36:41], v[248:251], v161, v160 op_sel_hi:[0,0,0] cbsz:4 blgp:2
	v_mfma_scale_f32_16x16x128_f8f6f4 v[48:51], v[196:199], v[36:41], v[252:255], v161, v160 op_sel_hi:[0,0,0] cbsz:4 blgp:2
	s_barrier
	s_cmpk_gt_u32 s33, 0xff
	s_cbranch_scc1 .LBB3_6
	s_barrier
.LBB3_6:
	s_mov_b32 s0, 0
	s_ashr_i32 s1, s0, 31
	v_add_u32_e32 v26, s0, v0
	v_ashrrev_i32_e32 v0, 6, v26
	v_and_b32_e32 v0, -4, v0
	v_bfe_u32 v177, v26, 5, 1
	v_lshl_add_u32 v178, s12, 3, v0
	v_bfe_u32 v27, v26, 4, 1
	v_or_b32_e32 v0, v178, v177
	s_lshl_b64 s[4:5], s[0:1], 2
	v_lshlrev_b32_e32 v36, 5, v0
	v_lshlrev_b32_e32 v179, 2, v27
	s_add_u32 s4, s10, s4
	v_or_b32_e32 v30, v36, v179
	s_addc_u32 s5, s11, s5
	v_ashrrev_i32_e32 v31, 31, v30
	v_lshl_add_u64 v[170:171], v[30:31], 2, s[4:5]
	global_load_dwordx4 v[192:195], v[170:171], off
	v_ashrrev_i32_e32 v31, 31, v36
	v_lshl_add_u64 v[172:173], v[30:31], 2, s[4:5]
	global_load_dwordx4 v[196:199], v[172:173], off offset:64
	v_and_b32_e32 v181, 0xcf, v26
	v_mul_u32_u24_e32 v160, 12, v27
	v_cmp_eq_u32_e64 s[0:1], 0, v27
	global_load_dwordx4 v[200:203], v[172:173], off offset:32
	s_lshl_b32 s11, s8, 6
	v_ashrrev_i32_e32 v30, 1, v178
	v_or_b32_e32 v176, 8, v179
	v_add_u32_e32 v34, s11, v30
	s_movk_i32 s9, 0x6000
	v_mov_b64_e32 v[32:33], s[2:3]
	s_add_u32 s6, s2, 0x3000000
	v_ashrrev_i32_e32 v35, 31, v34
	v_or_b32_e32 v30, v36, v176
	s_addc_u32 s7, s3, 0
	v_mad_i64_i32 v[168:169], s[8:9], v34, s9, v[32:33]
	v_lshlrev_b64 v[32:33], 10, v[34:35]
	v_lshl_add_u64 v[174:175], v[30:31], 2, s[4:5]
	v_lshl_add_u64 v[166:167], s[6:7], 0, v[32:33]
	global_load_dwordx4 v[204:207], v[174:175], off offset:64
	global_load_dwordx4 v[208:211], v[170:171], off offset:256
	global_load_dwordx4 v[212:215], v[172:173], off offset:320
	global_load_dwordx4 v[216:219], v[172:173], off offset:288
	global_load_dwordx4 v[220:223], v[174:175], off offset:320
	v_permlane32_swap_b32_e32 v14, v6
	v_permlane32_swap_b32_e32 v15, v7
	v_permlane32_swap_b32_e32 v16, v8
	v_permlane32_swap_b32_e32 v17, v9
	v_permlane32_swap_b32_e32 v10, v2
	v_permlane32_swap_b32_e32 v11, v3
	s_mov_b32 s20, 0x3e6d3388
	s_mov_b32 s22, 0xbf3a00e3
	s_mov_b32 s16, 0x3f07dc22
	s_mov_b32 s14, 0xbf38aa3b
	v_mov_b64_e32 v[0:1], s[22:23]
	s_mov_b32 s18, 0x3f35f0e3
	s_mov_b32 s10, 0xbe11a98e
	s_mov_b32 s12, 0x3e027906
	v_permlane32_swap_b32_e32 v12, v4
	v_permlane32_swap_b32_e32 v13, v5
	s_mov_b32 s9, 0x700000
	v_mov_b32_e32 v182, 0xffffff7f
	v_mov_b32_e32 v183, 0x64
	s_mov_b32 s8, 0xc2000000
	v_lshlrev_b32_e32 v180, 9, v177
	v_mov_b32_e32 v161, 0
	v_mov_b32_e32 v165, v161
	v_lshl_or_b32 v162, v181, 1, v180
	s_waitcnt vmcnt(4)
	v_pk_mul_f32 v[14:15], v[192:193], v[14:15]
	s_nop 0
	v_and_b32_e32 v19, 0x7fffffff, v15
	v_and_b32_e32 v18, 0x7fffffff, v14
	v_pk_mul_f32 v[16:17], v[194:195], v[16:17]
	v_pk_mul_f32 v[10:11], v[196:197], v[10:11]
	v_pk_fma_f32 v[22:23], v[18:19], s[20:21], 1.0 op_sel_hi:[1,0,0]
	v_and_b32_e32 v35, 0x7fffffff, v17
	v_and_b32_e32 v34, 0x7fffffff, v16
	v_rcp_f32_e32 v22, v22
	v_rcp_f32_e32 v23, v23
	v_pk_fma_f32 v[38:39], v[34:35], s[20:21], 1.0 op_sel_hi:[1,0,0]
	v_pk_mul_f32 v[20:21], v[14:15], v[14:15]
	v_rcp_f32_e32 v38, v38
	v_rcp_f32_e32 v39, v39
	v_pk_mul_f32 v[20:21], v[20:21], s[14:15] op_sel_hi:[1,0]
	v_pk_fma_f32 v[44:45], v[22:23], s[16:17], v[0:1] op_sel_hi:[1,0,0]
	v_pk_mul_f32 v[36:37], v[16:17], v[16:17]
	v_exp_f32_e32 v20, v20
	v_exp_f32_e32 v21, v21
	v_pk_fma_f32 v[44:45], v[22:23], v[44:45], s[18:19] op_sel_hi:[1,1,0]
	v_pk_mul_f32 v[36:37], v[36:37], s[14:15] op_sel_hi:[1,0]
	v_pk_fma_f32 v[46:47], v[38:39], s[16:17], v[0:1] op_sel_hi:[1,0,0]
	v_pk_fma_f32 v[44:45], v[22:23], v[44:45], s[10:11] op_sel_hi:[1,1,0]
	v_and_b32_e32 v41, 0x7fffffff, v11
	v_and_b32_e32 v40, 0x7fffffff, v10
	v_exp_f32_e32 v36, v36
	v_exp_f32_e32 v37, v37
	v_pk_fma_f32 v[46:47], v[38:39], v[46:47], s[18:19] op_sel_hi:[1,1,0]
	v_pk_fma_f32 v[44:45], v[22:23], v[44:45], s[12:13] op_sel_hi:[1,1,0]
	v_pk_fma_f32 v[42:43], v[40:41], s[20:21], 1.0 op_sel_hi:[1,0,0]
	v_pk_fma_f32 v[46:47], v[38:39], v[46:47], s[10:11] op_sel_hi:[1,1,0]
	v_pk_mul_f32 v[22:23], v[22:23], v[44:45]
	v_rcp_f32_e32 v42, v42
	v_pk_fma_f32 v[46:47], v[38:39], v[46:47], s[12:13] op_sel_hi:[1,1,0]
	v_pk_fma_f32 v[20:21], v[20:21], v[22:23], 0.5 op_sel_hi:[1,1,0] neg_lo:[1,0,0] neg_hi:[1,0,0]
	v_rcp_f32_e32 v43, v43
	v_pk_mul_f32 v[38:39], v[38:39], v[46:47]
	v_pk_mul_f32 v[18:19], v[18:19], v[20:21]
	v_pk_mul_f32 v[20:21], v[10:11], v[10:11]
	v_pk_fma_f32 v[14:15], v[14:15], 0.5, v[18:19] op_sel_hi:[1,0,1]
	v_pk_fma_f32 v[18:19], v[36:37], v[38:39], 0.5 op_sel_hi:[1,1,0] neg_lo:[1,0,0] neg_hi:[1,0,0]
	v_pk_mul_f32 v[20:21], v[20:21], s[14:15] op_sel_hi:[1,0]
	v_pk_mul_f32 v[18:19], v[34:35], v[18:19]
	v_pk_mul_f32 v[12:13], v[198:199], v[12:13]
	v_pk_fma_f32 v[16:17], v[16:17], 0.5, v[18:19] op_sel_hi:[1,0,1]
	v_pk_fma_f32 v[18:19], v[42:43], s[16:17], v[0:1] op_sel_hi:[1,0,0]
	v_exp_f32_e32 v20, v20
	v_pk_fma_f32 v[18:19], v[42:43], v[18:19], s[18:19] op_sel_hi:[1,1,0]
	v_exp_f32_e32 v21, v21
	v_and_b32_e32 v23, 0x7fffffff, v13
	v_and_b32_e32 v22, 0x7fffffff, v12
	v_pk_fma_f32 v[18:19], v[42:43], v[18:19], s[10:11] op_sel_hi:[1,1,0]
	v_pk_fma_f32 v[24:25], v[22:23], s[20:21], 1.0 op_sel_hi:[1,0,0]
	v_pk_fma_f32 v[18:19], v[42:43], v[18:19], s[12:13] op_sel_hi:[1,1,0]
	v_rcp_f32_e32 v24, v24
	v_rcp_f32_e32 v25, v25
	v_pk_mul_f32 v[18:19], v[42:43], v[18:19]
	v_pk_mul_f32 v[6:7], v[200:201], v[6:7]
	v_pk_fma_f32 v[18:19], v[20:21], v[18:19], 0.5 op_sel_hi:[1,1,0] neg_lo:[1,0,0] neg_hi:[1,0,0]
	v_pk_mul_f32 v[20:21], v[12:13], v[12:13]
	v_pk_mul_f32 v[18:19], v[40:41], v[18:19]
	v_pk_mul_f32 v[20:21], v[20:21], s[14:15] op_sel_hi:[1,0]
	v_pk_fma_f32 v[10:11], v[10:11], 0.5, v[18:19] op_sel_hi:[1,0,1]
	v_pk_fma_f32 v[18:19], v[24:25], s[16:17], v[0:1] op_sel_hi:[1,0,0]
	v_exp_f32_e32 v20, v20
	v_pk_fma_f32 v[18:19], v[24:25], v[18:19], s[18:19] op_sel_hi:[1,1,0]
	v_exp_f32_e32 v21, v21
	v_pk_fma_f32 v[18:19], v[24:25], v[18:19], s[10:11] op_sel_hi:[1,1,0]
	v_pk_mul_f32 v[8:9], v[202:203], v[8:9]
	v_pk_fma_f32 v[18:19], v[24:25], v[18:19], s[12:13] op_sel_hi:[1,1,0]
	v_pk_mul_f32 v[2:3], v[204:205], v[2:3]
	v_pk_mul_f32 v[18:19], v[24:25], v[18:19]
	v_and_b32_e32 v25, 0x7fffffff, v7
	v_and_b32_e32 v24, 0x7fffffff, v6
	v_pk_fma_f32 v[26:27], v[24:25], s[20:21], 1.0 op_sel_hi:[1,0,0]
	v_pk_fma_f32 v[18:19], v[20:21], v[18:19], 0.5 op_sel_hi:[1,1,0] neg_lo:[1,0,0] neg_hi:[1,0,0]
	v_rcp_f32_e32 v26, v26
	v_rcp_f32_e32 v27, v27
	v_pk_mul_f32 v[18:19], v[22:23], v[18:19]
	v_pk_mul_f32 v[20:21], v[6:7], v[6:7]
	v_pk_fma_f32 v[12:13], v[12:13], 0.5, v[18:19] op_sel_hi:[1,0,1]
	v_pk_fma_f32 v[18:19], v[26:27], s[16:17], v[0:1] op_sel_hi:[1,0,0]
	v_pk_mul_f32 v[20:21], v[20:21], s[14:15] op_sel_hi:[1,0]
	v_pk_fma_f32 v[18:19], v[26:27], v[18:19], s[18:19] op_sel_hi:[1,1,0]
	v_exp_f32_e32 v20, v20
	v_pk_fma_f32 v[18:19], v[26:27], v[18:19], s[10:11] op_sel_hi:[1,1,0]
	v_exp_f32_e32 v21, v21
	v_pk_fma_f32 v[18:19], v[26:27], v[18:19], s[12:13] op_sel_hi:[1,1,0]
	v_and_b32_e32 v23, 0x7fffffff, v9
	v_and_b32_e32 v22, 0x7fffffff, v8
	v_pk_mul_f32 v[18:19], v[26:27], v[18:19]
	v_pk_fma_f32 v[26:27], v[22:23], s[20:21], 1.0 op_sel_hi:[1,0,0]
	v_pk_fma_f32 v[18:19], v[20:21], v[18:19], 0.5 op_sel_hi:[1,1,0] neg_lo:[1,0,0] neg_hi:[1,0,0]
	v_rcp_f32_e32 v26, v26
	v_rcp_f32_e32 v27, v27
	v_pk_mul_f32 v[18:19], v[24:25], v[18:19]
	v_pk_mul_f32 v[20:21], v[8:9], v[8:9]
	v_pk_fma_f32 v[6:7], v[6:7], 0.5, v[18:19] op_sel_hi:[1,0,1]
	v_pk_fma_f32 v[18:19], v[26:27], s[16:17], v[0:1] op_sel_hi:[1,0,0]
	v_pk_mul_f32 v[20:21], v[20:21], s[14:15] op_sel_hi:[1,0]
	v_pk_fma_f32 v[18:19], v[26:27], v[18:19], s[18:19] op_sel_hi:[1,1,0]
	v_exp_f32_e32 v20, v20
	v_pk_fma_f32 v[18:19], v[26:27], v[18:19], s[10:11] op_sel_hi:[1,1,0]
	v_exp_f32_e32 v21, v21
	v_pk_fma_f32 v[18:19], v[26:27], v[18:19], s[12:13] op_sel_hi:[1,1,0]
	v_and_b32_e32 v25, 0x7fffffff, v3
	v_and_b32_e32 v24, 0x7fffffff, v2
	v_pk_mul_f32 v[18:19], v[26:27], v[18:19]
	v_pk_fma_f32 v[26:27], v[24:25], s[20:21], 1.0 op_sel_hi:[1,0,0]
	v_pk_fma_f32 v[18:19], v[20:21], v[18:19], 0.5 op_sel_hi:[1,1,0] neg_lo:[1,0,0] neg_hi:[1,0,0]
	v_rcp_f32_e32 v26, v26
	v_rcp_f32_e32 v27, v27
	v_pk_mul_f32 v[18:19], v[22:23], v[18:19]
	v_pk_mul_f32 v[20:21], v[2:3], v[2:3]
	v_pk_fma_f32 v[8:9], v[8:9], 0.5, v[18:19] op_sel_hi:[1,0,1]
	v_pk_fma_f32 v[18:19], v[26:27], s[16:17], v[0:1] op_sel_hi:[1,0,0]
	v_pk_mul_f32 v[20:21], v[20:21], s[14:15] op_sel_hi:[1,0]
	v_pk_fma_f32 v[18:19], v[26:27], v[18:19], s[18:19] op_sel_hi:[1,1,0]
	v_exp_f32_e32 v20, v20
	v_pk_fma_f32 v[18:19], v[26:27], v[18:19], s[10:11] op_sel_hi:[1,1,0]
	v_exp_f32_e32 v21, v21
	v_pk_mul_f32 v[4:5], v[206:207], v[4:5]
	v_pk_fma_f32 v[18:19], v[26:27], v[18:19], s[12:13] op_sel_hi:[1,1,0]
	v_and_b32_e32 v23, 0x7fffffff, v5
	v_and_b32_e32 v22, 0x7fffffff, v4
	v_pk_mul_f32 v[18:19], v[26:27], v[18:19]
	v_pk_fma_f32 v[26:27], v[22:23], s[20:21], 1.0 op_sel_hi:[1,0,0]
	v_pk_fma_f32 v[18:19], v[20:21], v[18:19], 0.5 op_sel_hi:[1,1,0] neg_lo:[1,0,0] neg_hi:[1,0,0]
	v_rcp_f32_e32 v26, v26
	v_rcp_f32_e32 v27, v27
	v_pk_mul_f32 v[18:19], v[24:25], v[18:19]
	v_pk_fma_f32 v[0:1], v[26:27], s[16:17], v[0:1] op_sel_hi:[1,0,0]
	v_pk_fma_f32 v[2:3], v[2:3], 0.5, v[18:19] op_sel_hi:[1,0,1]
	v_pk_mul_f32 v[18:19], v[4:5], v[4:5]
	v_pk_fma_f32 v[0:1], v[26:27], v[0:1], s[18:19] op_sel_hi:[1,1,0]
	v_pk_mul_f32 v[18:19], v[18:19], s[14:15] op_sel_hi:[1,0]
	v_pk_fma_f32 v[0:1], v[26:27], v[0:1], s[10:11] op_sel_hi:[1,1,0]
	v_exp_f32_e32 v18, v18
	v_exp_f32_e32 v19, v19
	v_pk_fma_f32 v[0:1], v[26:27], v[0:1], s[12:13] op_sel_hi:[1,1,0]
	s_movk_i32 s13, 0xff9c
	v_pk_mul_f32 v[0:1], v[26:27], v[0:1]
	s_mov_b32 s15, 0x42000000
	v_pk_fma_f32 v[0:1], v[18:19], v[0:1], 0.5 op_sel_hi:[1,1,0] neg_lo:[1,0,0] neg_hi:[1,0,0]
	v_max_f32_e64 v18, |v12|, |v13|
	v_pk_mul_f32 v[0:1], v[22:23], v[0:1]
	s_nop 0
	v_pk_fma_f32 v[0:1], v[4:5], 0.5, v[0:1] op_sel_hi:[1,0,1]
	v_max_f32_e64 v4, |v14|, |v15|
	v_max_f32_e64 v5, |v16|, |v17|
	v_max3_f32 v4, v4, 0, v5
	v_max_f32_e64 v5, |v10|, |v11|
	v_max3_f32 v4, v4, v5, v18
	v_max_f32_e64 v5, |v6|, |v7|
	v_max_f32_e64 v18, |v8|, |v9|
	v_max3_f32 v4, v4, v5, v18
	v_max_f32_e64 v5, |v2|, |v3|
	v_max_f32_e64 v18, |v0|, |v1|
	v_max3_f32 v4, v4, v5, v18
	v_mov_b32_e32 v5, v4
	s_nop 1
	v_permlane16_swap_b32_e32 v4, v5
	v_max_f32_e32 v5, v5, v5
	v_max_f32_e32 v4, v4, v4
	v_max_f32_e32 v4, v4, v5
	v_lshrrev_b32_e32 v5, 23, v4
	v_and_b32_e32 v4, 0x7fffff, v4
	v_cmp_lt_u32_e32 vcc, s9, v4
	s_nop 1
	v_addc_co_u32_e32 v4, vcc, v5, v182, vcc
	v_med3_i32 v163, v4, s13, v183
	v_lshlrev_b32_e32 v4, 23, v163
	v_sub_u32_e32 v4, 1.0, v4
	v_pk_mul_f32 v[40:41], v[4:5], v[6:7] op_sel_hi:[0,1]
	v_pk_mul_f32 v[42:43], v[4:5], v[8:9] op_sel_hi:[0,1]
	v_pk_mul_f32 v[44:45], v[4:5], v[2:3] op_sel_hi:[0,1]
	v_pk_mul_f32 v[46:47], v[4:5], v[0:1] op_sel_hi:[0,1]
	v_pk_mul_f32 v[32:33], v[4:5], v[14:15] op_sel_hi:[0,1]
	v_pk_mul_f32 v[34:35], v[4:5], v[16:17] op_sel_hi:[0,1]
	v_pk_mul_f32 v[36:37], v[4:5], v[10:11] op_sel_hi:[0,1]
	v_pk_mul_f32 v[38:39], v[4:5], v[12:13] op_sel_hi:[0,1]
	v_mov_b32_e32 v0, v40
	v_mov_b32_e32 v1, v41
	v_mov_b32_e32 v2, v42
	v_mov_b32_e32 v3, v43
	v_mov_b32_e32 v4, v44
	v_mov_b32_e32 v5, v45
	v_mov_b32_e32 v6, v46
	v_mov_b32_e32 v7, v47
	v_cvt_scalef32_2xpk16_fp6_f32 v[184:189], v[32:47], v[0:15], 1.0
	v_cvt_scalef32_pk32_f32_fp6 v[0:31], v[184:189], s15
	v_mov_b32_e32 v16, v0
	v_mov_b32_e32 v17, v2
	v_mov_b32_e32 v2, v1
	v_mov_b32_e32 v0, v4
	v_mov_b32_e32 v1, v6
	v_pk_fma_f32 v[18:19], v[34:35], s[8:9], v[0:1] op_sel_hi:[1,0,1]
	v_mov_b32_e32 v0, v8
	v_mov_b32_e32 v1, v10
	v_mov_b32_e32 v6, v5
	v_pk_fma_f32 v[20:21], v[36:37], s[8:9], v[0:1] op_sel_hi:[1,0,1]
	v_mov_b32_e32 v10, v9
	v_mov_b32_e32 v1, v14
	v_mov_b32_e32 v14, v13
	v_pk_fma_f32 v[24:25], v[40:41], s[8:9], v[2:3] op_sel_hi:[1,0,1]
	v_pk_fma_f32 v[26:27], v[42:43], s[8:9], v[6:7] op_sel_hi:[1,0,1]
	v_pk_fma_f32 v[28:29], v[44:45], s[8:9], v[10:11] op_sel_hi:[1,0,1]
	v_mov_b32_e32 v0, v12
	v_pk_fma_f32 v[30:31], v[46:47], s[8:9], v[14:15] op_sel_hi:[1,0,1]
	v_pk_fma_f32 v[16:17], v[32:33], s[8:9], v[16:17] op_sel_hi:[1,0,1]
	v_pk_fma_f32 v[22:23], v[38:39], s[8:9], v[0:1] op_sel_hi:[1,0,1]
	v_mov_b32_e32 v0, v24
	v_mov_b32_e32 v1, v25
	v_mov_b32_e32 v2, v26
	v_mov_b32_e32 v3, v27
	v_mov_b32_e32 v4, v28
	v_mov_b32_e32 v5, v29
	v_mov_b32_e32 v6, v30
	v_mov_b32_e32 v7, v31
	v_cvt_scalef32_2xpk16_fp6_f32 v[0:5], v[16:31], v[0:15], 1.0
	v_or_b32_e32 v3, v181, v180
	v_mul_u32_u24_e32 v164, 24, v3
	v_lshl_add_u64 v[4:5], v[168:169], 0, v[164:165]
	v_lshl_add_u64 v[4:5], v[4:5], 0, v[160:161]
	global_store_dwordx3 v[4:5], v[184:186], off nt
	v_add_co_u32_e32 v4, vcc, 0x1000, v4
	v_xor_b32_e32 v0, 0x20820820, v0
	v_xor_b32_e32 v1, 0x8208208, v1
	v_xor_b32_e32 v2, 0x82082082, v2
	v_addc_co_u32_e32 v5, vcc, 0, v5, vcc
	global_store_dwordx3 v[4:5], v[0:2], off offset:2048 nt
	s_and_saveexec_b64 s[24:25], s[0:1]
	s_cbranch_execz .LBB3_8
	v_mov_b32_e32 v1, 0x7a00
	v_add_u32_e32 v0, 0x7f, v163
	v_lshl_add_u32 v1, v163, 8, v1
	v_mov_b32_e32 v163, v161
	v_or_b32_e32 v2, v1, v0
	v_lshl_add_u64 v[0:1], v[166:167], 0, v[162:163]
	global_store_short v[0:1], v2, off
.LBB3_8:
	s_or_b64 exec, exec, s[24:25]
	v_permlane32_swap_b32_e32 v156, v148
	v_permlane32_swap_b32_e32 v157, v149
	v_permlane32_swap_b32_e32 v158, v150
	v_permlane32_swap_b32_e32 v159, v151
	v_permlane32_swap_b32_e32 v154, v146
	v_permlane32_swap_b32_e32 v155, v147
	v_permlane32_swap_b32_e32 v152, v144
	v_permlane32_swap_b32_e32 v153, v145
	v_mov_b64_e32 v[16:17], s[22:23]
	v_pk_mul_f32 v[0:1], v[192:193], v[156:157]
	v_pk_mul_f32 v[2:3], v[194:195], v[158:159]
	v_and_b32_e32 v19, 0x7fffffff, v1
	v_and_b32_e32 v18, 0x7fffffff, v0
	v_pk_mul_f32 v[6:7], v[198:199], v[154:155]
	v_and_b32_e32 v23, 0x7fffffff, v3
	v_and_b32_e32 v22, 0x7fffffff, v2
	v_pk_fma_f32 v[36:37], v[18:19], s[20:21], 1.0 op_sel_hi:[1,0,0]
	v_pk_mul_f32 v[4:5], v[196:197], v[152:153]
	v_and_b32_e32 v31, 0x7fffffff, v7
	v_and_b32_e32 v30, 0x7fffffff, v6
	v_pk_fma_f32 v[38:39], v[22:23], s[20:21], 1.0 op_sel_hi:[1,0,0]
	v_rcp_f32_e32 v36, v36
	v_rcp_f32_e32 v37, v37
	v_and_b32_e32 v27, 0x7fffffff, v5
	v_and_b32_e32 v26, 0x7fffffff, v4
	v_pk_fma_f32 v[42:43], v[30:31], s[20:21], 1.0 op_sel_hi:[1,0,0]
	v_rcp_f32_e32 v38, v38
	v_rcp_f32_e32 v39, v39
	v_pk_fma_f32 v[40:41], v[26:27], s[20:21], 1.0 op_sel_hi:[1,0,0]
	v_rcp_f32_e32 v42, v42
	v_rcp_f32_e32 v43, v43
	v_pk_mul_f32 v[20:21], v[0:1], v[0:1]
	v_rcp_f32_e32 v40, v40
	v_rcp_f32_e32 v41, v41
	v_pk_mul_f32 v[24:25], v[2:3], v[2:3]
	v_pk_mul_f32 v[20:21], v[20:21], s[14:15] op_sel_hi:[1,0]
	v_pk_fma_f32 v[46:47], v[36:37], s[16:17], v[16:17] op_sel_hi:[1,0,0]
	v_pk_mul_f32 v[8:9], v[200:201], v[148:149]
	v_pk_mul_f32 v[32:33], v[6:7], v[6:7]
	v_pk_mul_f32 v[24:25], v[24:25], s[14:15] op_sel_hi:[1,0]
	v_exp_f32_e32 v20, v20
	v_exp_f32_e32 v21, v21
	v_pk_fma_f32 v[148:149], v[38:39], s[16:17], v[16:17] op_sel_hi:[1,0,0]
	v_pk_fma_f32 v[46:47], v[36:37], v[46:47], s[18:19] op_sel_hi:[1,1,0]
	v_pk_mul_f32 v[28:29], v[4:5], v[4:5]
	v_pk_mul_f32 v[32:33], v[32:33], s[14:15] op_sel_hi:[1,0]
	v_exp_f32_e32 v24, v24
	v_exp_f32_e32 v25, v25
	v_pk_fma_f32 v[154:155], v[42:43], s[16:17], v[16:17] op_sel_hi:[1,0,0]
	v_pk_fma_f32 v[148:149], v[38:39], v[148:149], s[18:19] op_sel_hi:[1,1,0]
	v_pk_fma_f32 v[46:47], v[36:37], v[46:47], s[10:11] op_sel_hi:[1,1,0]
	v_and_b32_e32 v35, 0x7fffffff, v9
	v_and_b32_e32 v34, 0x7fffffff, v8
	v_pk_mul_f32 v[28:29], v[28:29], s[14:15] op_sel_hi:[1,0]
	v_exp_f32_e32 v32, v32
	v_exp_f32_e32 v33, v33
	v_pk_fma_f32 v[152:153], v[40:41], s[16:17], v[16:17] op_sel_hi:[1,0,0]
	v_pk_fma_f32 v[154:155], v[42:43], v[154:155], s[18:19] op_sel_hi:[1,1,0]
	v_pk_fma_f32 v[148:149], v[38:39], v[148:149], s[10:11] op_sel_hi:[1,1,0]
	v_pk_fma_f32 v[46:47], v[36:37], v[46:47], s[12:13] op_sel_hi:[1,1,0]
	v_pk_fma_f32 v[44:45], v[34:35], s[20:21], 1.0 op_sel_hi:[1,0,0]
	v_exp_f32_e32 v28, v28
	v_exp_f32_e32 v29, v29
	v_pk_fma_f32 v[152:153], v[40:41], v[152:153], s[18:19] op_sel_hi:[1,1,0]
	v_pk_fma_f32 v[154:155], v[42:43], v[154:155], s[10:11] op_sel_hi:[1,1,0]
	v_pk_fma_f32 v[148:149], v[38:39], v[148:149], s[12:13] op_sel_hi:[1,1,0]
	v_pk_mul_f32 v[36:37], v[36:37], v[46:47]
	v_rcp_f32_e32 v44, v44
	v_pk_fma_f32 v[152:153], v[40:41], v[152:153], s[10:11] op_sel_hi:[1,1,0]
	v_pk_fma_f32 v[154:155], v[42:43], v[154:155], s[12:13] op_sel_hi:[1,1,0]
	v_pk_mul_f32 v[38:39], v[38:39], v[148:149]
	v_pk_fma_f32 v[20:21], v[20:21], v[36:37], 0.5 op_sel_hi:[1,1,0] neg_lo:[1,0,0] neg_hi:[1,0,0]
	v_rcp_f32_e32 v45, v45
	v_pk_fma_f32 v[152:153], v[40:41], v[152:153], s[12:13] op_sel_hi:[1,1,0]
	v_pk_mul_f32 v[42:43], v[42:43], v[154:155]
	v_pk_fma_f32 v[24:25], v[24:25], v[38:39], 0.5 op_sel_hi:[1,1,0] neg_lo:[1,0,0] neg_hi:[1,0,0]
	v_pk_mul_f32 v[18:19], v[18:19], v[20:21]
	v_pk_mul_f32 v[40:41], v[40:41], v[152:153]
	v_pk_mul_f32 v[20:21], v[22:23], v[24:25]
	v_pk_fma_f32 v[0:1], v[0:1], 0.5, v[18:19] op_sel_hi:[1,0,1]
	v_pk_fma_f32 v[18:19], v[32:33], v[42:43], 0.5 op_sel_hi:[1,1,0] neg_lo:[1,0,0] neg_hi:[1,0,0]
	v_pk_fma_f32 v[28:29], v[28:29], v[40:41], 0.5 op_sel_hi:[1,1,0] neg_lo:[1,0,0] neg_hi:[1,0,0]
	v_pk_fma_f32 v[2:3], v[2:3], 0.5, v[20:21] op_sel_hi:[1,0,1]
	v_pk_mul_f32 v[18:19], v[30:31], v[18:19]
	v_pk_mul_f32 v[20:21], v[8:9], v[8:9]
	v_pk_mul_f32 v[22:23], v[26:27], v[28:29]
	v_pk_fma_f32 v[6:7], v[6:7], 0.5, v[18:19] op_sel_hi:[1,0,1]
	v_pk_fma_f32 v[18:19], v[44:45], s[16:17], v[16:17] op_sel_hi:[1,0,0]
	v_pk_mul_f32 v[20:21], v[20:21], s[14:15] op_sel_hi:[1,0]
	v_pk_mul_f32 v[10:11], v[202:203], v[150:151]
	v_pk_fma_f32 v[4:5], v[4:5], 0.5, v[22:23] op_sel_hi:[1,0,1]
	v_pk_fma_f32 v[18:19], v[44:45], v[18:19], s[18:19] op_sel_hi:[1,1,0]
	v_exp_f32_e32 v20, v20
	v_exp_f32_e32 v21, v21
	v_and_b32_e32 v23, 0x7fffffff, v11
	v_and_b32_e32 v22, 0x7fffffff, v10
	v_pk_fma_f32 v[18:19], v[44:45], v[18:19], s[10:11] op_sel_hi:[1,1,0]
	v_pk_fma_f32 v[24:25], v[22:23], s[20:21], 1.0 op_sel_hi:[1,0,0]
	v_pk_fma_f32 v[18:19], v[44:45], v[18:19], s[12:13] op_sel_hi:[1,1,0]
	v_rcp_f32_e32 v24, v24
	v_rcp_f32_e32 v25, v25
	v_pk_mul_f32 v[18:19], v[44:45], v[18:19]
	v_pk_mul_f32 v[12:13], v[204:205], v[144:145]
	v_pk_fma_f32 v[18:19], v[20:21], v[18:19], 0.5 op_sel_hi:[1,1,0] neg_lo:[1,0,0] neg_hi:[1,0,0]
	v_pk_mul_f32 v[20:21], v[10:11], v[10:11]
	v_pk_mul_f32 v[18:19], v[34:35], v[18:19]
	v_pk_mul_f32 v[20:21], v[20:21], s[14:15] op_sel_hi:[1,0]
	v_pk_fma_f32 v[8:9], v[8:9], 0.5, v[18:19] op_sel_hi:[1,0,1]
	v_pk_fma_f32 v[18:19], v[24:25], s[16:17], v[16:17] op_sel_hi:[1,0,0]
	v_exp_f32_e32 v20, v20
	v_pk_fma_f32 v[18:19], v[24:25], v[18:19], s[18:19] op_sel_hi:[1,1,0]
	v_exp_f32_e32 v21, v21
	v_pk_fma_f32 v[18:19], v[24:25], v[18:19], s[10:11] op_sel_hi:[1,1,0]
	v_pk_mul_f32 v[14:15], v[206:207], v[146:147]
	v_pk_fma_f32 v[18:19], v[24:25], v[18:19], s[12:13] op_sel_hi:[1,1,0]
	v_mov_b32_e32 v147, v161
	v_pk_mul_f32 v[18:19], v[24:25], v[18:19]
	v_and_b32_e32 v25, 0x7fffffff, v13
	v_and_b32_e32 v24, 0x7fffffff, v12
	v_pk_fma_f32 v[26:27], v[24:25], s[20:21], 1.0 op_sel_hi:[1,0,0]
	v_pk_fma_f32 v[18:19], v[20:21], v[18:19], 0.5 op_sel_hi:[1,1,0] neg_lo:[1,0,0] neg_hi:[1,0,0]
	v_rcp_f32_e32 v26, v26
	v_rcp_f32_e32 v27, v27
	v_pk_mul_f32 v[18:19], v[22:23], v[18:19]
	v_pk_mul_f32 v[20:21], v[12:13], v[12:13]
	v_pk_fma_f32 v[10:11], v[10:11], 0.5, v[18:19] op_sel_hi:[1,0,1]
	v_pk_fma_f32 v[18:19], v[26:27], s[16:17], v[16:17] op_sel_hi:[1,0,0]
	v_pk_mul_f32 v[20:21], v[20:21], s[14:15] op_sel_hi:[1,0]
	v_pk_fma_f32 v[18:19], v[26:27], v[18:19], s[18:19] op_sel_hi:[1,1,0]
	v_exp_f32_e32 v20, v20
	v_pk_fma_f32 v[18:19], v[26:27], v[18:19], s[10:11] op_sel_hi:[1,1,0]
	v_exp_f32_e32 v21, v21
	v_pk_fma_f32 v[18:19], v[26:27], v[18:19], s[12:13] op_sel_hi:[1,1,0]
	v_and_b32_e32 v23, 0x7fffffff, v15
	v_and_b32_e32 v22, 0x7fffffff, v14
	v_pk_mul_f32 v[18:19], v[26:27], v[18:19]
	v_pk_fma_f32 v[26:27], v[22:23], s[20:21], 1.0 op_sel_hi:[1,0,0]
	v_pk_fma_f32 v[18:19], v[20:21], v[18:19], 0.5 op_sel_hi:[1,1,0] neg_lo:[1,0,0] neg_hi:[1,0,0]
	v_rcp_f32_e32 v26, v26
	v_rcp_f32_e32 v27, v27
	v_pk_mul_f32 v[18:19], v[24:25], v[18:19]
	v_pk_fma_f32 v[16:17], v[26:27], s[16:17], v[16:17] op_sel_hi:[1,0,0]
	v_pk_fma_f32 v[12:13], v[12:13], 0.5, v[18:19] op_sel_hi:[1,0,1]
	v_pk_mul_f32 v[18:19], v[14:15], v[14:15]
	v_pk_fma_f32 v[16:17], v[26:27], v[16:17], s[18:19] op_sel_hi:[1,1,0]
	v_pk_mul_f32 v[18:19], v[18:19], s[14:15] op_sel_hi:[1,0]
	v_pk_fma_f32 v[16:17], v[26:27], v[16:17], s[10:11] op_sel_hi:[1,1,0]
	v_exp_f32_e32 v18, v18
	v_exp_f32_e32 v19, v19
	v_pk_fma_f32 v[16:17], v[26:27], v[16:17], s[12:13] op_sel_hi:[1,1,0]
	s_nop 0
	v_pk_mul_f32 v[16:17], v[26:27], v[16:17]
	s_nop 0
	v_pk_fma_f32 v[16:17], v[18:19], v[16:17], 0.5 op_sel_hi:[1,1,0] neg_lo:[1,0,0] neg_hi:[1,0,0]
	v_max_f32_e64 v18, |v6|, |v7|
	v_pk_mul_f32 v[16:17], v[22:23], v[16:17]
	s_nop 0
	v_pk_fma_f32 v[14:15], v[14:15], 0.5, v[16:17] op_sel_hi:[1,0,1]
	v_max_f32_e64 v16, |v0|, |v1|
	v_max_f32_e64 v17, |v2|, |v3|
	v_max3_f32 v16, v16, 0, v17
	v_max_f32_e64 v17, |v4|, |v5|
	v_max3_f32 v16, v16, v17, v18
	v_max_f32_e64 v17, |v8|, |v9|
	v_max_f32_e64 v18, |v10|, |v11|
	v_max3_f32 v16, v16, v17, v18
	v_max_f32_e64 v17, |v12|, |v13|
	v_max_f32_e64 v18, |v14|, |v15|
	v_max3_f32 v16, v16, v17, v18
	v_mov_b32_e32 v17, v16
	s_nop 1
	v_permlane16_swap_b32_e32 v16, v17
	v_max_f32_e32 v17, v17, v17
	v_max_f32_e32 v16, v16, v16
	v_max_f32_e32 v16, v16, v17
	v_lshrrev_b32_e32 v17, 23, v16
	v_and_b32_e32 v16, 0x7fffff, v16
	v_cmp_lt_u32_e32 vcc, s9, v16
	s_nop 1
	v_addc_co_u32_e32 v16, vcc, v17, v182, vcc
	v_med3_i32 v145, v16, s13, v183
	v_lshlrev_b32_e32 v16, 23, v145
	v_sub_u32_e32 v16, 1.0, v16
	v_pk_mul_f32 v[40:41], v[16:17], v[8:9] op_sel_hi:[0,1]
	v_pk_mul_f32 v[42:43], v[16:17], v[10:11] op_sel_hi:[0,1]
	v_pk_mul_f32 v[44:45], v[16:17], v[12:13] op_sel_hi:[0,1]
	v_pk_mul_f32 v[46:47], v[16:17], v[14:15] op_sel_hi:[0,1]
	v_pk_mul_f32 v[32:33], v[16:17], v[0:1] op_sel_hi:[0,1]
	v_pk_mul_f32 v[34:35], v[16:17], v[2:3] op_sel_hi:[0,1]
	v_pk_mul_f32 v[36:37], v[16:17], v[4:5] op_sel_hi:[0,1]
	v_pk_mul_f32 v[38:39], v[16:17], v[6:7] op_sel_hi:[0,1]
	v_mov_b32_e32 v0, v40
	v_mov_b32_e32 v1, v41
	v_mov_b32_e32 v2, v42
	v_mov_b32_e32 v3, v43
	v_mov_b32_e32 v4, v44
	v_mov_b32_e32 v5, v45
	v_mov_b32_e32 v6, v46
	v_mov_b32_e32 v7, v47
	v_cvt_scalef32_2xpk16_fp6_f32 v[148:153], v[32:47], v[0:15], 1.0
	v_cvt_scalef32_pk32_f32_fp6 v[0:31], v[148:153], s15
	v_mov_b32_e32 v16, v0
	v_mov_b32_e32 v17, v2
	v_mov_b32_e32 v2, v1
	v_mov_b32_e32 v0, v4
	v_mov_b32_e32 v1, v6
	v_pk_fma_f32 v[18:19], v[34:35], s[8:9], v[0:1] op_sel_hi:[1,0,1]
	v_mov_b32_e32 v0, v8
	v_mov_b32_e32 v1, v10
	v_mov_b32_e32 v6, v5
	v_pk_fma_f32 v[20:21], v[36:37], s[8:9], v[0:1] op_sel_hi:[1,0,1]
	v_mov_b32_e32 v10, v9
	v_mov_b32_e32 v1, v14
	v_mov_b32_e32 v14, v13
	v_pk_fma_f32 v[24:25], v[40:41], s[8:9], v[2:3] op_sel_hi:[1,0,1]
	v_pk_fma_f32 v[26:27], v[42:43], s[8:9], v[6:7] op_sel_hi:[1,0,1]
	v_pk_fma_f32 v[28:29], v[44:45], s[8:9], v[10:11] op_sel_hi:[1,0,1]
	v_mov_b32_e32 v0, v12
	v_pk_fma_f32 v[30:31], v[46:47], s[8:9], v[14:15] op_sel_hi:[1,0,1]
	v_pk_fma_f32 v[16:17], v[32:33], s[8:9], v[16:17] op_sel_hi:[1,0,1]
	v_pk_fma_f32 v[22:23], v[38:39], s[8:9], v[0:1] op_sel_hi:[1,0,1]
	v_mov_b32_e32 v0, v24
	v_mov_b32_e32 v1, v25
	v_mov_b32_e32 v2, v26
	v_mov_b32_e32 v3, v27
	v_mov_b32_e32 v4, v28
	v_mov_b32_e32 v5, v29
	v_mov_b32_e32 v6, v30
	v_mov_b32_e32 v7, v31
	v_cvt_scalef32_2xpk16_fp6_f32 v[0:5], v[16:31], v[0:15], 1.0
	v_or_b32_e32 v3, 16, v181
	v_or_b32_e32 v4, v3, v180
	v_mul_u32_u24_e32 v146, 24, v4
	v_lshl_add_u64 v[4:5], v[168:169], 0, v[146:147]
	v_lshl_add_u64 v[4:5], v[4:5], 0, v[160:161]
	global_store_dwordx3 v[4:5], v[148:150], off nt
	v_add_co_u32_e32 v4, vcc, 0x1000, v4
	v_xor_b32_e32 v0, 0x20820820, v0
	v_xor_b32_e32 v1, 0x8208208, v1
	v_xor_b32_e32 v2, 0x82082082, v2
	v_addc_co_u32_e32 v5, vcc, 0, v5, vcc
	v_lshl_or_b32 v144, v3, 1, v180
	global_store_dwordx3 v[4:5], v[0:2], off offset:2048 nt
	s_and_saveexec_b64 s[8:9], s[0:1]
	s_cbranch_execz .LBB3_10
	v_mov_b32_e32 v1, 0x7a00
	v_add_u32_e32 v0, 0x7f, v145
	v_lshl_add_u32 v1, v145, 8, v1
	v_mov_b32_e32 v145, 0
	v_or_b32_e32 v2, v1, v0
	v_lshl_add_u64 v[0:1], v[166:167], 0, v[144:145]
	global_store_short v[0:1], v2, off
.LBB3_10:
	s_or_b64 exec, exec, s[8:9]
	v_permlane32_swap_b32_e32 v140, v132
	v_permlane32_swap_b32_e32 v141, v133
	v_permlane32_swap_b32_e32 v142, v134
	v_permlane32_swap_b32_e32 v143, v135
	v_permlane32_swap_b32_e32 v136, v128
	v_permlane32_swap_b32_e32 v137, v129
	s_mov_b32 s18, 0x3e6d3388
	v_permlane32_swap_b32_e32 v138, v130
	v_permlane32_swap_b32_e32 v139, v131
	s_mov_b32 s14, 0x3f07dc22
	s_mov_b32 s12, 0xbf38aa3b
	v_mov_b64_e32 v[16:17], s[22:23]
	s_mov_b32 s16, 0x3f35f0e3
	s_mov_b32 s8, 0xbe11a98e
	s_mov_b32 s10, 0x3e027906
	s_mov_b32 s20, 0xc2000000
	v_pk_mul_f32 v[0:1], v[192:193], v[140:141]
	v_pk_mul_f32 v[2:3], v[194:195], v[142:143]
	v_pk_mul_f32 v[4:5], v[196:197], v[136:137]
	v_and_b32_e32 v19, 0x7fffffff, v1
	v_and_b32_e32 v18, 0x7fffffff, v0
	v_and_b32_e32 v23, 0x7fffffff, v3
	v_and_b32_e32 v22, 0x7fffffff, v2
	v_and_b32_e32 v27, 0x7fffffff, v5
	v_and_b32_e32 v26, 0x7fffffff, v4
	v_pk_fma_f32 v[34:35], v[18:19], s[18:19], 1.0 op_sel_hi:[1,0,0]
	v_pk_fma_f32 v[36:37], v[22:23], s[18:19], 1.0 op_sel_hi:[1,0,0]
	v_pk_fma_f32 v[38:39], v[26:27], s[18:19], 1.0 op_sel_hi:[1,0,0]
	v_rcp_f32_e32 v34, v34
	v_rcp_f32_e32 v35, v35
	v_rcp_f32_e32 v36, v36
	v_rcp_f32_e32 v37, v37
	v_rcp_f32_e32 v38, v38
	v_rcp_f32_e32 v39, v39
	v_pk_mul_f32 v[6:7], v[198:199], v[138:139]
	v_pk_mul_f32 v[20:21], v[0:1], v[0:1]
	v_pk_mul_f32 v[24:25], v[2:3], v[2:3]
	v_pk_mul_f32 v[28:29], v[4:5], v[4:5]
	v_and_b32_e32 v31, 0x7fffffff, v7
	v_and_b32_e32 v30, 0x7fffffff, v6
	v_pk_mul_f32 v[20:21], v[20:21], s[12:13] op_sel_hi:[1,0]
	v_pk_mul_f32 v[24:25], v[24:25], s[12:13] op_sel_hi:[1,0]
	v_pk_fma_f32 v[42:43], v[34:35], s[14:15], v[16:17] op_sel_hi:[1,0,0]
	v_pk_fma_f32 v[44:45], v[36:37], s[14:15], v[16:17] op_sel_hi:[1,0,0]
	v_pk_mul_f32 v[28:29], v[28:29], s[12:13] op_sel_hi:[1,0]
	v_pk_fma_f32 v[40:41], v[30:31], s[18:19], 1.0 op_sel_hi:[1,0,0]
	v_exp_f32_e32 v20, v20
	v_exp_f32_e32 v21, v21
	v_exp_f32_e32 v24, v24
	v_exp_f32_e32 v25, v25
	v_pk_fma_f32 v[46:47], v[38:39], s[14:15], v[16:17] op_sel_hi:[1,0,0]
	v_pk_fma_f32 v[42:43], v[34:35], v[42:43], s[16:17] op_sel_hi:[1,1,0]
	v_pk_fma_f32 v[44:45], v[36:37], v[44:45], s[16:17] op_sel_hi:[1,1,0]
	v_exp_f32_e32 v28, v28
	v_exp_f32_e32 v29, v29
	v_rcp_f32_e32 v40, v40
	v_rcp_f32_e32 v41, v41
	v_pk_fma_f32 v[46:47], v[38:39], v[46:47], s[16:17] op_sel_hi:[1,1,0]
	v_pk_fma_f32 v[42:43], v[34:35], v[42:43], s[8:9] op_sel_hi:[1,1,0]
	v_pk_fma_f32 v[44:45], v[36:37], v[44:45], s[8:9] op_sel_hi:[1,1,0]
	v_pk_fma_f32 v[46:47], v[38:39], v[46:47], s[8:9] op_sel_hi:[1,1,0]
	v_pk_fma_f32 v[42:43], v[34:35], v[42:43], s[10:11] op_sel_hi:[1,1,0]
	v_pk_fma_f32 v[44:45], v[36:37], v[44:45], s[10:11] op_sel_hi:[1,1,0]
	v_pk_fma_f32 v[46:47], v[38:39], v[46:47], s[10:11] op_sel_hi:[1,1,0]
	v_pk_mul_f32 v[34:35], v[34:35], v[42:43]
	v_pk_mul_f32 v[36:37], v[36:37], v[44:45]
	v_pk_mul_f32 v[32:33], v[6:7], v[6:7]
	v_pk_mul_f32 v[38:39], v[38:39], v[46:47]
	v_pk_fma_f32 v[20:21], v[20:21], v[34:35], 0.5 op_sel_hi:[1,1,0] neg_lo:[1,0,0] neg_hi:[1,0,0]
	v_pk_fma_f32 v[24:25], v[24:25], v[36:37], 0.5 op_sel_hi:[1,1,0] neg_lo:[1,0,0] neg_hi:[1,0,0]
	v_pk_mul_f32 v[32:33], v[32:33], s[12:13] op_sel_hi:[1,0]
	v_pk_fma_f32 v[136:137], v[40:41], s[14:15], v[16:17] op_sel_hi:[1,0,0]
	v_pk_fma_f32 v[28:29], v[28:29], v[38:39], 0.5 op_sel_hi:[1,1,0] neg_lo:[1,0,0] neg_hi:[1,0,0]
	v_pk_mul_f32 v[18:19], v[18:19], v[20:21]
	v_pk_mul_f32 v[20:21], v[22:23], v[24:25]
	v_pk_mul_f32 v[8:9], v[200:201], v[132:133]
	v_pk_fma_f32 v[136:137], v[40:41], v[136:137], s[16:17] op_sel_hi:[1,1,0]
	v_pk_mul_f32 v[22:23], v[26:27], v[28:29]
	v_pk_fma_f32 v[0:1], v[0:1], 0.5, v[18:19] op_sel_hi:[1,0,1]
	v_pk_fma_f32 v[2:3], v[2:3], 0.5, v[20:21] op_sel_hi:[1,0,1]
	v_exp_f32_e32 v18, v32
	v_exp_f32_e32 v19, v33
	v_and_b32_e32 v21, 0x7fffffff, v9
	v_and_b32_e32 v20, 0x7fffffff, v8
	v_pk_fma_f32 v[136:137], v[40:41], v[136:137], s[8:9] op_sel_hi:[1,1,0]
	v_pk_fma_f32 v[4:5], v[4:5], 0.5, v[22:23] op_sel_hi:[1,0,1]
	v_pk_fma_f32 v[22:23], v[20:21], s[18:19], 1.0 op_sel_hi:[1,0,0]
	v_pk_fma_f32 v[136:137], v[40:41], v[136:137], s[10:11] op_sel_hi:[1,1,0]
	v_rcp_f32_e32 v22, v22
	v_rcp_f32_e32 v23, v23
	v_pk_mul_f32 v[40:41], v[40:41], v[136:137]
	v_pk_mul_f32 v[10:11], v[202:203], v[134:135]
	v_pk_fma_f32 v[18:19], v[18:19], v[40:41], 0.5 op_sel_hi:[1,1,0] neg_lo:[1,0,0] neg_hi:[1,0,0]
	v_and_b32_e32 v25, 0x7fffffff, v11
	v_pk_mul_f32 v[18:19], v[30:31], v[18:19]
	v_and_b32_e32 v24, 0x7fffffff, v10
	v_pk_fma_f32 v[6:7], v[6:7], 0.5, v[18:19] op_sel_hi:[1,0,1]
	v_pk_fma_f32 v[18:19], v[22:23], s[14:15], v[16:17] op_sel_hi:[1,0,0]
	v_pk_fma_f32 v[26:27], v[24:25], s[18:19], 1.0 op_sel_hi:[1,0,0]
	v_pk_fma_f32 v[18:19], v[22:23], v[18:19], s[16:17] op_sel_hi:[1,1,0]
	v_rcp_f32_e32 v26, v26
	v_pk_fma_f32 v[18:19], v[22:23], v[18:19], s[8:9] op_sel_hi:[1,1,0]
	v_rcp_f32_e32 v27, v27
	v_pk_fma_f32 v[18:19], v[22:23], v[18:19], s[10:11] op_sel_hi:[1,1,0]
	v_pk_mul_f32 v[12:13], v[204:205], v[128:129]
	v_pk_mul_f32 v[18:19], v[22:23], v[18:19]
	v_pk_mul_f32 v[22:23], v[8:9], v[8:9]
	v_pk_mul_f32 v[14:15], v[206:207], v[130:131]
	v_pk_mul_f32 v[22:23], v[22:23], s[12:13] op_sel_hi:[1,0]
	v_mov_b32_e32 v132, 0xffffff7f
	v_exp_f32_e32 v22, v22
	v_exp_f32_e32 v23, v23
	v_mov_b32_e32 v133, 0x64
	v_mov_b32_e32 v131, 0
	v_pk_fma_f32 v[18:19], v[22:23], v[18:19], 0.5 op_sel_hi:[1,1,0] neg_lo:[1,0,0] neg_hi:[1,0,0]
	s_nop 0
	v_pk_mul_f32 v[18:19], v[20:21], v[18:19]
	v_pk_mul_f32 v[20:21], v[10:11], v[10:11]
	v_pk_fma_f32 v[8:9], v[8:9], 0.5, v[18:19] op_sel_hi:[1,0,1]
	v_pk_fma_f32 v[18:19], v[26:27], s[14:15], v[16:17] op_sel_hi:[1,0,0]
	v_pk_mul_f32 v[20:21], v[20:21], s[12:13] op_sel_hi:[1,0]
	v_pk_fma_f32 v[18:19], v[26:27], v[18:19], s[16:17] op_sel_hi:[1,1,0]
	v_exp_f32_e32 v20, v20
	v_pk_fma_f32 v[18:19], v[26:27], v[18:19], s[8:9] op_sel_hi:[1,1,0]
	v_exp_f32_e32 v21, v21
	v_pk_fma_f32 v[18:19], v[26:27], v[18:19], s[10:11] op_sel_hi:[1,1,0]
	v_and_b32_e32 v23, 0x7fffffff, v13
	v_and_b32_e32 v22, 0x7fffffff, v12
	v_pk_mul_f32 v[18:19], v[26:27], v[18:19]
	v_pk_fma_f32 v[26:27], v[22:23], s[18:19], 1.0 op_sel_hi:[1,0,0]
	v_pk_fma_f32 v[18:19], v[20:21], v[18:19], 0.5 op_sel_hi:[1,1,0] neg_lo:[1,0,0] neg_hi:[1,0,0]
	v_rcp_f32_e32 v26, v26
	v_rcp_f32_e32 v27, v27
	v_pk_mul_f32 v[18:19], v[24:25], v[18:19]
	v_pk_mul_f32 v[20:21], v[12:13], v[12:13]
	v_pk_fma_f32 v[10:11], v[10:11], 0.5, v[18:19] op_sel_hi:[1,0,1]
	v_pk_fma_f32 v[18:19], v[26:27], s[14:15], v[16:17] op_sel_hi:[1,0,0]
	v_pk_mul_f32 v[20:21], v[20:21], s[12:13] op_sel_hi:[1,0]
	v_pk_fma_f32 v[18:19], v[26:27], v[18:19], s[16:17] op_sel_hi:[1,1,0]
	v_exp_f32_e32 v20, v20
	v_pk_fma_f32 v[18:19], v[26:27], v[18:19], s[8:9] op_sel_hi:[1,1,0]
	v_exp_f32_e32 v21, v21
	v_pk_fma_f32 v[18:19], v[26:27], v[18:19], s[10:11] op_sel_hi:[1,1,0]
	v_and_b32_e32 v25, 0x7fffffff, v15
	v_and_b32_e32 v24, 0x7fffffff, v14
	v_pk_mul_f32 v[18:19], v[26:27], v[18:19]
	v_pk_fma_f32 v[26:27], v[24:25], s[18:19], 1.0 op_sel_hi:[1,0,0]
	v_pk_fma_f32 v[18:19], v[20:21], v[18:19], 0.5 op_sel_hi:[1,1,0] neg_lo:[1,0,0] neg_hi:[1,0,0]
	v_rcp_f32_e32 v26, v26
	v_rcp_f32_e32 v27, v27
	v_pk_mul_f32 v[18:19], v[22:23], v[18:19]
	v_pk_fma_f32 v[16:17], v[26:27], s[14:15], v[16:17] op_sel_hi:[1,0,0]
	v_pk_fma_f32 v[12:13], v[12:13], 0.5, v[18:19] op_sel_hi:[1,0,1]
	v_pk_mul_f32 v[18:19], v[14:15], v[14:15]
	v_pk_fma_f32 v[16:17], v[26:27], v[16:17], s[16:17] op_sel_hi:[1,1,0]
	v_pk_mul_f32 v[18:19], v[18:19], s[12:13] op_sel_hi:[1,0]
	v_pk_fma_f32 v[16:17], v[26:27], v[16:17], s[8:9] op_sel_hi:[1,1,0]
	v_exp_f32_e32 v18, v18
	v_exp_f32_e32 v19, v19
	v_pk_fma_f32 v[16:17], v[26:27], v[16:17], s[10:11] op_sel_hi:[1,1,0]
	s_mov_b32 s9, 0x700000
	v_pk_mul_f32 v[16:17], v[26:27], v[16:17]
	s_nop 0
	v_pk_fma_f32 v[16:17], v[18:19], v[16:17], 0.5 op_sel_hi:[1,1,0] neg_lo:[1,0,0] neg_hi:[1,0,0]
	v_max_f32_e64 v18, |v6|, |v7|
	v_pk_mul_f32 v[16:17], v[24:25], v[16:17]
	s_nop 0
	v_pk_fma_f32 v[14:15], v[14:15], 0.5, v[16:17] op_sel_hi:[1,0,1]
	v_max_f32_e64 v16, |v0|, |v1|
	v_max_f32_e64 v17, |v2|, |v3|
	v_max3_f32 v16, v16, 0, v17
	v_max_f32_e64 v17, |v4|, |v5|
	v_max3_f32 v16, v16, v17, v18
	v_max_f32_e64 v17, |v8|, |v9|
	v_max_f32_e64 v18, |v10|, |v11|
	v_max3_f32 v16, v16, v17, v18
	v_max_f32_e64 v17, |v12|, |v13|
	v_max_f32_e64 v18, |v14|, |v15|
	v_max3_f32 v16, v16, v17, v18
	v_mov_b32_e32 v17, v16
	s_nop 1
	v_permlane16_swap_b32_e32 v16, v17
	v_max_f32_e32 v17, v17, v17
	v_max_f32_e32 v16, v16, v16
	v_max_f32_e32 v16, v16, v17
	v_lshrrev_b32_e32 v17, 23, v16
	v_and_b32_e32 v16, 0x7fffff, v16
	v_cmp_lt_u32_e32 vcc, s9, v16
	s_nop 1
	v_addc_co_u32_e32 v16, vcc, v17, v132, vcc
	v_med3_i32 v129, v16, s13, v133
	v_lshlrev_b32_e32 v16, 23, v129
	v_sub_u32_e32 v16, 1.0, v16
	v_pk_mul_f32 v[40:41], v[16:17], v[8:9] op_sel_hi:[0,1]
	v_pk_mul_f32 v[42:43], v[16:17], v[10:11] op_sel_hi:[0,1]
	v_pk_mul_f32 v[44:45], v[16:17], v[12:13] op_sel_hi:[0,1]
	v_pk_mul_f32 v[46:47], v[16:17], v[14:15] op_sel_hi:[0,1]
	v_pk_mul_f32 v[32:33], v[16:17], v[0:1] op_sel_hi:[0,1]
	v_pk_mul_f32 v[34:35], v[16:17], v[2:3] op_sel_hi:[0,1]
	v_pk_mul_f32 v[36:37], v[16:17], v[4:5] op_sel_hi:[0,1]
	v_pk_mul_f32 v[38:39], v[16:17], v[6:7] op_sel_hi:[0,1]
	v_mov_b32_e32 v0, v40
	v_mov_b32_e32 v1, v41
	v_mov_b32_e32 v2, v42
	v_mov_b32_e32 v3, v43
	v_mov_b32_e32 v4, v44
	v_mov_b32_e32 v5, v45
	v_mov_b32_e32 v6, v46
	v_mov_b32_e32 v7, v47
	v_cvt_scalef32_2xpk16_fp6_f32 v[134:139], v[32:47], v[0:15], 1.0
	v_cvt_scalef32_pk32_f32_fp6 v[0:31], v[134:139], s15
	v_mov_b32_e32 v16, v0
	v_mov_b32_e32 v17, v2
	v_mov_b32_e32 v2, v1
	v_mov_b32_e32 v0, v4
	v_mov_b32_e32 v1, v6
	v_pk_fma_f32 v[18:19], v[34:35], s[20:21], v[0:1] op_sel_hi:[1,0,1]
	v_mov_b32_e32 v0, v8
	v_mov_b32_e32 v1, v10
	v_mov_b32_e32 v6, v5
	v_pk_fma_f32 v[20:21], v[36:37], s[20:21], v[0:1] op_sel_hi:[1,0,1]
	v_mov_b32_e32 v10, v9
	v_mov_b32_e32 v1, v14
	v_mov_b32_e32 v14, v13
	v_pk_fma_f32 v[24:25], v[40:41], s[20:21], v[2:3] op_sel_hi:[1,0,1]
	v_pk_fma_f32 v[26:27], v[42:43], s[20:21], v[6:7] op_sel_hi:[1,0,1]
	v_pk_fma_f32 v[28:29], v[44:45], s[20:21], v[10:11] op_sel_hi:[1,0,1]
	v_mov_b32_e32 v0, v12
	v_pk_fma_f32 v[30:31], v[46:47], s[20:21], v[14:15] op_sel_hi:[1,0,1]
	v_pk_fma_f32 v[16:17], v[32:33], s[20:21], v[16:17] op_sel_hi:[1,0,1]
	v_pk_fma_f32 v[22:23], v[38:39], s[20:21], v[0:1] op_sel_hi:[1,0,1]
	v_mov_b32_e32 v0, v24
	v_mov_b32_e32 v1, v25
	v_mov_b32_e32 v2, v26
	v_mov_b32_e32 v3, v27
	v_mov_b32_e32 v4, v28
	v_mov_b32_e32 v5, v29
	v_mov_b32_e32 v6, v30
	v_mov_b32_e32 v7, v31
	v_cvt_scalef32_2xpk16_fp6_f32 v[0:5], v[16:31], v[0:15], 1.0
	v_or_b32_e32 v3, 32, v181
	v_or_b32_e32 v4, v3, v180
	v_mul_u32_u24_e32 v130, 24, v4
	v_lshl_add_u64 v[4:5], v[168:169], 0, v[130:131]
	v_lshl_add_u64 v[4:5], v[4:5], 0, v[160:161]
	global_store_dwordx3 v[4:5], v[134:136], off nt
	v_add_co_u32_e32 v4, vcc, 0x1000, v4
	v_xor_b32_e32 v0, 0x20820820, v0
	v_xor_b32_e32 v1, 0x8208208, v1
	v_xor_b32_e32 v2, 0x82082082, v2
	v_addc_co_u32_e32 v5, vcc, 0, v5, vcc
	v_lshl_or_b32 v128, v3, 1, v180
	global_store_dwordx3 v[4:5], v[0:2], off offset:2048 nt
	s_and_saveexec_b64 s[24:25], s[0:1]
	s_cbranch_execz .LBB3_12
	v_mov_b32_e32 v1, 0x7a00
	v_add_u32_e32 v0, 0x7f, v129
	v_lshl_add_u32 v1, v129, 8, v1
	v_mov_b32_e32 v129, v131
	v_or_b32_e32 v2, v1, v0
	v_lshl_add_u64 v[0:1], v[166:167], 0, v[128:129]
	global_store_short v[0:1], v2, off
.LBB3_12:
	s_or_b64 exec, exec, s[24:25]
	v_permlane32_swap_b32_e32 v124, v116
	v_permlane32_swap_b32_e32 v125, v117
	v_permlane32_swap_b32_e32 v126, v118
	v_permlane32_swap_b32_e32 v127, v119
	v_permlane32_swap_b32_e32 v122, v114
	v_permlane32_swap_b32_e32 v123, v115
	v_permlane32_swap_b32_e32 v120, v112
	v_permlane32_swap_b32_e32 v121, v113
	v_mov_b64_e32 v[16:17], s[22:23]
	v_pk_mul_f32 v[0:1], v[192:193], v[124:125]
	v_pk_mul_f32 v[2:3], v[194:195], v[126:127]
	v_and_b32_e32 v19, 0x7fffffff, v1
	v_and_b32_e32 v18, 0x7fffffff, v0
	v_pk_mul_f32 v[6:7], v[198:199], v[122:123]
	v_and_b32_e32 v23, 0x7fffffff, v3
	v_and_b32_e32 v22, 0x7fffffff, v2
	v_pk_fma_f32 v[36:37], v[18:19], s[18:19], 1.0 op_sel_hi:[1,0,0]
	v_pk_mul_f32 v[4:5], v[196:197], v[120:121]
	v_and_b32_e32 v31, 0x7fffffff, v7
	v_and_b32_e32 v30, 0x7fffffff, v6
	v_pk_fma_f32 v[38:39], v[22:23], s[18:19], 1.0 op_sel_hi:[1,0,0]
	v_rcp_f32_e32 v36, v36
	v_rcp_f32_e32 v37, v37
	v_and_b32_e32 v27, 0x7fffffff, v5
	v_and_b32_e32 v26, 0x7fffffff, v4
	v_pk_fma_f32 v[42:43], v[30:31], s[18:19], 1.0 op_sel_hi:[1,0,0]
	v_rcp_f32_e32 v38, v38
	v_rcp_f32_e32 v39, v39
	v_pk_fma_f32 v[40:41], v[26:27], s[18:19], 1.0 op_sel_hi:[1,0,0]
	v_rcp_f32_e32 v42, v42
	v_rcp_f32_e32 v43, v43
	v_pk_mul_f32 v[20:21], v[0:1], v[0:1]
	v_rcp_f32_e32 v40, v40
	v_rcp_f32_e32 v41, v41
	v_pk_mul_f32 v[24:25], v[2:3], v[2:3]
	v_pk_mul_f32 v[20:21], v[20:21], s[12:13] op_sel_hi:[1,0]
	v_pk_fma_f32 v[46:47], v[36:37], s[14:15], v[16:17] op_sel_hi:[1,0,0]
	v_pk_mul_f32 v[8:9], v[200:201], v[116:117]
	v_pk_mul_f32 v[32:33], v[6:7], v[6:7]
	v_pk_mul_f32 v[24:25], v[24:25], s[12:13] op_sel_hi:[1,0]
	v_exp_f32_e32 v20, v20
	v_exp_f32_e32 v21, v21
	v_pk_fma_f32 v[116:117], v[38:39], s[14:15], v[16:17] op_sel_hi:[1,0,0]
	v_pk_fma_f32 v[46:47], v[36:37], v[46:47], s[16:17] op_sel_hi:[1,1,0]
	v_pk_mul_f32 v[28:29], v[4:5], v[4:5]
	v_pk_mul_f32 v[32:33], v[32:33], s[12:13] op_sel_hi:[1,0]
	v_exp_f32_e32 v24, v24
	v_exp_f32_e32 v25, v25
	v_pk_fma_f32 v[122:123], v[42:43], s[14:15], v[16:17] op_sel_hi:[1,0,0]
	v_pk_fma_f32 v[116:117], v[38:39], v[116:117], s[16:17] op_sel_hi:[1,1,0]
	v_pk_fma_f32 v[46:47], v[36:37], v[46:47], s[8:9] op_sel_hi:[1,1,0]
	v_and_b32_e32 v35, 0x7fffffff, v9
	v_and_b32_e32 v34, 0x7fffffff, v8
	v_pk_mul_f32 v[28:29], v[28:29], s[12:13] op_sel_hi:[1,0]
	v_exp_f32_e32 v32, v32
	v_exp_f32_e32 v33, v33
	v_pk_fma_f32 v[120:121], v[40:41], s[14:15], v[16:17] op_sel_hi:[1,0,0]
	v_pk_fma_f32 v[122:123], v[42:43], v[122:123], s[16:17] op_sel_hi:[1,1,0]
	v_pk_fma_f32 v[116:117], v[38:39], v[116:117], s[8:9] op_sel_hi:[1,1,0]
	v_pk_fma_f32 v[46:47], v[36:37], v[46:47], s[10:11] op_sel_hi:[1,1,0]
	v_pk_fma_f32 v[44:45], v[34:35], s[18:19], 1.0 op_sel_hi:[1,0,0]
	v_exp_f32_e32 v28, v28
	v_exp_f32_e32 v29, v29
	v_pk_fma_f32 v[120:121], v[40:41], v[120:121], s[16:17] op_sel_hi:[1,1,0]
	v_pk_fma_f32 v[122:123], v[42:43], v[122:123], s[8:9] op_sel_hi:[1,1,0]
	v_pk_fma_f32 v[116:117], v[38:39], v[116:117], s[10:11] op_sel_hi:[1,1,0]
	v_pk_mul_f32 v[36:37], v[36:37], v[46:47]
	v_rcp_f32_e32 v44, v44
	v_pk_fma_f32 v[120:121], v[40:41], v[120:121], s[8:9] op_sel_hi:[1,1,0]
	v_pk_fma_f32 v[122:123], v[42:43], v[122:123], s[10:11] op_sel_hi:[1,1,0]
	v_pk_mul_f32 v[38:39], v[38:39], v[116:117]
	v_pk_fma_f32 v[20:21], v[20:21], v[36:37], 0.5 op_sel_hi:[1,1,0] neg_lo:[1,0,0] neg_hi:[1,0,0]
	v_rcp_f32_e32 v45, v45
	v_pk_fma_f32 v[120:121], v[40:41], v[120:121], s[10:11] op_sel_hi:[1,1,0]
	v_pk_mul_f32 v[42:43], v[42:43], v[122:123]
	v_pk_fma_f32 v[24:25], v[24:25], v[38:39], 0.5 op_sel_hi:[1,1,0] neg_lo:[1,0,0] neg_hi:[1,0,0]
	v_pk_mul_f32 v[18:19], v[18:19], v[20:21]
	v_pk_mul_f32 v[40:41], v[40:41], v[120:121]
	v_pk_mul_f32 v[20:21], v[22:23], v[24:25]
	v_pk_fma_f32 v[0:1], v[0:1], 0.5, v[18:19] op_sel_hi:[1,0,1]
	v_pk_fma_f32 v[18:19], v[32:33], v[42:43], 0.5 op_sel_hi:[1,1,0] neg_lo:[1,0,0] neg_hi:[1,0,0]
	v_pk_fma_f32 v[28:29], v[28:29], v[40:41], 0.5 op_sel_hi:[1,1,0] neg_lo:[1,0,0] neg_hi:[1,0,0]
	v_pk_fma_f32 v[2:3], v[2:3], 0.5, v[20:21] op_sel_hi:[1,0,1]
	v_pk_mul_f32 v[18:19], v[30:31], v[18:19]
	v_pk_mul_f32 v[20:21], v[8:9], v[8:9]
	v_pk_mul_f32 v[22:23], v[26:27], v[28:29]
	v_pk_fma_f32 v[6:7], v[6:7], 0.5, v[18:19] op_sel_hi:[1,0,1]
	v_pk_fma_f32 v[18:19], v[44:45], s[14:15], v[16:17] op_sel_hi:[1,0,0]
	v_pk_mul_f32 v[20:21], v[20:21], s[12:13] op_sel_hi:[1,0]
	v_pk_mul_f32 v[10:11], v[202:203], v[118:119]
	v_pk_fma_f32 v[4:5], v[4:5], 0.5, v[22:23] op_sel_hi:[1,0,1]
	v_pk_fma_f32 v[18:19], v[44:45], v[18:19], s[16:17] op_sel_hi:[1,1,0]
	v_exp_f32_e32 v20, v20
	v_exp_f32_e32 v21, v21
	v_and_b32_e32 v23, 0x7fffffff, v11
	v_and_b32_e32 v22, 0x7fffffff, v10
	v_pk_fma_f32 v[18:19], v[44:45], v[18:19], s[8:9] op_sel_hi:[1,1,0]
	v_pk_fma_f32 v[24:25], v[22:23], s[18:19], 1.0 op_sel_hi:[1,0,0]
	v_pk_fma_f32 v[18:19], v[44:45], v[18:19], s[10:11] op_sel_hi:[1,1,0]
	v_rcp_f32_e32 v24, v24
	v_rcp_f32_e32 v25, v25
	v_pk_mul_f32 v[18:19], v[44:45], v[18:19]
	v_pk_mul_f32 v[12:13], v[204:205], v[112:113]
	v_pk_fma_f32 v[18:19], v[20:21], v[18:19], 0.5 op_sel_hi:[1,1,0] neg_lo:[1,0,0] neg_hi:[1,0,0]
	v_pk_mul_f32 v[20:21], v[10:11], v[10:11]
	v_pk_mul_f32 v[18:19], v[34:35], v[18:19]
	v_pk_mul_f32 v[20:21], v[20:21], s[12:13] op_sel_hi:[1,0]
	v_pk_fma_f32 v[8:9], v[8:9], 0.5, v[18:19] op_sel_hi:[1,0,1]
	v_pk_fma_f32 v[18:19], v[24:25], s[14:15], v[16:17] op_sel_hi:[1,0,0]
	v_exp_f32_e32 v20, v20
	v_pk_fma_f32 v[18:19], v[24:25], v[18:19], s[16:17] op_sel_hi:[1,1,0]
	v_exp_f32_e32 v21, v21
	v_pk_fma_f32 v[18:19], v[24:25], v[18:19], s[8:9] op_sel_hi:[1,1,0]
	v_pk_mul_f32 v[14:15], v[206:207], v[114:115]
	v_pk_fma_f32 v[18:19], v[24:25], v[18:19], s[10:11] op_sel_hi:[1,1,0]
	v_mov_b32_e32 v115, v131
	v_pk_mul_f32 v[18:19], v[24:25], v[18:19]
	v_and_b32_e32 v25, 0x7fffffff, v13
	v_and_b32_e32 v24, 0x7fffffff, v12
	v_pk_fma_f32 v[26:27], v[24:25], s[18:19], 1.0 op_sel_hi:[1,0,0]
	v_pk_fma_f32 v[18:19], v[20:21], v[18:19], 0.5 op_sel_hi:[1,1,0] neg_lo:[1,0,0] neg_hi:[1,0,0]
	v_rcp_f32_e32 v26, v26
	v_rcp_f32_e32 v27, v27
	v_pk_mul_f32 v[18:19], v[22:23], v[18:19]
	v_pk_mul_f32 v[20:21], v[12:13], v[12:13]
	v_pk_fma_f32 v[10:11], v[10:11], 0.5, v[18:19] op_sel_hi:[1,0,1]
	v_pk_fma_f32 v[18:19], v[26:27], s[14:15], v[16:17] op_sel_hi:[1,0,0]
	v_pk_mul_f32 v[20:21], v[20:21], s[12:13] op_sel_hi:[1,0]
	v_pk_fma_f32 v[18:19], v[26:27], v[18:19], s[16:17] op_sel_hi:[1,1,0]
	v_exp_f32_e32 v20, v20
	v_pk_fma_f32 v[18:19], v[26:27], v[18:19], s[8:9] op_sel_hi:[1,1,0]
	v_exp_f32_e32 v21, v21
	v_pk_fma_f32 v[18:19], v[26:27], v[18:19], s[10:11] op_sel_hi:[1,1,0]
	v_and_b32_e32 v23, 0x7fffffff, v15
	v_and_b32_e32 v22, 0x7fffffff, v14
	v_pk_mul_f32 v[18:19], v[26:27], v[18:19]
	v_pk_fma_f32 v[26:27], v[22:23], s[18:19], 1.0 op_sel_hi:[1,0,0]
	v_pk_fma_f32 v[18:19], v[20:21], v[18:19], 0.5 op_sel_hi:[1,1,0] neg_lo:[1,0,0] neg_hi:[1,0,0]
	v_rcp_f32_e32 v26, v26
	v_rcp_f32_e32 v27, v27
	v_pk_mul_f32 v[18:19], v[24:25], v[18:19]
	v_pk_fma_f32 v[16:17], v[26:27], s[14:15], v[16:17] op_sel_hi:[1,0,0]
	v_pk_fma_f32 v[12:13], v[12:13], 0.5, v[18:19] op_sel_hi:[1,0,1]
	v_pk_mul_f32 v[18:19], v[14:15], v[14:15]
	v_pk_fma_f32 v[16:17], v[26:27], v[16:17], s[16:17] op_sel_hi:[1,1,0]
	v_pk_mul_f32 v[18:19], v[18:19], s[12:13] op_sel_hi:[1,0]
	v_pk_fma_f32 v[16:17], v[26:27], v[16:17], s[8:9] op_sel_hi:[1,1,0]
	v_exp_f32_e32 v18, v18
	v_exp_f32_e32 v19, v19
	v_pk_fma_f32 v[16:17], v[26:27], v[16:17], s[10:11] op_sel_hi:[1,1,0]
	s_nop 0
	v_pk_mul_f32 v[16:17], v[26:27], v[16:17]
	s_nop 0
	v_pk_fma_f32 v[16:17], v[18:19], v[16:17], 0.5 op_sel_hi:[1,1,0] neg_lo:[1,0,0] neg_hi:[1,0,0]
	v_max_f32_e64 v18, |v6|, |v7|
	v_pk_mul_f32 v[16:17], v[22:23], v[16:17]
	s_nop 0
	v_pk_fma_f32 v[14:15], v[14:15], 0.5, v[16:17] op_sel_hi:[1,0,1]
	v_max_f32_e64 v16, |v0|, |v1|
	v_max_f32_e64 v17, |v2|, |v3|
	v_max3_f32 v16, v16, 0, v17
	v_max_f32_e64 v17, |v4|, |v5|
	v_max3_f32 v16, v16, v17, v18
	v_max_f32_e64 v17, |v8|, |v9|
	v_max_f32_e64 v18, |v10|, |v11|
	v_max3_f32 v16, v16, v17, v18
	v_max_f32_e64 v17, |v12|, |v13|
	v_max_f32_e64 v18, |v14|, |v15|
	v_max3_f32 v16, v16, v17, v18
	v_mov_b32_e32 v17, v16
	s_nop 1
	v_permlane16_swap_b32_e32 v16, v17
	v_max_f32_e32 v17, v17, v17
	v_max_f32_e32 v16, v16, v16
	v_max_f32_e32 v16, v16, v17
	v_lshrrev_b32_e32 v17, 23, v16
	v_and_b32_e32 v16, 0x7fffff, v16
	v_cmp_lt_u32_e32 vcc, s9, v16
	s_nop 1
	v_addc_co_u32_e32 v16, vcc, v17, v132, vcc
	v_med3_i32 v113, v16, s13, v133
	v_lshlrev_b32_e32 v16, 23, v113
	v_sub_u32_e32 v16, 1.0, v16
	v_pk_mul_f32 v[40:41], v[16:17], v[8:9] op_sel_hi:[0,1]
	v_pk_mul_f32 v[42:43], v[16:17], v[10:11] op_sel_hi:[0,1]
	v_pk_mul_f32 v[44:45], v[16:17], v[12:13] op_sel_hi:[0,1]
	v_pk_mul_f32 v[46:47], v[16:17], v[14:15] op_sel_hi:[0,1]
	v_pk_mul_f32 v[32:33], v[16:17], v[0:1] op_sel_hi:[0,1]
	v_pk_mul_f32 v[34:35], v[16:17], v[2:3] op_sel_hi:[0,1]
	v_pk_mul_f32 v[36:37], v[16:17], v[4:5] op_sel_hi:[0,1]
	v_pk_mul_f32 v[38:39], v[16:17], v[6:7] op_sel_hi:[0,1]
	v_mov_b32_e32 v0, v40
	v_mov_b32_e32 v1, v41
	v_mov_b32_e32 v2, v42
	v_mov_b32_e32 v3, v43
	v_mov_b32_e32 v4, v44
	v_mov_b32_e32 v5, v45
	v_mov_b32_e32 v6, v46
	v_mov_b32_e32 v7, v47
	v_cvt_scalef32_2xpk16_fp6_f32 v[116:121], v[32:47], v[0:15], 1.0
	v_cvt_scalef32_pk32_f32_fp6 v[0:31], v[116:121], s15
	v_mov_b32_e32 v16, v0
	v_mov_b32_e32 v17, v2
	v_mov_b32_e32 v2, v1
	v_mov_b32_e32 v0, v4
	v_mov_b32_e32 v1, v6
	v_pk_fma_f32 v[18:19], v[34:35], s[20:21], v[0:1] op_sel_hi:[1,0,1]
	v_mov_b32_e32 v0, v8
	v_mov_b32_e32 v1, v10
	v_mov_b32_e32 v6, v5
	v_pk_fma_f32 v[20:21], v[36:37], s[20:21], v[0:1] op_sel_hi:[1,0,1]
	v_mov_b32_e32 v10, v9
	v_mov_b32_e32 v1, v14
	v_mov_b32_e32 v14, v13
	v_pk_fma_f32 v[24:25], v[40:41], s[20:21], v[2:3] op_sel_hi:[1,0,1]
	v_pk_fma_f32 v[26:27], v[42:43], s[20:21], v[6:7] op_sel_hi:[1,0,1]
	v_pk_fma_f32 v[28:29], v[44:45], s[20:21], v[10:11] op_sel_hi:[1,0,1]
	v_mov_b32_e32 v0, v12
	v_pk_fma_f32 v[30:31], v[46:47], s[20:21], v[14:15] op_sel_hi:[1,0,1]
	v_pk_fma_f32 v[16:17], v[32:33], s[20:21], v[16:17] op_sel_hi:[1,0,1]
	v_pk_fma_f32 v[22:23], v[38:39], s[20:21], v[0:1] op_sel_hi:[1,0,1]
	v_mov_b32_e32 v0, v24
	v_mov_b32_e32 v1, v25
	v_mov_b32_e32 v2, v26
	v_mov_b32_e32 v3, v27
	v_mov_b32_e32 v4, v28
	v_mov_b32_e32 v5, v29
	v_mov_b32_e32 v6, v30
	v_mov_b32_e32 v7, v31
	v_cvt_scalef32_2xpk16_fp6_f32 v[0:5], v[16:31], v[0:15], 1.0
	v_or_b32_e32 v3, 48, v181
	v_or_b32_e32 v4, v3, v180
	v_mul_u32_u24_e32 v114, 24, v4
	v_lshl_add_u64 v[4:5], v[168:169], 0, v[114:115]
	v_lshl_add_u64 v[4:5], v[4:5], 0, v[160:161]
	global_store_dwordx3 v[4:5], v[116:118], off nt
	v_add_co_u32_e32 v4, vcc, 0x1000, v4
	v_xor_b32_e32 v0, 0x20820820, v0
	v_xor_b32_e32 v1, 0x8208208, v1
	v_xor_b32_e32 v2, 0x82082082, v2
	v_addc_co_u32_e32 v5, vcc, 0, v5, vcc
	v_lshl_or_b32 v112, v3, 1, v180
	global_store_dwordx3 v[4:5], v[0:2], off offset:2048 nt
	s_and_saveexec_b64 s[8:9], s[0:1]
	s_cbranch_execz .LBB3_14
	v_mov_b32_e32 v1, 0x7a00
	v_add_u32_e32 v0, 0x7f, v113
	v_lshl_add_u32 v1, v113, 8, v1
	v_mov_b32_e32 v113, 0
	v_or_b32_e32 v2, v1, v0
	v_lshl_add_u64 v[0:1], v[166:167], 0, v[112:113]
	global_store_short v[0:1], v2, off
.LBB3_14:
	s_or_b64 exec, exec, s[8:9]
	v_or_b32_e32 v8, 2, v178
	v_or_b32_e32 v0, v8, v177
	v_lshlrev_b32_e32 v20, 5, v0
	v_or_b32_e32 v12, v20, v179
	v_ashrrev_i32_e32 v13, 31, v12
	v_lshl_add_u64 v[120:121], v[12:13], 2, s[4:5]
	v_ashrrev_i32_e32 v13, 31, v20
	v_lshl_add_u64 v[122:123], v[12:13], 2, s[4:5]
	v_ashrrev_i32_e32 v12, 1, v8
	v_add_u32_e32 v18, s11, v12
	s_movk_i32 s9, 0x6000
	v_mov_b64_e32 v[14:15], s[2:3]
	v_ashrrev_i32_e32 v19, 31, v18
	v_or_b32_e32 v12, v20, v176
	v_mad_i64_i32 v[118:119], s[20:21], v18, s9, v[14:15]
	v_lshlrev_b64 v[14:15], 10, v[18:19]
	v_lshl_add_u64 v[124:125], v[12:13], 2, s[4:5]
	v_lshl_add_u64 v[116:117], s[6:7], 0, v[14:15]
	v_permlane32_swap_b32_e32 v108, v100
	v_permlane32_swap_b32_e32 v109, v101
	s_mov_b32 s16, 0x3e6d3388
	v_permlane32_swap_b32_e32 v110, v102
	v_permlane32_swap_b32_e32 v111, v103
	v_permlane32_swap_b32_e32 v104, v96
	v_permlane32_swap_b32_e32 v105, v97
	s_mov_b32 s18, 0xbf3a00e3
	s_mov_b32 s12, 0x3f07dc22
	s_mov_b32 s10, 0xbf38aa3b
	v_mov_b64_e32 v[16:17], s[18:19]
	s_mov_b32 s14, 0x3f35f0e3
	s_mov_b32 s2, 0xbe11a98e
	s_mov_b32 s8, 0x3e027906
	v_permlane32_swap_b32_e32 v106, v98
	v_permlane32_swap_b32_e32 v107, v99
	s_movk_i32 s5, 0xff9c
	s_mov_b32 s4, 0xc2000000
	s_waitcnt vmcnt(8)
	v_pk_mul_f32 v[0:1], v[208:209], v[108:109]
	s_nop 0
	v_and_b32_e32 v19, 0x7fffffff, v1
	v_and_b32_e32 v18, 0x7fffffff, v0
	v_pk_fma_f32 v[26:27], v[18:19], s[16:17], 1.0 op_sel_hi:[1,0,0]
	v_pk_mul_f32 v[2:3], v[210:211], v[110:111]
	v_rcp_f32_e32 v26, v26
	v_rcp_f32_e32 v27, v27
	v_and_b32_e32 v23, 0x7fffffff, v3
	v_and_b32_e32 v22, 0x7fffffff, v2
	v_pk_mul_f32 v[4:5], v[212:213], v[104:105]
	v_pk_fma_f32 v[28:29], v[22:23], s[16:17], 1.0 op_sel_hi:[1,0,0]
	v_pk_mul_f32 v[20:21], v[0:1], v[0:1]
	v_and_b32_e32 v31, 0x7fffffff, v5
	v_and_b32_e32 v30, 0x7fffffff, v4
	v_rcp_f32_e32 v28, v28
	v_rcp_f32_e32 v29, v29
	v_pk_mul_f32 v[20:21], v[20:21], s[10:11] op_sel_hi:[1,0]
	v_pk_fma_f32 v[36:37], v[30:31], s[16:17], 1.0 op_sel_hi:[1,0,0]
	v_pk_fma_f32 v[38:39], v[26:27], s[12:13], v[16:17] op_sel_hi:[1,0,0]
	v_exp_f32_e32 v20, v20
	v_exp_f32_e32 v21, v21
	v_rcp_f32_e32 v36, v36
	v_rcp_f32_e32 v37, v37
	v_pk_fma_f32 v[38:39], v[26:27], v[38:39], s[14:15] op_sel_hi:[1,1,0]
	v_pk_mul_f32 v[24:25], v[2:3], v[2:3]
	v_pk_fma_f32 v[38:39], v[26:27], v[38:39], s[2:3] op_sel_hi:[1,1,0]
	v_pk_mul_f32 v[24:25], v[24:25], s[10:11] op_sel_hi:[1,0]
	v_pk_fma_f32 v[40:41], v[28:29], s[12:13], v[16:17] op_sel_hi:[1,0,0]
	v_pk_fma_f32 v[38:39], v[26:27], v[38:39], s[8:9] op_sel_hi:[1,1,0]
	v_pk_mul_f32 v[32:33], v[4:5], v[4:5]
	v_exp_f32_e32 v24, v24
	v_exp_f32_e32 v25, v25
	v_pk_fma_f32 v[40:41], v[28:29], v[40:41], s[14:15] op_sel_hi:[1,1,0]
	v_pk_mul_f32 v[26:27], v[26:27], v[38:39]
	v_pk_mul_f32 v[6:7], v[214:215], v[106:107]
	v_pk_mul_f32 v[32:33], v[32:33], s[10:11] op_sel_hi:[1,0]
	v_pk_fma_f32 v[42:43], v[36:37], s[12:13], v[16:17] op_sel_hi:[1,0,0]
	v_pk_fma_f32 v[40:41], v[28:29], v[40:41], s[2:3] op_sel_hi:[1,1,0]
	v_pk_fma_f32 v[20:21], v[20:21], v[26:27], 0.5 op_sel_hi:[1,1,0] neg_lo:[1,0,0] neg_hi:[1,0,0]
	v_and_b32_e32 v35, 0x7fffffff, v7
	v_and_b32_e32 v34, 0x7fffffff, v6
	v_exp_f32_e32 v32, v32
	v_exp_f32_e32 v33, v33
	v_pk_fma_f32 v[42:43], v[36:37], v[42:43], s[14:15] op_sel_hi:[1,1,0]
	v_pk_fma_f32 v[40:41], v[28:29], v[40:41], s[8:9] op_sel_hi:[1,1,0]
	v_pk_mul_f32 v[18:19], v[18:19], v[20:21]
	v_pk_fma_f32 v[42:43], v[36:37], v[42:43], s[2:3] op_sel_hi:[1,1,0]
	v_pk_mul_f32 v[28:29], v[28:29], v[40:41]
	v_pk_fma_f32 v[0:1], v[0:1], 0.5, v[18:19] op_sel_hi:[1,0,1]
	v_pk_fma_f32 v[18:19], v[34:35], s[16:17], 1.0 op_sel_hi:[1,0,0]
	v_pk_fma_f32 v[38:39], v[36:37], v[42:43], s[8:9] op_sel_hi:[1,1,0]
	v_pk_fma_f32 v[24:25], v[24:25], v[28:29], 0.5 op_sel_hi:[1,1,0] neg_lo:[1,0,0] neg_hi:[1,0,0]
	v_rcp_f32_e32 v18, v18
	v_rcp_f32_e32 v19, v19
	v_pk_mul_f32 v[26:27], v[36:37], v[38:39]
	v_pk_mul_f32 v[20:21], v[22:23], v[24:25]
	v_pk_mul_f32 v[8:9], v[216:217], v[100:101]
	v_pk_fma_f32 v[2:3], v[2:3], 0.5, v[20:21] op_sel_hi:[1,0,1]
	v_pk_fma_f32 v[20:21], v[32:33], v[26:27], 0.5 op_sel_hi:[1,1,0] neg_lo:[1,0,0] neg_hi:[1,0,0]
	v_and_b32_e32 v23, 0x7fffffff, v9
	v_pk_mul_f32 v[20:21], v[30:31], v[20:21]
	v_and_b32_e32 v22, 0x7fffffff, v8
	v_pk_fma_f32 v[4:5], v[4:5], 0.5, v[20:21] op_sel_hi:[1,0,1]
	v_pk_fma_f32 v[20:21], v[18:19], s[12:13], v[16:17] op_sel_hi:[1,0,0]
	v_pk_fma_f32 v[24:25], v[22:23], s[16:17], 1.0 op_sel_hi:[1,0,0]
	v_pk_fma_f32 v[20:21], v[18:19], v[20:21], s[14:15] op_sel_hi:[1,1,0]
	v_rcp_f32_e32 v24, v24
	v_pk_fma_f32 v[20:21], v[18:19], v[20:21], s[2:3] op_sel_hi:[1,1,0]
	v_rcp_f32_e32 v25, v25
	v_pk_fma_f32 v[20:21], v[18:19], v[20:21], s[8:9] op_sel_hi:[1,1,0]
	v_pk_mul_f32 v[10:11], v[218:219], v[102:103]
	v_pk_mul_f32 v[18:19], v[18:19], v[20:21]
	v_pk_mul_f32 v[20:21], v[6:7], v[6:7]
	v_pk_mul_f32 v[12:13], v[220:221], v[96:97]
	v_pk_mul_f32 v[20:21], v[20:21], s[10:11] op_sel_hi:[1,0]
	v_pk_mul_f32 v[14:15], v[222:223], v[98:99]
	v_exp_f32_e32 v20, v20
	v_exp_f32_e32 v21, v21
	v_mov_b32_e32 v96, 0xffffff7f
	v_mov_b32_e32 v97, 0x64
	v_pk_fma_f32 v[18:19], v[20:21], v[18:19], 0.5 op_sel_hi:[1,1,0] neg_lo:[1,0,0] neg_hi:[1,0,0]
	s_nop 0
	v_pk_mul_f32 v[18:19], v[34:35], v[18:19]
	v_pk_mul_f32 v[20:21], v[8:9], v[8:9]
	v_pk_fma_f32 v[6:7], v[6:7], 0.5, v[18:19] op_sel_hi:[1,0,1]
	v_pk_fma_f32 v[18:19], v[24:25], s[12:13], v[16:17] op_sel_hi:[1,0,0]
	v_pk_mul_f32 v[20:21], v[20:21], s[10:11] op_sel_hi:[1,0]
	v_pk_fma_f32 v[18:19], v[24:25], v[18:19], s[14:15] op_sel_hi:[1,1,0]
	v_exp_f32_e32 v20, v20
	v_pk_fma_f32 v[18:19], v[24:25], v[18:19], s[2:3] op_sel_hi:[1,1,0]
	v_exp_f32_e32 v21, v21
	v_pk_fma_f32 v[18:19], v[24:25], v[18:19], s[8:9] op_sel_hi:[1,1,0]
	s_nop 0
	v_pk_mul_f32 v[18:19], v[24:25], v[18:19]
	v_and_b32_e32 v25, 0x7fffffff, v11
	v_and_b32_e32 v24, 0x7fffffff, v10
	v_pk_fma_f32 v[26:27], v[24:25], s[16:17], 1.0 op_sel_hi:[1,0,0]
	v_pk_fma_f32 v[18:19], v[20:21], v[18:19], 0.5 op_sel_hi:[1,1,0] neg_lo:[1,0,0] neg_hi:[1,0,0]
	v_rcp_f32_e32 v26, v26
	v_rcp_f32_e32 v27, v27
	v_pk_mul_f32 v[18:19], v[22:23], v[18:19]
	v_pk_mul_f32 v[20:21], v[10:11], v[10:11]
	v_pk_fma_f32 v[8:9], v[8:9], 0.5, v[18:19] op_sel_hi:[1,0,1]
	v_pk_fma_f32 v[18:19], v[26:27], s[12:13], v[16:17] op_sel_hi:[1,0,0]
	v_pk_mul_f32 v[20:21], v[20:21], s[10:11] op_sel_hi:[1,0]
	v_pk_fma_f32 v[18:19], v[26:27], v[18:19], s[14:15] op_sel_hi:[1,1,0]
	v_exp_f32_e32 v20, v20
	v_pk_fma_f32 v[18:19], v[26:27], v[18:19], s[2:3] op_sel_hi:[1,1,0]
	v_exp_f32_e32 v21, v21
	v_pk_fma_f32 v[18:19], v[26:27], v[18:19], s[8:9] op_sel_hi:[1,1,0]
	v_and_b32_e32 v23, 0x7fffffff, v13
	v_and_b32_e32 v22, 0x7fffffff, v12
	v_pk_mul_f32 v[18:19], v[26:27], v[18:19]
	v_pk_fma_f32 v[26:27], v[22:23], s[16:17], 1.0 op_sel_hi:[1,0,0]
	v_pk_fma_f32 v[18:19], v[20:21], v[18:19], 0.5 op_sel_hi:[1,1,0] neg_lo:[1,0,0] neg_hi:[1,0,0]
	v_rcp_f32_e32 v26, v26
	v_rcp_f32_e32 v27, v27
	v_pk_mul_f32 v[18:19], v[24:25], v[18:19]
	v_pk_mul_f32 v[20:21], v[12:13], v[12:13]
	v_pk_fma_f32 v[10:11], v[10:11], 0.5, v[18:19] op_sel_hi:[1,0,1]
	v_pk_fma_f32 v[18:19], v[26:27], s[12:13], v[16:17] op_sel_hi:[1,0,0]
	v_pk_mul_f32 v[20:21], v[20:21], s[10:11] op_sel_hi:[1,0]
	v_pk_fma_f32 v[18:19], v[26:27], v[18:19], s[14:15] op_sel_hi:[1,1,0]
	v_exp_f32_e32 v20, v20
	v_pk_fma_f32 v[18:19], v[26:27], v[18:19], s[2:3] op_sel_hi:[1,1,0]
	v_exp_f32_e32 v21, v21
	v_pk_fma_f32 v[18:19], v[26:27], v[18:19], s[8:9] op_sel_hi:[1,1,0]
	v_and_b32_e32 v25, 0x7fffffff, v15
	v_and_b32_e32 v24, 0x7fffffff, v14
	v_pk_mul_f32 v[18:19], v[26:27], v[18:19]
	v_pk_fma_f32 v[26:27], v[24:25], s[16:17], 1.0 op_sel_hi:[1,0,0]
	v_pk_fma_f32 v[18:19], v[20:21], v[18:19], 0.5 op_sel_hi:[1,1,0] neg_lo:[1,0,0] neg_hi:[1,0,0]
	v_rcp_f32_e32 v26, v26
	v_rcp_f32_e32 v27, v27
	v_pk_mul_f32 v[18:19], v[22:23], v[18:19]
	v_pk_fma_f32 v[16:17], v[26:27], s[12:13], v[16:17] op_sel_hi:[1,0,0]
	v_pk_fma_f32 v[12:13], v[12:13], 0.5, v[18:19] op_sel_hi:[1,0,1]
	v_pk_mul_f32 v[18:19], v[14:15], v[14:15]
	v_pk_fma_f32 v[16:17], v[26:27], v[16:17], s[14:15] op_sel_hi:[1,1,0]
	v_pk_mul_f32 v[18:19], v[18:19], s[10:11] op_sel_hi:[1,0]
	v_pk_fma_f32 v[16:17], v[26:27], v[16:17], s[2:3] op_sel_hi:[1,1,0]
	v_exp_f32_e32 v18, v18
	v_exp_f32_e32 v19, v19
	v_pk_fma_f32 v[16:17], v[26:27], v[16:17], s[8:9] op_sel_hi:[1,1,0]
	s_mov_b32 s3, 0x700000
	v_pk_mul_f32 v[16:17], v[26:27], v[16:17]
	s_mov_b32 s9, 0x42000000
	v_pk_fma_f32 v[16:17], v[18:19], v[16:17], 0.5 op_sel_hi:[1,1,0] neg_lo:[1,0,0] neg_hi:[1,0,0]
	v_max_f32_e64 v18, |v6|, |v7|
	v_pk_mul_f32 v[16:17], v[24:25], v[16:17]
	s_nop 0
	v_pk_fma_f32 v[14:15], v[14:15], 0.5, v[16:17] op_sel_hi:[1,0,1]
	v_max_f32_e64 v16, |v0|, |v1|
	v_max_f32_e64 v17, |v2|, |v3|
	v_max3_f32 v16, v16, 0, v17
	v_max_f32_e64 v17, |v4|, |v5|
	v_max3_f32 v16, v16, v17, v18
	v_max_f32_e64 v17, |v8|, |v9|
	v_max_f32_e64 v18, |v10|, |v11|
	v_max3_f32 v16, v16, v17, v18
	v_max_f32_e64 v17, |v12|, |v13|
	v_max_f32_e64 v18, |v14|, |v15|
	v_max3_f32 v16, v16, v17, v18
	v_mov_b32_e32 v17, v16
	s_nop 1
	v_permlane16_swap_b32_e32 v16, v17
	v_max_f32_e32 v17, v17, v17
	v_max_f32_e32 v16, v16, v16
	v_max_f32_e32 v16, v16, v17
	v_lshrrev_b32_e32 v17, 23, v16
	v_and_b32_e32 v16, 0x7fffff, v16
	v_cmp_lt_u32_e32 vcc, s3, v16
	s_nop 1
	v_addc_co_u32_e32 v16, vcc, v17, v96, vcc
	v_med3_i32 v98, v16, s5, v97
	v_lshlrev_b32_e32 v16, 23, v98
	v_sub_u32_e32 v16, 1.0, v16
	v_pk_mul_f32 v[40:41], v[16:17], v[8:9] op_sel_hi:[0,1]
	v_pk_mul_f32 v[42:43], v[16:17], v[10:11] op_sel_hi:[0,1]
	v_pk_mul_f32 v[44:45], v[16:17], v[12:13] op_sel_hi:[0,1]
	v_pk_mul_f32 v[46:47], v[16:17], v[14:15] op_sel_hi:[0,1]
	v_pk_mul_f32 v[32:33], v[16:17], v[0:1] op_sel_hi:[0,1]
	v_pk_mul_f32 v[34:35], v[16:17], v[2:3] op_sel_hi:[0,1]
	v_pk_mul_f32 v[36:37], v[16:17], v[4:5] op_sel_hi:[0,1]
	v_pk_mul_f32 v[38:39], v[16:17], v[6:7] op_sel_hi:[0,1]
	v_mov_b32_e32 v0, v40
	v_mov_b32_e32 v1, v41
	v_mov_b32_e32 v2, v42
	v_mov_b32_e32 v3, v43
	v_mov_b32_e32 v4, v44
	v_mov_b32_e32 v5, v45
	v_mov_b32_e32 v6, v46
	v_mov_b32_e32 v7, v47
	v_cvt_scalef32_2xpk16_fp6_f32 v[100:105], v[32:47], v[0:15], 1.0
	v_cvt_scalef32_pk32_f32_fp6 v[0:31], v[100:105], s9
	v_mov_b32_e32 v16, v0
	v_mov_b32_e32 v17, v2
	v_mov_b32_e32 v2, v1
	v_mov_b32_e32 v0, v4
	v_mov_b32_e32 v1, v6
	v_pk_fma_f32 v[18:19], v[34:35], s[4:5], v[0:1] op_sel_hi:[1,0,1]
	v_mov_b32_e32 v0, v8
	v_mov_b32_e32 v1, v10
	v_mov_b32_e32 v6, v5
	v_pk_fma_f32 v[20:21], v[36:37], s[4:5], v[0:1] op_sel_hi:[1,0,1]
	v_mov_b32_e32 v10, v9
	v_mov_b32_e32 v1, v14
	v_mov_b32_e32 v14, v13
	v_pk_fma_f32 v[24:25], v[40:41], s[4:5], v[2:3] op_sel_hi:[1,0,1]
	v_pk_fma_f32 v[26:27], v[42:43], s[4:5], v[6:7] op_sel_hi:[1,0,1]
	v_pk_fma_f32 v[28:29], v[44:45], s[4:5], v[10:11] op_sel_hi:[1,0,1]
	v_mov_b32_e32 v0, v12
	v_pk_fma_f32 v[30:31], v[46:47], s[4:5], v[14:15] op_sel_hi:[1,0,1]
	v_pk_fma_f32 v[16:17], v[32:33], s[4:5], v[16:17] op_sel_hi:[1,0,1]
	v_pk_fma_f32 v[22:23], v[38:39], s[4:5], v[0:1] op_sel_hi:[1,0,1]
	v_mov_b32_e32 v0, v24
	v_mov_b32_e32 v1, v25
	v_mov_b32_e32 v2, v26
	v_mov_b32_e32 v3, v27
	v_mov_b32_e32 v4, v28
	v_mov_b32_e32 v5, v29
	v_mov_b32_e32 v6, v30
	v_mov_b32_e32 v7, v31
	v_cvt_scalef32_2xpk16_fp6_f32 v[0:5], v[16:31], v[0:15], 1.0
	v_lshl_add_u64 v[4:5], v[118:119], 0, v[164:165]
	v_lshl_add_u64 v[4:5], v[4:5], 0, v[160:161]
	global_store_dwordx3 v[4:5], v[100:102], off nt
	v_add_co_u32_e32 v4, vcc, 0x1000, v4
	v_xor_b32_e32 v0, 0x20820820, v0
	v_xor_b32_e32 v1, 0x8208208, v1
	v_xor_b32_e32 v2, 0x82082082, v2
	v_addc_co_u32_e32 v5, vcc, 0, v5, vcc
	global_store_dwordx3 v[4:5], v[0:2], off offset:2048 nt
	s_and_saveexec_b64 s[6:7], s[0:1]
	s_cbranch_execz .LBB3_16
	v_mov_b32_e32 v1, 0x7a00
	v_add_u32_e32 v0, 0x7f, v98
	v_lshl_add_u32 v1, v98, 8, v1
	v_mov_b32_e32 v163, 0
	v_or_b32_e32 v2, v1, v0
	v_lshl_add_u64 v[0:1], v[116:117], 0, v[162:163]
	global_store_short v[0:1], v2, off
.LBB3_16:
	s_or_b64 exec, exec, s[6:7]
	v_permlane32_swap_b32_e32 v92, v84
	v_permlane32_swap_b32_e32 v93, v85
	v_permlane32_swap_b32_e32 v94, v86
	v_permlane32_swap_b32_e32 v95, v87
	v_permlane32_swap_b32_e32 v90, v82
	v_permlane32_swap_b32_e32 v91, v83
	v_permlane32_swap_b32_e32 v88, v80
	v_permlane32_swap_b32_e32 v89, v81
	v_mov_b64_e32 v[16:17], s[18:19]
	v_pk_mul_f32 v[0:1], v[208:209], v[92:93]
	v_pk_mul_f32 v[2:3], v[210:211], v[94:95]
	v_and_b32_e32 v19, 0x7fffffff, v1
	v_and_b32_e32 v18, 0x7fffffff, v0
	v_pk_mul_f32 v[6:7], v[214:215], v[90:91]
	v_and_b32_e32 v23, 0x7fffffff, v3
	v_and_b32_e32 v22, 0x7fffffff, v2
	v_pk_fma_f32 v[36:37], v[18:19], s[16:17], 1.0 op_sel_hi:[1,0,0]
	v_pk_mul_f32 v[4:5], v[212:213], v[88:89]
	v_and_b32_e32 v31, 0x7fffffff, v7
	v_and_b32_e32 v30, 0x7fffffff, v6
	v_pk_fma_f32 v[38:39], v[22:23], s[16:17], 1.0 op_sel_hi:[1,0,0]
	v_rcp_f32_e32 v36, v36
	v_rcp_f32_e32 v37, v37
	v_and_b32_e32 v27, 0x7fffffff, v5
	v_and_b32_e32 v26, 0x7fffffff, v4
	v_pk_fma_f32 v[42:43], v[30:31], s[16:17], 1.0 op_sel_hi:[1,0,0]
	v_rcp_f32_e32 v38, v38
	v_rcp_f32_e32 v39, v39
	v_pk_fma_f32 v[40:41], v[26:27], s[16:17], 1.0 op_sel_hi:[1,0,0]
	v_rcp_f32_e32 v42, v42
	v_rcp_f32_e32 v43, v43
	v_pk_mul_f32 v[20:21], v[0:1], v[0:1]
	v_rcp_f32_e32 v40, v40
	v_rcp_f32_e32 v41, v41
	v_pk_mul_f32 v[24:25], v[2:3], v[2:3]
	v_pk_mul_f32 v[20:21], v[20:21], s[10:11] op_sel_hi:[1,0]
	v_pk_fma_f32 v[46:47], v[36:37], s[12:13], v[16:17] op_sel_hi:[1,0,0]
	v_pk_mul_f32 v[8:9], v[216:217], v[84:85]
	v_pk_mul_f32 v[32:33], v[6:7], v[6:7]
	v_pk_mul_f32 v[24:25], v[24:25], s[10:11] op_sel_hi:[1,0]
	v_exp_f32_e32 v20, v20
	v_exp_f32_e32 v21, v21
	v_pk_fma_f32 v[84:85], v[38:39], s[12:13], v[16:17] op_sel_hi:[1,0,0]
	v_pk_fma_f32 v[46:47], v[36:37], v[46:47], s[14:15] op_sel_hi:[1,1,0]
	v_pk_mul_f32 v[28:29], v[4:5], v[4:5]
	v_pk_mul_f32 v[32:33], v[32:33], s[10:11] op_sel_hi:[1,0]
	v_exp_f32_e32 v24, v24
	v_exp_f32_e32 v25, v25
	v_pk_fma_f32 v[90:91], v[42:43], s[12:13], v[16:17] op_sel_hi:[1,0,0]
	v_pk_fma_f32 v[84:85], v[38:39], v[84:85], s[14:15] op_sel_hi:[1,1,0]
	v_pk_fma_f32 v[46:47], v[36:37], v[46:47], s[2:3] op_sel_hi:[1,1,0]
	v_and_b32_e32 v35, 0x7fffffff, v9
	v_and_b32_e32 v34, 0x7fffffff, v8
	v_pk_mul_f32 v[28:29], v[28:29], s[10:11] op_sel_hi:[1,0]
	v_exp_f32_e32 v32, v32
	v_exp_f32_e32 v33, v33
	v_pk_fma_f32 v[88:89], v[40:41], s[12:13], v[16:17] op_sel_hi:[1,0,0]
	v_pk_fma_f32 v[90:91], v[42:43], v[90:91], s[14:15] op_sel_hi:[1,1,0]
	v_pk_fma_f32 v[84:85], v[38:39], v[84:85], s[2:3] op_sel_hi:[1,1,0]
	v_pk_fma_f32 v[46:47], v[36:37], v[46:47], s[8:9] op_sel_hi:[1,1,0]
	v_pk_fma_f32 v[44:45], v[34:35], s[16:17], 1.0 op_sel_hi:[1,0,0]
	v_exp_f32_e32 v28, v28
	v_exp_f32_e32 v29, v29
	v_pk_fma_f32 v[88:89], v[40:41], v[88:89], s[14:15] op_sel_hi:[1,1,0]
	v_pk_fma_f32 v[90:91], v[42:43], v[90:91], s[2:3] op_sel_hi:[1,1,0]
	v_pk_fma_f32 v[84:85], v[38:39], v[84:85], s[8:9] op_sel_hi:[1,1,0]
	v_pk_mul_f32 v[36:37], v[36:37], v[46:47]
	v_rcp_f32_e32 v44, v44
	v_pk_fma_f32 v[88:89], v[40:41], v[88:89], s[2:3] op_sel_hi:[1,1,0]
	v_pk_fma_f32 v[90:91], v[42:43], v[90:91], s[8:9] op_sel_hi:[1,1,0]
	v_pk_mul_f32 v[38:39], v[38:39], v[84:85]
	v_pk_fma_f32 v[20:21], v[20:21], v[36:37], 0.5 op_sel_hi:[1,1,0] neg_lo:[1,0,0] neg_hi:[1,0,0]
	v_rcp_f32_e32 v45, v45
	v_pk_fma_f32 v[88:89], v[40:41], v[88:89], s[8:9] op_sel_hi:[1,1,0]
	v_pk_mul_f32 v[42:43], v[42:43], v[90:91]
	v_pk_fma_f32 v[24:25], v[24:25], v[38:39], 0.5 op_sel_hi:[1,1,0] neg_lo:[1,0,0] neg_hi:[1,0,0]
	v_pk_mul_f32 v[18:19], v[18:19], v[20:21]
	v_pk_mul_f32 v[40:41], v[40:41], v[88:89]
	v_pk_mul_f32 v[20:21], v[22:23], v[24:25]
	v_pk_fma_f32 v[0:1], v[0:1], 0.5, v[18:19] op_sel_hi:[1,0,1]
	v_pk_fma_f32 v[18:19], v[32:33], v[42:43], 0.5 op_sel_hi:[1,1,0] neg_lo:[1,0,0] neg_hi:[1,0,0]
	v_pk_fma_f32 v[28:29], v[28:29], v[40:41], 0.5 op_sel_hi:[1,1,0] neg_lo:[1,0,0] neg_hi:[1,0,0]
	v_pk_fma_f32 v[2:3], v[2:3], 0.5, v[20:21] op_sel_hi:[1,0,1]
	v_pk_mul_f32 v[18:19], v[30:31], v[18:19]
	v_pk_mul_f32 v[20:21], v[8:9], v[8:9]
	v_pk_mul_f32 v[22:23], v[26:27], v[28:29]
	v_pk_fma_f32 v[6:7], v[6:7], 0.5, v[18:19] op_sel_hi:[1,0,1]
	v_pk_fma_f32 v[18:19], v[44:45], s[12:13], v[16:17] op_sel_hi:[1,0,0]
	v_pk_mul_f32 v[20:21], v[20:21], s[10:11] op_sel_hi:[1,0]
	v_pk_mul_f32 v[10:11], v[218:219], v[86:87]
	v_pk_fma_f32 v[4:5], v[4:5], 0.5, v[22:23] op_sel_hi:[1,0,1]
	v_pk_fma_f32 v[18:19], v[44:45], v[18:19], s[14:15] op_sel_hi:[1,1,0]
	v_exp_f32_e32 v20, v20
	v_exp_f32_e32 v21, v21
	v_and_b32_e32 v23, 0x7fffffff, v11
	v_and_b32_e32 v22, 0x7fffffff, v10
	v_pk_fma_f32 v[18:19], v[44:45], v[18:19], s[2:3] op_sel_hi:[1,1,0]
	v_pk_fma_f32 v[24:25], v[22:23], s[16:17], 1.0 op_sel_hi:[1,0,0]
	v_pk_fma_f32 v[18:19], v[44:45], v[18:19], s[8:9] op_sel_hi:[1,1,0]
	v_rcp_f32_e32 v24, v24
	v_rcp_f32_e32 v25, v25
	v_pk_mul_f32 v[18:19], v[44:45], v[18:19]
	v_pk_mul_f32 v[12:13], v[220:221], v[80:81]
	v_pk_fma_f32 v[18:19], v[20:21], v[18:19], 0.5 op_sel_hi:[1,1,0] neg_lo:[1,0,0] neg_hi:[1,0,0]
	v_pk_mul_f32 v[20:21], v[10:11], v[10:11]
	v_pk_mul_f32 v[18:19], v[34:35], v[18:19]
	v_pk_mul_f32 v[20:21], v[20:21], s[10:11] op_sel_hi:[1,0]
	v_pk_fma_f32 v[8:9], v[8:9], 0.5, v[18:19] op_sel_hi:[1,0,1]
	v_pk_fma_f32 v[18:19], v[24:25], s[12:13], v[16:17] op_sel_hi:[1,0,0]
	v_exp_f32_e32 v20, v20
	v_pk_fma_f32 v[18:19], v[24:25], v[18:19], s[14:15] op_sel_hi:[1,1,0]
	v_exp_f32_e32 v21, v21
	v_pk_fma_f32 v[18:19], v[24:25], v[18:19], s[2:3] op_sel_hi:[1,1,0]
	v_pk_mul_f32 v[14:15], v[222:223], v[82:83]
	v_pk_fma_f32 v[18:19], v[24:25], v[18:19], s[8:9] op_sel_hi:[1,1,0]
	s_nop 0
	v_pk_mul_f32 v[18:19], v[24:25], v[18:19]
	v_and_b32_e32 v25, 0x7fffffff, v13
	v_and_b32_e32 v24, 0x7fffffff, v12
	v_pk_fma_f32 v[26:27], v[24:25], s[16:17], 1.0 op_sel_hi:[1,0,0]
	v_pk_fma_f32 v[18:19], v[20:21], v[18:19], 0.5 op_sel_hi:[1,1,0] neg_lo:[1,0,0] neg_hi:[1,0,0]
	v_rcp_f32_e32 v26, v26
	v_rcp_f32_e32 v27, v27
	v_pk_mul_f32 v[18:19], v[22:23], v[18:19]
	v_pk_mul_f32 v[20:21], v[12:13], v[12:13]
	v_pk_fma_f32 v[10:11], v[10:11], 0.5, v[18:19] op_sel_hi:[1,0,1]
	v_pk_fma_f32 v[18:19], v[26:27], s[12:13], v[16:17] op_sel_hi:[1,0,0]
	v_pk_mul_f32 v[20:21], v[20:21], s[10:11] op_sel_hi:[1,0]
	v_pk_fma_f32 v[18:19], v[26:27], v[18:19], s[14:15] op_sel_hi:[1,1,0]
	v_exp_f32_e32 v20, v20
	v_pk_fma_f32 v[18:19], v[26:27], v[18:19], s[2:3] op_sel_hi:[1,1,0]
	v_exp_f32_e32 v21, v21
	v_pk_fma_f32 v[18:19], v[26:27], v[18:19], s[8:9] op_sel_hi:[1,1,0]
	v_and_b32_e32 v23, 0x7fffffff, v15
	v_and_b32_e32 v22, 0x7fffffff, v14
	v_pk_mul_f32 v[18:19], v[26:27], v[18:19]
	v_pk_fma_f32 v[26:27], v[22:23], s[16:17], 1.0 op_sel_hi:[1,0,0]
	v_pk_fma_f32 v[18:19], v[20:21], v[18:19], 0.5 op_sel_hi:[1,1,0] neg_lo:[1,0,0] neg_hi:[1,0,0]
	v_rcp_f32_e32 v26, v26
	v_rcp_f32_e32 v27, v27
	v_pk_mul_f32 v[18:19], v[24:25], v[18:19]
	v_pk_fma_f32 v[16:17], v[26:27], s[12:13], v[16:17] op_sel_hi:[1,0,0]
	v_pk_fma_f32 v[12:13], v[12:13], 0.5, v[18:19] op_sel_hi:[1,0,1]
	v_pk_mul_f32 v[18:19], v[14:15], v[14:15]
	v_pk_fma_f32 v[16:17], v[26:27], v[16:17], s[14:15] op_sel_hi:[1,1,0]
	v_pk_mul_f32 v[18:19], v[18:19], s[10:11] op_sel_hi:[1,0]
	v_pk_fma_f32 v[16:17], v[26:27], v[16:17], s[2:3] op_sel_hi:[1,1,0]
	v_exp_f32_e32 v18, v18
	v_exp_f32_e32 v19, v19
	v_pk_fma_f32 v[16:17], v[26:27], v[16:17], s[8:9] op_sel_hi:[1,1,0]
	s_nop 0
	v_pk_mul_f32 v[16:17], v[26:27], v[16:17]
	s_nop 0
	v_pk_fma_f32 v[16:17], v[18:19], v[16:17], 0.5 op_sel_hi:[1,1,0] neg_lo:[1,0,0] neg_hi:[1,0,0]
	v_max_f32_e64 v18, |v6|, |v7|
	v_pk_mul_f32 v[16:17], v[22:23], v[16:17]
	s_nop 0
	v_pk_fma_f32 v[14:15], v[14:15], 0.5, v[16:17] op_sel_hi:[1,0,1]
	v_max_f32_e64 v16, |v0|, |v1|
	v_max_f32_e64 v17, |v2|, |v3|
	v_max3_f32 v16, v16, 0, v17
	v_max_f32_e64 v17, |v4|, |v5|
	v_max3_f32 v16, v16, v17, v18
	v_max_f32_e64 v17, |v8|, |v9|
	v_max_f32_e64 v18, |v10|, |v11|
	v_max3_f32 v16, v16, v17, v18
	v_max_f32_e64 v17, |v12|, |v13|
	v_max_f32_e64 v18, |v14|, |v15|
	v_max3_f32 v16, v16, v17, v18
	v_mov_b32_e32 v17, v16
	s_nop 1
	v_permlane16_swap_b32_e32 v16, v17
	v_max_f32_e32 v17, v17, v17
	v_max_f32_e32 v16, v16, v16
	v_max_f32_e32 v16, v16, v17
	v_lshrrev_b32_e32 v17, 23, v16
	v_and_b32_e32 v16, 0x7fffff, v16
	v_cmp_lt_u32_e32 vcc, s3, v16
	s_nop 1
	v_addc_co_u32_e32 v16, vcc, v17, v96, vcc
	v_med3_i32 v80, v16, s5, v97
	v_lshlrev_b32_e32 v16, 23, v80
	v_sub_u32_e32 v16, 1.0, v16
	v_pk_mul_f32 v[40:41], v[16:17], v[8:9] op_sel_hi:[0,1]
	v_pk_mul_f32 v[42:43], v[16:17], v[10:11] op_sel_hi:[0,1]
	v_pk_mul_f32 v[44:45], v[16:17], v[12:13] op_sel_hi:[0,1]
	v_pk_mul_f32 v[46:47], v[16:17], v[14:15] op_sel_hi:[0,1]
	v_pk_mul_f32 v[32:33], v[16:17], v[0:1] op_sel_hi:[0,1]
	v_pk_mul_f32 v[34:35], v[16:17], v[2:3] op_sel_hi:[0,1]
	v_pk_mul_f32 v[36:37], v[16:17], v[4:5] op_sel_hi:[0,1]
	v_pk_mul_f32 v[38:39], v[16:17], v[6:7] op_sel_hi:[0,1]
	v_mov_b32_e32 v0, v40
	v_mov_b32_e32 v1, v41
	v_mov_b32_e32 v2, v42
	v_mov_b32_e32 v3, v43
	v_mov_b32_e32 v4, v44
	v_mov_b32_e32 v5, v45
	v_mov_b32_e32 v6, v46
	v_mov_b32_e32 v7, v47
	v_cvt_scalef32_2xpk16_fp6_f32 v[82:87], v[32:47], v[0:15], 1.0
	v_cvt_scalef32_pk32_f32_fp6 v[0:31], v[82:87], s9
	v_mov_b32_e32 v16, v0
	v_mov_b32_e32 v17, v2
	v_mov_b32_e32 v2, v1
	v_mov_b32_e32 v0, v4
	v_mov_b32_e32 v1, v6
	v_pk_fma_f32 v[18:19], v[34:35], s[4:5], v[0:1] op_sel_hi:[1,0,1]
	v_mov_b32_e32 v0, v8
	v_mov_b32_e32 v1, v10
	v_mov_b32_e32 v6, v5
	v_pk_fma_f32 v[20:21], v[36:37], s[4:5], v[0:1] op_sel_hi:[1,0,1]
	v_mov_b32_e32 v10, v9
	v_mov_b32_e32 v1, v14
	v_mov_b32_e32 v14, v13
	v_pk_fma_f32 v[24:25], v[40:41], s[4:5], v[2:3] op_sel_hi:[1,0,1]
	v_pk_fma_f32 v[26:27], v[42:43], s[4:5], v[6:7] op_sel_hi:[1,0,1]
	v_pk_fma_f32 v[28:29], v[44:45], s[4:5], v[10:11] op_sel_hi:[1,0,1]
	v_mov_b32_e32 v0, v12
	v_pk_fma_f32 v[30:31], v[46:47], s[4:5], v[14:15] op_sel_hi:[1,0,1]
	v_pk_fma_f32 v[16:17], v[32:33], s[4:5], v[16:17] op_sel_hi:[1,0,1]
	v_pk_fma_f32 v[22:23], v[38:39], s[4:5], v[0:1] op_sel_hi:[1,0,1]
	v_mov_b32_e32 v0, v24
	v_mov_b32_e32 v1, v25
	v_mov_b32_e32 v2, v26
	v_mov_b32_e32 v3, v27
	v_mov_b32_e32 v4, v28
	v_mov_b32_e32 v5, v29
	v_mov_b32_e32 v6, v30
	v_mov_b32_e32 v7, v31
	v_cvt_scalef32_2xpk16_fp6_f32 v[0:5], v[16:31], v[0:15], 1.0
	v_lshl_add_u64 v[4:5], v[118:119], 0, v[146:147]
	v_lshl_add_u64 v[4:5], v[4:5], 0, v[160:161]
	global_store_dwordx3 v[4:5], v[82:84], off nt
	v_add_co_u32_e32 v4, vcc, 0x1000, v4
	v_xor_b32_e32 v0, 0x20820820, v0
	v_xor_b32_e32 v1, 0x8208208, v1
	v_xor_b32_e32 v2, 0x82082082, v2
	v_addc_co_u32_e32 v5, vcc, 0, v5, vcc
	global_store_dwordx3 v[4:5], v[0:2], off offset:2048 nt
	s_and_saveexec_b64 s[2:3], s[0:1]
	s_cbranch_execz .LBB3_18
	v_mov_b32_e32 v1, 0x7a00
	v_add_u32_e32 v0, 0x7f, v80
	v_lshl_add_u32 v1, v80, 8, v1
	v_mov_b32_e32 v145, 0
	v_or_b32_e32 v2, v1, v0
	v_lshl_add_u64 v[0:1], v[116:117], 0, v[144:145]
	global_store_short v[0:1], v2, off
.LBB3_18:
	s_or_b64 exec, exec, s[2:3]
	v_permlane32_swap_b32_e32 v76, v68
	v_permlane32_swap_b32_e32 v77, v69
	v_permlane32_swap_b32_e32 v78, v70
	v_permlane32_swap_b32_e32 v79, v71
	v_permlane32_swap_b32_e32 v72, v64
	v_permlane32_swap_b32_e32 v73, v65
	s_mov_b32 s12, 0x3e6d3388
	v_permlane32_swap_b32_e32 v74, v66
	v_permlane32_swap_b32_e32 v75, v67
	s_mov_b32 s16, 0xbf3a00e3
	s_mov_b32 s8, 0x3f07dc22
	s_mov_b32 s6, 0xbf38aa3b
	v_mov_b64_e32 v[16:17], s[16:17]
	s_mov_b32 s10, 0x3f35f0e3
	s_mov_b32 s2, 0xbe11a98e
	s_mov_b32 s4, 0x3e027906
	s_mov_b32 s14, 0xc2000000
	v_pk_mul_f32 v[0:1], v[208:209], v[76:77]
	v_pk_mul_f32 v[2:3], v[210:211], v[78:79]
	v_pk_mul_f32 v[4:5], v[212:213], v[72:73]
	v_and_b32_e32 v19, 0x7fffffff, v1
	v_and_b32_e32 v18, 0x7fffffff, v0
	v_and_b32_e32 v23, 0x7fffffff, v3
	v_and_b32_e32 v22, 0x7fffffff, v2
	v_and_b32_e32 v27, 0x7fffffff, v5
	v_and_b32_e32 v26, 0x7fffffff, v4
	v_pk_fma_f32 v[34:35], v[18:19], s[12:13], 1.0 op_sel_hi:[1,0,0]
	v_pk_fma_f32 v[36:37], v[22:23], s[12:13], 1.0 op_sel_hi:[1,0,0]
	v_pk_fma_f32 v[38:39], v[26:27], s[12:13], 1.0 op_sel_hi:[1,0,0]
	v_rcp_f32_e32 v34, v34
	v_rcp_f32_e32 v35, v35
	v_rcp_f32_e32 v36, v36
	v_rcp_f32_e32 v37, v37
	v_rcp_f32_e32 v38, v38
	v_rcp_f32_e32 v39, v39
	v_pk_mul_f32 v[6:7], v[214:215], v[74:75]
	v_pk_mul_f32 v[20:21], v[0:1], v[0:1]
	v_pk_mul_f32 v[24:25], v[2:3], v[2:3]
	v_pk_mul_f32 v[28:29], v[4:5], v[4:5]
	v_and_b32_e32 v31, 0x7fffffff, v7
	v_and_b32_e32 v30, 0x7fffffff, v6
	v_pk_mul_f32 v[20:21], v[20:21], s[6:7] op_sel_hi:[1,0]
	v_pk_mul_f32 v[24:25], v[24:25], s[6:7] op_sel_hi:[1,0]
	v_pk_fma_f32 v[42:43], v[34:35], s[8:9], v[16:17] op_sel_hi:[1,0,0]
	v_pk_fma_f32 v[44:45], v[36:37], s[8:9], v[16:17] op_sel_hi:[1,0,0]
	v_pk_mul_f32 v[28:29], v[28:29], s[6:7] op_sel_hi:[1,0]
	v_pk_fma_f32 v[40:41], v[30:31], s[12:13], 1.0 op_sel_hi:[1,0,0]
	v_exp_f32_e32 v20, v20
	v_exp_f32_e32 v21, v21
	v_exp_f32_e32 v24, v24
	v_exp_f32_e32 v25, v25
	v_pk_fma_f32 v[46:47], v[38:39], s[8:9], v[16:17] op_sel_hi:[1,0,0]
	v_pk_fma_f32 v[42:43], v[34:35], v[42:43], s[10:11] op_sel_hi:[1,1,0]
	v_pk_fma_f32 v[44:45], v[36:37], v[44:45], s[10:11] op_sel_hi:[1,1,0]
	v_exp_f32_e32 v28, v28
	v_exp_f32_e32 v29, v29
	v_rcp_f32_e32 v40, v40
	v_rcp_f32_e32 v41, v41
	v_pk_fma_f32 v[46:47], v[38:39], v[46:47], s[10:11] op_sel_hi:[1,1,0]
	v_pk_fma_f32 v[42:43], v[34:35], v[42:43], s[2:3] op_sel_hi:[1,1,0]
	v_pk_fma_f32 v[44:45], v[36:37], v[44:45], s[2:3] op_sel_hi:[1,1,0]
	v_pk_fma_f32 v[46:47], v[38:39], v[46:47], s[2:3] op_sel_hi:[1,1,0]
	v_pk_fma_f32 v[42:43], v[34:35], v[42:43], s[4:5] op_sel_hi:[1,1,0]
	v_pk_fma_f32 v[44:45], v[36:37], v[44:45], s[4:5] op_sel_hi:[1,1,0]
	v_pk_fma_f32 v[46:47], v[38:39], v[46:47], s[4:5] op_sel_hi:[1,1,0]
	v_pk_mul_f32 v[34:35], v[34:35], v[42:43]
	v_pk_mul_f32 v[36:37], v[36:37], v[44:45]
	v_pk_mul_f32 v[32:33], v[6:7], v[6:7]
	v_pk_mul_f32 v[38:39], v[38:39], v[46:47]
	v_pk_fma_f32 v[20:21], v[20:21], v[34:35], 0.5 op_sel_hi:[1,1,0] neg_lo:[1,0,0] neg_hi:[1,0,0]
	v_pk_fma_f32 v[24:25], v[24:25], v[36:37], 0.5 op_sel_hi:[1,1,0] neg_lo:[1,0,0] neg_hi:[1,0,0]
	v_pk_mul_f32 v[32:33], v[32:33], s[6:7] op_sel_hi:[1,0]
	v_pk_fma_f32 v[72:73], v[40:41], s[8:9], v[16:17] op_sel_hi:[1,0,0]
	v_pk_fma_f32 v[28:29], v[28:29], v[38:39], 0.5 op_sel_hi:[1,1,0] neg_lo:[1,0,0] neg_hi:[1,0,0]
	v_pk_mul_f32 v[18:19], v[18:19], v[20:21]
	v_pk_mul_f32 v[20:21], v[22:23], v[24:25]
	v_pk_mul_f32 v[8:9], v[216:217], v[68:69]
	v_pk_fma_f32 v[72:73], v[40:41], v[72:73], s[10:11] op_sel_hi:[1,1,0]
	v_pk_mul_f32 v[22:23], v[26:27], v[28:29]
	v_pk_fma_f32 v[0:1], v[0:1], 0.5, v[18:19] op_sel_hi:[1,0,1]
	v_pk_fma_f32 v[2:3], v[2:3], 0.5, v[20:21] op_sel_hi:[1,0,1]
	v_exp_f32_e32 v18, v32
	v_exp_f32_e32 v19, v33
	v_and_b32_e32 v21, 0x7fffffff, v9
	v_and_b32_e32 v20, 0x7fffffff, v8
	v_pk_fma_f32 v[72:73], v[40:41], v[72:73], s[2:3] op_sel_hi:[1,1,0]
	v_pk_fma_f32 v[4:5], v[4:5], 0.5, v[22:23] op_sel_hi:[1,0,1]
	v_pk_fma_f32 v[22:23], v[20:21], s[12:13], 1.0 op_sel_hi:[1,0,0]
	v_pk_fma_f32 v[72:73], v[40:41], v[72:73], s[4:5] op_sel_hi:[1,1,0]
	v_rcp_f32_e32 v22, v22
	v_rcp_f32_e32 v23, v23
	v_pk_mul_f32 v[40:41], v[40:41], v[72:73]
	v_pk_mul_f32 v[10:11], v[218:219], v[70:71]
	v_pk_fma_f32 v[18:19], v[18:19], v[40:41], 0.5 op_sel_hi:[1,1,0] neg_lo:[1,0,0] neg_hi:[1,0,0]
	v_and_b32_e32 v25, 0x7fffffff, v11
	v_pk_mul_f32 v[18:19], v[30:31], v[18:19]
	v_and_b32_e32 v24, 0x7fffffff, v10
	v_pk_fma_f32 v[6:7], v[6:7], 0.5, v[18:19] op_sel_hi:[1,0,1]
	v_pk_fma_f32 v[18:19], v[22:23], s[8:9], v[16:17] op_sel_hi:[1,0,0]
	v_pk_fma_f32 v[26:27], v[24:25], s[12:13], 1.0 op_sel_hi:[1,0,0]
	v_pk_fma_f32 v[18:19], v[22:23], v[18:19], s[10:11] op_sel_hi:[1,1,0]
	v_rcp_f32_e32 v26, v26
	v_pk_fma_f32 v[18:19], v[22:23], v[18:19], s[2:3] op_sel_hi:[1,1,0]
	v_rcp_f32_e32 v27, v27
	v_pk_fma_f32 v[18:19], v[22:23], v[18:19], s[4:5] op_sel_hi:[1,1,0]
	v_pk_mul_f32 v[12:13], v[220:221], v[64:65]
	v_pk_mul_f32 v[18:19], v[22:23], v[18:19]
	v_pk_mul_f32 v[22:23], v[8:9], v[8:9]
	v_pk_mul_f32 v[14:15], v[222:223], v[66:67]
	v_pk_mul_f32 v[22:23], v[22:23], s[6:7] op_sel_hi:[1,0]
	v_mov_b32_e32 v64, 0xffffff7f
	v_exp_f32_e32 v22, v22
	v_exp_f32_e32 v23, v23
	v_mov_b32_e32 v65, 0x64
	v_pk_fma_f32 v[18:19], v[22:23], v[18:19], 0.5 op_sel_hi:[1,1,0] neg_lo:[1,0,0] neg_hi:[1,0,0]
	s_nop 0
	v_pk_mul_f32 v[18:19], v[20:21], v[18:19]
	v_pk_mul_f32 v[20:21], v[10:11], v[10:11]
	v_pk_fma_f32 v[8:9], v[8:9], 0.5, v[18:19] op_sel_hi:[1,0,1]
	v_pk_fma_f32 v[18:19], v[26:27], s[8:9], v[16:17] op_sel_hi:[1,0,0]
	v_pk_mul_f32 v[20:21], v[20:21], s[6:7] op_sel_hi:[1,0]
	v_pk_fma_f32 v[18:19], v[26:27], v[18:19], s[10:11] op_sel_hi:[1,1,0]
	v_exp_f32_e32 v20, v20
	v_pk_fma_f32 v[18:19], v[26:27], v[18:19], s[2:3] op_sel_hi:[1,1,0]
	v_exp_f32_e32 v21, v21
	v_pk_fma_f32 v[18:19], v[26:27], v[18:19], s[4:5] op_sel_hi:[1,1,0]
	v_and_b32_e32 v23, 0x7fffffff, v13
	v_and_b32_e32 v22, 0x7fffffff, v12
	v_pk_mul_f32 v[18:19], v[26:27], v[18:19]
	v_pk_fma_f32 v[26:27], v[22:23], s[12:13], 1.0 op_sel_hi:[1,0,0]
	v_pk_fma_f32 v[18:19], v[20:21], v[18:19], 0.5 op_sel_hi:[1,1,0] neg_lo:[1,0,0] neg_hi:[1,0,0]
	v_rcp_f32_e32 v26, v26
	v_rcp_f32_e32 v27, v27
	v_pk_mul_f32 v[18:19], v[24:25], v[18:19]
	v_pk_mul_f32 v[20:21], v[12:13], v[12:13]
	v_pk_fma_f32 v[10:11], v[10:11], 0.5, v[18:19] op_sel_hi:[1,0,1]
	v_pk_fma_f32 v[18:19], v[26:27], s[8:9], v[16:17] op_sel_hi:[1,0,0]
	v_pk_mul_f32 v[20:21], v[20:21], s[6:7] op_sel_hi:[1,0]
	v_pk_fma_f32 v[18:19], v[26:27], v[18:19], s[10:11] op_sel_hi:[1,1,0]
	v_exp_f32_e32 v20, v20
	v_pk_fma_f32 v[18:19], v[26:27], v[18:19], s[2:3] op_sel_hi:[1,1,0]
	v_exp_f32_e32 v21, v21
	v_pk_fma_f32 v[18:19], v[26:27], v[18:19], s[4:5] op_sel_hi:[1,1,0]
	v_and_b32_e32 v25, 0x7fffffff, v15
	v_and_b32_e32 v24, 0x7fffffff, v14
	v_pk_mul_f32 v[18:19], v[26:27], v[18:19]
	v_pk_fma_f32 v[26:27], v[24:25], s[12:13], 1.0 op_sel_hi:[1,0,0]
	v_pk_fma_f32 v[18:19], v[20:21], v[18:19], 0.5 op_sel_hi:[1,1,0] neg_lo:[1,0,0] neg_hi:[1,0,0]
	v_rcp_f32_e32 v26, v26
	v_rcp_f32_e32 v27, v27
	v_pk_mul_f32 v[18:19], v[22:23], v[18:19]
	v_pk_fma_f32 v[16:17], v[26:27], s[8:9], v[16:17] op_sel_hi:[1,0,0]
	v_pk_fma_f32 v[12:13], v[12:13], 0.5, v[18:19] op_sel_hi:[1,0,1]
	v_pk_mul_f32 v[18:19], v[14:15], v[14:15]
	v_pk_fma_f32 v[16:17], v[26:27], v[16:17], s[10:11] op_sel_hi:[1,1,0]
	v_pk_mul_f32 v[18:19], v[18:19], s[6:7] op_sel_hi:[1,0]
	v_pk_fma_f32 v[16:17], v[26:27], v[16:17], s[2:3] op_sel_hi:[1,1,0]
	v_exp_f32_e32 v18, v18
	v_exp_f32_e32 v19, v19
	v_pk_fma_f32 v[16:17], v[26:27], v[16:17], s[4:5] op_sel_hi:[1,1,0]
	s_mov_b32 s3, 0x700000
	v_pk_mul_f32 v[16:17], v[26:27], v[16:17]
	s_mov_b32 s7, 0x42000000
	v_pk_fma_f32 v[16:17], v[18:19], v[16:17], 0.5 op_sel_hi:[1,1,0] neg_lo:[1,0,0] neg_hi:[1,0,0]
	v_max_f32_e64 v18, |v6|, |v7|
	v_pk_mul_f32 v[16:17], v[24:25], v[16:17]
	s_nop 0
	v_pk_fma_f32 v[14:15], v[14:15], 0.5, v[16:17] op_sel_hi:[1,0,1]
	v_max_f32_e64 v16, |v0|, |v1|
	v_max_f32_e64 v17, |v2|, |v3|
	v_max3_f32 v16, v16, 0, v17
	v_max_f32_e64 v17, |v4|, |v5|
	v_max3_f32 v16, v16, v17, v18
	v_max_f32_e64 v17, |v8|, |v9|
	v_max_f32_e64 v18, |v10|, |v11|
	v_max3_f32 v16, v16, v17, v18
	v_max_f32_e64 v17, |v12|, |v13|
	v_max_f32_e64 v18, |v14|, |v15|
	v_max3_f32 v16, v16, v17, v18
	v_mov_b32_e32 v17, v16
	s_nop 1
	v_permlane16_swap_b32_e32 v16, v17
	v_max_f32_e32 v17, v17, v17
	v_max_f32_e32 v16, v16, v16
	v_max_f32_e32 v16, v16, v17
	v_lshrrev_b32_e32 v17, 23, v16
	v_and_b32_e32 v16, 0x7fffff, v16
	v_cmp_lt_u32_e32 vcc, s3, v16
	s_nop 1
	v_addc_co_u32_e32 v16, vcc, v17, v64, vcc
	v_med3_i32 v66, v16, s5, v65
	v_lshlrev_b32_e32 v16, 23, v66
	v_sub_u32_e32 v16, 1.0, v16
	v_pk_mul_f32 v[40:41], v[16:17], v[8:9] op_sel_hi:[0,1]
	v_pk_mul_f32 v[42:43], v[16:17], v[10:11] op_sel_hi:[0,1]
	v_pk_mul_f32 v[44:45], v[16:17], v[12:13] op_sel_hi:[0,1]
	v_pk_mul_f32 v[46:47], v[16:17], v[14:15] op_sel_hi:[0,1]
	v_pk_mul_f32 v[32:33], v[16:17], v[0:1] op_sel_hi:[0,1]
	v_pk_mul_f32 v[34:35], v[16:17], v[2:3] op_sel_hi:[0,1]
	v_pk_mul_f32 v[36:37], v[16:17], v[4:5] op_sel_hi:[0,1]
	v_pk_mul_f32 v[38:39], v[16:17], v[6:7] op_sel_hi:[0,1]
	v_mov_b32_e32 v0, v40
	v_mov_b32_e32 v1, v41
	v_mov_b32_e32 v2, v42
	v_mov_b32_e32 v3, v43
	v_mov_b32_e32 v4, v44
	v_mov_b32_e32 v5, v45
	v_mov_b32_e32 v6, v46
	v_mov_b32_e32 v7, v47
	v_cvt_scalef32_2xpk16_fp6_f32 v[68:73], v[32:47], v[0:15], 1.0
	v_cvt_scalef32_pk32_f32_fp6 v[0:31], v[68:73], s7
	v_mov_b32_e32 v16, v0
	v_mov_b32_e32 v17, v2
	v_mov_b32_e32 v2, v1
	v_mov_b32_e32 v0, v4
	v_mov_b32_e32 v1, v6
	v_pk_fma_f32 v[18:19], v[34:35], s[14:15], v[0:1] op_sel_hi:[1,0,1]
	v_mov_b32_e32 v0, v8
	v_mov_b32_e32 v1, v10
	v_mov_b32_e32 v6, v5
	v_pk_fma_f32 v[20:21], v[36:37], s[14:15], v[0:1] op_sel_hi:[1,0,1]
	v_mov_b32_e32 v10, v9
	v_mov_b32_e32 v1, v14
	v_mov_b32_e32 v14, v13
	v_pk_fma_f32 v[24:25], v[40:41], s[14:15], v[2:3] op_sel_hi:[1,0,1]
	v_pk_fma_f32 v[26:27], v[42:43], s[14:15], v[6:7] op_sel_hi:[1,0,1]
	v_pk_fma_f32 v[28:29], v[44:45], s[14:15], v[10:11] op_sel_hi:[1,0,1]
	v_mov_b32_e32 v0, v12
	v_pk_fma_f32 v[30:31], v[46:47], s[14:15], v[14:15] op_sel_hi:[1,0,1]
	v_pk_fma_f32 v[16:17], v[32:33], s[14:15], v[16:17] op_sel_hi:[1,0,1]
	v_pk_fma_f32 v[22:23], v[38:39], s[14:15], v[0:1] op_sel_hi:[1,0,1]
	v_mov_b32_e32 v0, v24
	v_mov_b32_e32 v1, v25
	v_mov_b32_e32 v2, v26
	v_mov_b32_e32 v3, v27
	v_mov_b32_e32 v4, v28
	v_mov_b32_e32 v5, v29
	v_mov_b32_e32 v6, v30
	v_mov_b32_e32 v7, v31
	v_cvt_scalef32_2xpk16_fp6_f32 v[0:5], v[16:31], v[0:15], 1.0
	v_lshl_add_u64 v[4:5], v[118:119], 0, v[130:131]
	v_lshl_add_u64 v[4:5], v[4:5], 0, v[160:161]
	global_store_dwordx3 v[4:5], v[68:70], off nt
	v_add_co_u32_e32 v4, vcc, 0x1000, v4
	v_xor_b32_e32 v0, 0x20820820, v0
	v_xor_b32_e32 v1, 0x8208208, v1
	v_xor_b32_e32 v2, 0x82082082, v2
	v_addc_co_u32_e32 v5, vcc, 0, v5, vcc
	global_store_dwordx3 v[4:5], v[0:2], off offset:2048 nt
	s_and_saveexec_b64 s[18:19], s[0:1]
	s_cbranch_execz .LBB3_20
	v_mov_b32_e32 v1, 0x7a00
	v_add_u32_e32 v0, 0x7f, v66
	v_lshl_add_u32 v1, v66, 8, v1
	v_mov_b32_e32 v129, 0
	v_or_b32_e32 v2, v1, v0
	v_lshl_add_u64 v[0:1], v[116:117], 0, v[128:129]
	global_store_short v[0:1], v2, off
.LBB3_20:
	s_or_b64 exec, exec, s[18:19]
	v_permlane32_swap_b32_e32 v60, v52
	v_permlane32_swap_b32_e32 v61, v53
	v_permlane32_swap_b32_e32 v62, v54
	v_permlane32_swap_b32_e32 v63, v55
	v_permlane32_swap_b32_e32 v58, v50
	v_permlane32_swap_b32_e32 v59, v51
	v_permlane32_swap_b32_e32 v56, v48
	v_permlane32_swap_b32_e32 v57, v49
	v_mov_b64_e32 v[16:17], s[16:17]
	v_pk_mul_f32 v[0:1], v[208:209], v[60:61]
	v_pk_mul_f32 v[2:3], v[210:211], v[62:63]
	v_and_b32_e32 v19, 0x7fffffff, v1
	v_and_b32_e32 v18, 0x7fffffff, v0
	v_pk_mul_f32 v[6:7], v[214:215], v[58:59]
	v_and_b32_e32 v23, 0x7fffffff, v3
	v_and_b32_e32 v22, 0x7fffffff, v2
	v_pk_fma_f32 v[36:37], v[18:19], s[12:13], 1.0 op_sel_hi:[1,0,0]
	v_pk_mul_f32 v[4:5], v[212:213], v[56:57]
	v_and_b32_e32 v31, 0x7fffffff, v7
	v_and_b32_e32 v30, 0x7fffffff, v6
	v_pk_fma_f32 v[38:39], v[22:23], s[12:13], 1.0 op_sel_hi:[1,0,0]
	v_rcp_f32_e32 v36, v36
	v_rcp_f32_e32 v37, v37
	v_and_b32_e32 v27, 0x7fffffff, v5
	v_and_b32_e32 v26, 0x7fffffff, v4
	v_pk_fma_f32 v[42:43], v[30:31], s[12:13], 1.0 op_sel_hi:[1,0,0]
	v_rcp_f32_e32 v38, v38
	v_rcp_f32_e32 v39, v39
	v_pk_fma_f32 v[40:41], v[26:27], s[12:13], 1.0 op_sel_hi:[1,0,0]
	v_rcp_f32_e32 v42, v42
	v_rcp_f32_e32 v43, v43
	v_pk_mul_f32 v[20:21], v[0:1], v[0:1]
	v_rcp_f32_e32 v40, v40
	v_rcp_f32_e32 v41, v41
	v_pk_mul_f32 v[24:25], v[2:3], v[2:3]
	v_pk_mul_f32 v[20:21], v[20:21], s[6:7] op_sel_hi:[1,0]
	v_pk_fma_f32 v[46:47], v[36:37], s[8:9], v[16:17] op_sel_hi:[1,0,0]
	v_pk_mul_f32 v[8:9], v[216:217], v[52:53]
	v_pk_mul_f32 v[32:33], v[6:7], v[6:7]
	v_pk_mul_f32 v[24:25], v[24:25], s[6:7] op_sel_hi:[1,0]
	v_exp_f32_e32 v20, v20
	v_exp_f32_e32 v21, v21
	v_pk_fma_f32 v[52:53], v[38:39], s[8:9], v[16:17] op_sel_hi:[1,0,0]
	v_pk_fma_f32 v[46:47], v[36:37], v[46:47], s[10:11] op_sel_hi:[1,1,0]
	v_pk_mul_f32 v[28:29], v[4:5], v[4:5]
	v_pk_mul_f32 v[32:33], v[32:33], s[6:7] op_sel_hi:[1,0]
	v_exp_f32_e32 v24, v24
	v_exp_f32_e32 v25, v25
	v_pk_fma_f32 v[58:59], v[42:43], s[8:9], v[16:17] op_sel_hi:[1,0,0]
	v_pk_fma_f32 v[52:53], v[38:39], v[52:53], s[10:11] op_sel_hi:[1,1,0]
	v_pk_fma_f32 v[46:47], v[36:37], v[46:47], s[2:3] op_sel_hi:[1,1,0]
	v_and_b32_e32 v35, 0x7fffffff, v9
	v_and_b32_e32 v34, 0x7fffffff, v8
	v_pk_mul_f32 v[28:29], v[28:29], s[6:7] op_sel_hi:[1,0]
	v_exp_f32_e32 v32, v32
	v_exp_f32_e32 v33, v33
	v_pk_fma_f32 v[56:57], v[40:41], s[8:9], v[16:17] op_sel_hi:[1,0,0]
	v_pk_fma_f32 v[58:59], v[42:43], v[58:59], s[10:11] op_sel_hi:[1,1,0]
	v_pk_fma_f32 v[52:53], v[38:39], v[52:53], s[2:3] op_sel_hi:[1,1,0]
	v_pk_fma_f32 v[46:47], v[36:37], v[46:47], s[4:5] op_sel_hi:[1,1,0]
	v_pk_fma_f32 v[44:45], v[34:35], s[12:13], 1.0 op_sel_hi:[1,0,0]
	v_exp_f32_e32 v28, v28
	v_exp_f32_e32 v29, v29
	v_pk_fma_f32 v[56:57], v[40:41], v[56:57], s[10:11] op_sel_hi:[1,1,0]
	v_pk_fma_f32 v[58:59], v[42:43], v[58:59], s[2:3] op_sel_hi:[1,1,0]
	v_pk_fma_f32 v[52:53], v[38:39], v[52:53], s[4:5] op_sel_hi:[1,1,0]
	v_pk_mul_f32 v[36:37], v[36:37], v[46:47]
	v_rcp_f32_e32 v44, v44
	v_pk_fma_f32 v[56:57], v[40:41], v[56:57], s[2:3] op_sel_hi:[1,1,0]
	v_pk_fma_f32 v[58:59], v[42:43], v[58:59], s[4:5] op_sel_hi:[1,1,0]
	v_pk_mul_f32 v[38:39], v[38:39], v[52:53]
	v_pk_fma_f32 v[20:21], v[20:21], v[36:37], 0.5 op_sel_hi:[1,1,0] neg_lo:[1,0,0] neg_hi:[1,0,0]
	v_rcp_f32_e32 v45, v45
	v_pk_fma_f32 v[56:57], v[40:41], v[56:57], s[4:5] op_sel_hi:[1,1,0]
	v_pk_mul_f32 v[42:43], v[42:43], v[58:59]
	v_pk_fma_f32 v[24:25], v[24:25], v[38:39], 0.5 op_sel_hi:[1,1,0] neg_lo:[1,0,0] neg_hi:[1,0,0]
	v_pk_mul_f32 v[18:19], v[18:19], v[20:21]
	v_pk_mul_f32 v[40:41], v[40:41], v[56:57]
	v_pk_mul_f32 v[20:21], v[22:23], v[24:25]
	v_pk_fma_f32 v[0:1], v[0:1], 0.5, v[18:19] op_sel_hi:[1,0,1]
	v_pk_fma_f32 v[18:19], v[32:33], v[42:43], 0.5 op_sel_hi:[1,1,0] neg_lo:[1,0,0] neg_hi:[1,0,0]
	v_pk_fma_f32 v[28:29], v[28:29], v[40:41], 0.5 op_sel_hi:[1,1,0] neg_lo:[1,0,0] neg_hi:[1,0,0]
	v_pk_fma_f32 v[2:3], v[2:3], 0.5, v[20:21] op_sel_hi:[1,0,1]
	v_pk_mul_f32 v[18:19], v[30:31], v[18:19]
	v_pk_mul_f32 v[20:21], v[8:9], v[8:9]
	v_pk_mul_f32 v[22:23], v[26:27], v[28:29]
	v_pk_fma_f32 v[6:7], v[6:7], 0.5, v[18:19] op_sel_hi:[1,0,1]
	v_pk_fma_f32 v[18:19], v[44:45], s[8:9], v[16:17] op_sel_hi:[1,0,0]
	v_pk_mul_f32 v[20:21], v[20:21], s[6:7] op_sel_hi:[1,0]
	v_pk_mul_f32 v[10:11], v[218:219], v[54:55]
	v_pk_fma_f32 v[4:5], v[4:5], 0.5, v[22:23] op_sel_hi:[1,0,1]
	v_pk_fma_f32 v[18:19], v[44:45], v[18:19], s[10:11] op_sel_hi:[1,1,0]
	v_exp_f32_e32 v20, v20
	v_exp_f32_e32 v21, v21
	v_and_b32_e32 v23, 0x7fffffff, v11
	v_and_b32_e32 v22, 0x7fffffff, v10
	v_pk_fma_f32 v[18:19], v[44:45], v[18:19], s[2:3] op_sel_hi:[1,1,0]
	v_pk_fma_f32 v[24:25], v[22:23], s[12:13], 1.0 op_sel_hi:[1,0,0]
	v_pk_fma_f32 v[18:19], v[44:45], v[18:19], s[4:5] op_sel_hi:[1,1,0]
	v_rcp_f32_e32 v24, v24
	v_rcp_f32_e32 v25, v25
	v_pk_mul_f32 v[18:19], v[44:45], v[18:19]
	v_pk_mul_f32 v[12:13], v[220:221], v[48:49]
	v_pk_fma_f32 v[18:19], v[20:21], v[18:19], 0.5 op_sel_hi:[1,1,0] neg_lo:[1,0,0] neg_hi:[1,0,0]
	v_pk_mul_f32 v[20:21], v[10:11], v[10:11]
	v_pk_mul_f32 v[18:19], v[34:35], v[18:19]
	v_pk_mul_f32 v[20:21], v[20:21], s[6:7] op_sel_hi:[1,0]
	v_pk_fma_f32 v[8:9], v[8:9], 0.5, v[18:19] op_sel_hi:[1,0,1]
	v_pk_fma_f32 v[18:19], v[24:25], s[8:9], v[16:17] op_sel_hi:[1,0,0]
	v_exp_f32_e32 v20, v20
	v_pk_fma_f32 v[18:19], v[24:25], v[18:19], s[10:11] op_sel_hi:[1,1,0]
	v_exp_f32_e32 v21, v21
	v_pk_fma_f32 v[18:19], v[24:25], v[18:19], s[2:3] op_sel_hi:[1,1,0]
	v_pk_mul_f32 v[14:15], v[222:223], v[50:51]
	v_pk_fma_f32 v[18:19], v[24:25], v[18:19], s[4:5] op_sel_hi:[1,1,0]
	s_nop 0
	v_pk_mul_f32 v[18:19], v[24:25], v[18:19]
	v_and_b32_e32 v25, 0x7fffffff, v13
	v_and_b32_e32 v24, 0x7fffffff, v12
	v_pk_fma_f32 v[26:27], v[24:25], s[12:13], 1.0 op_sel_hi:[1,0,0]
	v_pk_fma_f32 v[18:19], v[20:21], v[18:19], 0.5 op_sel_hi:[1,1,0] neg_lo:[1,0,0] neg_hi:[1,0,0]
	v_rcp_f32_e32 v26, v26
	v_rcp_f32_e32 v27, v27
	v_pk_mul_f32 v[18:19], v[22:23], v[18:19]
	v_pk_mul_f32 v[20:21], v[12:13], v[12:13]
	v_pk_fma_f32 v[10:11], v[10:11], 0.5, v[18:19] op_sel_hi:[1,0,1]
	v_pk_fma_f32 v[18:19], v[26:27], s[8:9], v[16:17] op_sel_hi:[1,0,0]
	v_pk_mul_f32 v[20:21], v[20:21], s[6:7] op_sel_hi:[1,0]
	v_pk_fma_f32 v[18:19], v[26:27], v[18:19], s[10:11] op_sel_hi:[1,1,0]
	v_exp_f32_e32 v20, v20
	v_pk_fma_f32 v[18:19], v[26:27], v[18:19], s[2:3] op_sel_hi:[1,1,0]
	v_exp_f32_e32 v21, v21
	v_pk_fma_f32 v[18:19], v[26:27], v[18:19], s[4:5] op_sel_hi:[1,1,0]
	v_and_b32_e32 v23, 0x7fffffff, v15
	v_and_b32_e32 v22, 0x7fffffff, v14
	v_pk_mul_f32 v[18:19], v[26:27], v[18:19]
	v_pk_fma_f32 v[26:27], v[22:23], s[12:13], 1.0 op_sel_hi:[1,0,0]
	v_pk_fma_f32 v[18:19], v[20:21], v[18:19], 0.5 op_sel_hi:[1,1,0] neg_lo:[1,0,0] neg_hi:[1,0,0]
	v_rcp_f32_e32 v26, v26
	v_rcp_f32_e32 v27, v27
	v_pk_mul_f32 v[18:19], v[24:25], v[18:19]
	v_pk_fma_f32 v[16:17], v[26:27], s[8:9], v[16:17] op_sel_hi:[1,0,0]
	v_pk_fma_f32 v[12:13], v[12:13], 0.5, v[18:19] op_sel_hi:[1,0,1]
	v_pk_mul_f32 v[18:19], v[14:15], v[14:15]
	v_pk_fma_f32 v[16:17], v[26:27], v[16:17], s[10:11] op_sel_hi:[1,1,0]
	v_pk_mul_f32 v[18:19], v[18:19], s[6:7] op_sel_hi:[1,0]
	v_pk_fma_f32 v[16:17], v[26:27], v[16:17], s[2:3] op_sel_hi:[1,1,0]
	v_exp_f32_e32 v18, v18
	v_exp_f32_e32 v19, v19
	v_pk_fma_f32 v[16:17], v[26:27], v[16:17], s[4:5] op_sel_hi:[1,1,0]
	s_nop 0
	v_pk_mul_f32 v[16:17], v[26:27], v[16:17]
	s_nop 0
	v_pk_fma_f32 v[16:17], v[18:19], v[16:17], 0.5 op_sel_hi:[1,1,0] neg_lo:[1,0,0] neg_hi:[1,0,0]
	v_max_f32_e64 v18, |v6|, |v7|
	v_pk_mul_f32 v[16:17], v[22:23], v[16:17]
	s_nop 0
	v_pk_fma_f32 v[14:15], v[14:15], 0.5, v[16:17] op_sel_hi:[1,0,1]
	v_max_f32_e64 v16, |v0|, |v1|
	v_max_f32_e64 v17, |v2|, |v3|
	v_max3_f32 v16, v16, 0, v17
	v_max_f32_e64 v17, |v4|, |v5|
	v_max3_f32 v16, v16, v17, v18
	v_max_f32_e64 v17, |v8|, |v9|
	v_max_f32_e64 v18, |v10|, |v11|
	v_max3_f32 v16, v16, v17, v18
	v_max_f32_e64 v17, |v12|, |v13|
	v_max_f32_e64 v18, |v14|, |v15|
	v_max3_f32 v16, v16, v17, v18
	v_mov_b32_e32 v17, v16
	s_nop 1
	v_permlane16_swap_b32_e32 v16, v17
	v_max_f32_e32 v17, v17, v17
	v_max_f32_e32 v16, v16, v16
	v_max_f32_e32 v16, v16, v17
	v_lshrrev_b32_e32 v17, 23, v16
	v_and_b32_e32 v16, 0x7fffff, v16
	v_cmp_lt_u32_e32 vcc, s3, v16
	s_nop 1
	v_addc_co_u32_e32 v16, vcc, v17, v64, vcc
	v_med3_i32 v48, v16, s5, v65
	v_lshlrev_b32_e32 v16, 23, v48
	v_sub_u32_e32 v16, 1.0, v16
	v_pk_mul_f32 v[40:41], v[16:17], v[8:9] op_sel_hi:[0,1]
	v_pk_mul_f32 v[42:43], v[16:17], v[10:11] op_sel_hi:[0,1]
	v_pk_mul_f32 v[44:45], v[16:17], v[12:13] op_sel_hi:[0,1]
	v_pk_mul_f32 v[46:47], v[16:17], v[14:15] op_sel_hi:[0,1]
	v_pk_mul_f32 v[32:33], v[16:17], v[0:1] op_sel_hi:[0,1]
	v_pk_mul_f32 v[34:35], v[16:17], v[2:3] op_sel_hi:[0,1]
	v_pk_mul_f32 v[36:37], v[16:17], v[4:5] op_sel_hi:[0,1]
	v_pk_mul_f32 v[38:39], v[16:17], v[6:7] op_sel_hi:[0,1]
	v_mov_b32_e32 v0, v40
	v_mov_b32_e32 v1, v41
	v_mov_b32_e32 v2, v42
	v_mov_b32_e32 v3, v43
	v_mov_b32_e32 v4, v44
	v_mov_b32_e32 v5, v45
	v_mov_b32_e32 v6, v46
	v_mov_b32_e32 v7, v47
	v_cvt_scalef32_2xpk16_fp6_f32 v[50:55], v[32:47], v[0:15], 1.0
	v_cvt_scalef32_pk32_f32_fp6 v[0:31], v[50:55], s7
	v_mov_b32_e32 v16, v0
	v_mov_b32_e32 v17, v2
	v_mov_b32_e32 v2, v1
	v_mov_b32_e32 v0, v4
	v_mov_b32_e32 v1, v6
	v_pk_fma_f32 v[18:19], v[34:35], s[14:15], v[0:1] op_sel_hi:[1,0,1]
	v_mov_b32_e32 v0, v8
	v_mov_b32_e32 v1, v10
	v_mov_b32_e32 v6, v5
	v_pk_fma_f32 v[20:21], v[36:37], s[14:15], v[0:1] op_sel_hi:[1,0,1]
	v_mov_b32_e32 v10, v9
	v_mov_b32_e32 v1, v14
	v_mov_b32_e32 v14, v13
	v_pk_fma_f32 v[24:25], v[40:41], s[14:15], v[2:3] op_sel_hi:[1,0,1]
	v_pk_fma_f32 v[26:27], v[42:43], s[14:15], v[6:7] op_sel_hi:[1,0,1]
	v_pk_fma_f32 v[28:29], v[44:45], s[14:15], v[10:11] op_sel_hi:[1,0,1]
	v_mov_b32_e32 v0, v12
	v_pk_fma_f32 v[30:31], v[46:47], s[14:15], v[14:15] op_sel_hi:[1,0,1]
	v_pk_fma_f32 v[16:17], v[32:33], s[14:15], v[16:17] op_sel_hi:[1,0,1]
	v_pk_fma_f32 v[22:23], v[38:39], s[14:15], v[0:1] op_sel_hi:[1,0,1]
	v_mov_b32_e32 v0, v24
	v_mov_b32_e32 v1, v25
	v_mov_b32_e32 v2, v26
	v_mov_b32_e32 v3, v27
	v_mov_b32_e32 v4, v28
	v_mov_b32_e32 v5, v29
	v_mov_b32_e32 v6, v30
	v_mov_b32_e32 v7, v31
	v_cvt_scalef32_2xpk16_fp6_f32 v[0:5], v[16:31], v[0:15], 1.0
	v_lshl_add_u64 v[4:5], v[118:119], 0, v[114:115]
	v_lshl_add_u64 v[4:5], v[4:5], 0, v[160:161]
	global_store_dwordx3 v[4:5], v[50:52], off nt
	v_add_co_u32_e32 v4, vcc, 0x1000, v4
	v_xor_b32_e32 v0, 0x20820820, v0
	v_xor_b32_e32 v1, 0x8208208, v1
	v_xor_b32_e32 v2, 0x82082082, v2
	v_addc_co_u32_e32 v5, vcc, 0, v5, vcc
	global_store_dwordx3 v[4:5], v[0:2], off offset:2048 nt
	s_and_saveexec_b64 s[2:3], s[0:1]
	s_cbranch_execz .LBB3_22
	v_mov_b32_e32 v1, 0x7a00
	v_add_u32_e32 v0, 0x7f, v48
	v_lshl_add_u32 v1, v48, 8, v1
	v_mov_b32_e32 v113, 0
	v_or_b32_e32 v2, v1, v0
	v_lshl_add_u64 v[0:1], v[116:117], 0, v[112:113]
	global_store_short v[0:1], v2, off

	.amdhsa_kernel _Z6mxgemmILi1ELi4096ELi4EEvPKcS1_PKfS3_Pvi
		.amdhsa_group_segment_fixed_size 0
		.amdhsa_private_segment_fixed_size 0
		.amdhsa_kernarg_size 44
		.amdhsa_user_sgpr_count 2
		.amdhsa_user_sgpr_dispatch_ptr 0
		.amdhsa_user_sgpr_queue_ptr 0
		.amdhsa_user_sgpr_kernarg_segment_ptr 1
		.amdhsa_user_sgpr_dispatch_id 0
		.amdhsa_user_sgpr_kernarg_preload_length 0
		.amdhsa_user_sgpr_kernarg_preload_offset 0
		.amdhsa_user_sgpr_private_segment_size 0
		.amdhsa_uses_dynamic_stack 0
		.amdhsa_enable_private_segment 0
		.amdhsa_system_sgpr_workgroup_id_x 1
		.amdhsa_system_sgpr_workgroup_id_y 0
		.amdhsa_system_sgpr_workgroup_id_z 0
		.amdhsa_system_sgpr_workgroup_info 0
		.amdhsa_system_vgpr_workitem_id 0
		.amdhsa_next_free_vgpr 256
		.amdhsa_next_free_sgpr 72
		.amdhsa_accum_offset 256
		.amdhsa_reserve_vcc 1
		.amdhsa_float_round_mode_32 0
		.amdhsa_float_round_mode_16_64 0
		.amdhsa_float_denorm_mode_32 3
		.amdhsa_float_denorm_mode_16_64 3
		.amdhsa_dx10_clamp 1
		.amdhsa_ieee_mode 1
		.amdhsa_fp16_overflow 0
		.amdhsa_tg_split 0
		.amdhsa_exception_fp_ieee_invalid_op 0
		.amdhsa_exception_fp_denorm_src 0
		.amdhsa_exception_fp_ieee_div_zero 0
		.amdhsa_exception_fp_ieee_overflow 0
		.amdhsa_exception_fp_ieee_underflow 0
		.amdhsa_exception_fp_ieee_inexact 0
		.amdhsa_exception_int_div_zero 0
	.end_amdhsa_kernel
	.section	.text._Z6mxgemmILi1ELi4096ELi4EEvPKcS1_PKfS3_Pvi,"axG",@progbits,_Z6mxgemmILi1ELi4096ELi4EEvPKcS1_PKfS3_Pvi,comdat
	.p2alignl 8, 3212836864
